# speedup vs baseline: 1.0493x; 1.0458x over previous
.LBB0_6:
	s_lshl_b32 s8, s7, 9
	s_lshl_b32 s9, s6, 9
	v_or_b32_e32 v11, s8, v3
	v_or_b32_e32 v12, s9, v0
	v_add_u32_e32 v13, s8, v5
	v_add_u32_e32 v14, s9, v4
	v_add_u32_e32 v15, s8, v7
	v_add_u32_e32 v16, s9, v6
	v_add_u32_e32 v17, s8, v9
	v_add_u32_e32 v18, s9, v8
	v_lshrrev_b32_e32 v19, 8, v11
	v_lshrrev_b32_e32 v20, 8, v12
	v_lshrrev_b32_e32 v21, 8, v13
	v_lshrrev_b32_e32 v22, 8, v14
	v_lshrrev_b32_e32 v23, 8, v15
	v_lshrrev_b32_e32 v24, 8, v16
	v_lshrrev_b32_e32 v25, 8, v17
	v_lshrrev_b32_e32 v26, 8, v18
	v_mad_u32_u24 v20, v20, s12, v10
	v_mad_u32_u24 v19, v19, s12, v10
	v_mad_u32_u24 v22, v22, s12, v10
	v_mad_u32_u24 v21, v21, s12, v10
	v_mad_u32_u24 v24, v24, s12, v10
	v_mad_u32_u24 v23, v23, s12, v10
	v_mad_u32_u24 v26, v26, s12, v10
	v_mad_u32_u24 v25, v25, s12, v10
	ds_read_b32 v20, v20
	ds_read_b32 v19, v19
	ds_read_b32 v22, v22
	ds_read_b32 v21, v21
	ds_read_b32 v24, v24
	ds_read_b32 v23, v23
	ds_read_b32 v26, v26
	ds_read_b32 v25, v25
	v_and_b32_e32 v12, 0x3f00, v12
	s_add_i32 s6, s6, 8
	s_add_i32 s7, s7, 8
	s_add_i32 s3, s3, -8
	v_and_b32_e32 v11, 0x3f00, v11
	v_and_b32_e32 v13, 0x3f00, v13
	v_and_b32_e32 v14, 0x3f00, v14
	v_and_b32_e32 v15, 0x3f00, v15
	v_and_b32_e32 v16, 0x3f00, v16
	v_and_b32_e32 v17, 0x3f00, v17
	v_and_b32_e32 v18, 0x3f00, v18
	v_or_b32_e32 v12, v12, v2
	s_cmp_lg_u32 s3, 0
	v_or_b32_e32 v11, v11, v1
	v_or_b32_e32 v13, v13, v1
	v_or_b32_e32 v14, v14, v2
	v_or_b32_e32 v15, v15, v1
	v_or_b32_e32 v16, v16, v2
	v_or_b32_e32 v17, v17, v1
	v_or_b32_e32 v18, v18, v2
	v_lshlrev_b32_e32 v12, 2, v12
	v_lshlrev_b32_e32 v11, 2, v11
	v_lshlrev_b32_e32 v14, 2, v14
	v_lshlrev_b32_e32 v13, 2, v13
	v_lshlrev_b32_e32 v16, 2, v16
	v_lshlrev_b32_e32 v15, 2, v15
	v_lshlrev_b32_e32 v18, 2, v18
	v_lshlrev_b32_e32 v17, 2, v17
	s_waitcnt lgkmcnt(7)
	global_store_dword v12, v20, s[4:5] sc1
	s_waitcnt lgkmcnt(6)
	global_store_dword v11, v19, s[4:5] sc1
	s_waitcnt lgkmcnt(5)
	global_store_dword v14, v22, s[4:5] sc1
	s_waitcnt lgkmcnt(4)
	global_store_dword v13, v21, s[4:5] sc1
	s_waitcnt lgkmcnt(3)
	global_store_dword v16, v24, s[4:5] sc1
	s_waitcnt lgkmcnt(2)
	global_store_dword v15, v23, s[4:5] sc1
	s_waitcnt lgkmcnt(1)
	global_store_dword v18, v26, s[4:5] sc1
	s_waitcnt lgkmcnt(0)
	global_store_dword v17, v25, s[4:5] sc1
	s_cbranch_scc1 .LBB0_6
	s_mov_b64 s[4:5], 0

_Z7k_frontPKDF16_S0_PKfS2_S0_S2_S2_S2_PjPfS4_S4_S4_:
	s_mov_b32 s12, s3
	s_load_dwordx8 s[4:11], s[0:1], 0x0
	s_lshl_b32 s3, s2, 6
	s_ashr_i32 s13, s12, 31
	s_lshl_b64 s[14:15], s[12:13], 12
	s_ashr_i32 s16, s3, 31
	s_add_u32 s14, s14, s3
	s_addc_u32 s15, s15, s16
	s_lshl_b32 s16, s12, 22
	s_and_b32 s16, s16, 0x400000
	s_waitcnt lgkmcnt(0)
	s_add_u32 s16, s4, s16
	s_addc_u32 s17, s5, 0
	s_lshl_b32 s4, s12, 6
	s_and_b32 s4, s4, 0xffffff80
	s_ashr_i32 s5, s4, 31
	s_lshl_b64 s[4:5], s[4:5], 1
	s_add_u32 s4, s16, s4
	s_addc_u32 s5, s17, s5
	s_add_i32 s3, s3, -16
	v_lshrrev_b32_e32 v134, 4, v0
	v_lshlrev_b32_e32 v1, 4, v0
	v_mov_b32_e32 v91, 0
	v_or_b32_e32 v24, s3, v134
	v_and_b32_e32 v90, 0xf0, v1
	v_max_i32_e32 v2, 0, v24
	v_mov_b32_e32 v3, v91
	v_lshl_add_u64 v[18:19], s[4:5], 0, v[90:91]
	v_lshlrev_b64 v[2:3], 10, v[2:3]
	v_lshl_add_u64 v[10:11], v[18:19], 0, v[2:3]
	v_or_b32_e32 v2, 0x100, v0
	v_lshrrev_b32_e32 v135, 4, v2
	v_add_u32_e32 v25, s3, v135
	v_max_i32_e32 v2, 0, v25
	v_mov_b32_e32 v3, v91
	v_lshlrev_b64 v[2:3], 10, v[2:3]
	v_lshl_add_u64 v[12:13], v[18:19], 0, v[2:3]
	global_load_dwordx4 v[2:5], v[10:11], off
	global_load_dwordx4 v[6:9], v[12:13], off
	v_or_b32_e32 v10, 0x200, v0
	v_lshrrev_b32_e32 v136, 4, v10
	v_or_b32_e32 v14, 0x300, v0
	v_add_u32_e32 v30, s3, v136
	v_lshrrev_b32_e32 v137, 4, v14
	v_max_i32_e32 v10, 0, v30
	v_mov_b32_e32 v11, v91
	v_add_u32_e32 v31, s3, v137
	v_lshlrev_b64 v[10:11], 10, v[10:11]
	v_max_i32_e32 v14, 0, v31
	v_mov_b32_e32 v15, v91
	v_add_u32_e32 v32, 64, v24
	v_lshl_add_u64 v[10:11], v[18:19], 0, v[10:11]
	v_lshlrev_b64 v[14:15], 10, v[14:15]
	v_max_i32_e32 v20, 0, v32
	v_mov_b32_e32 v21, v91
	global_load_dwordx4 v[10:13], v[10:11], off
	v_lshl_add_u64 v[14:15], v[18:19], 0, v[14:15]
	v_lshlrev_b64 v[20:21], 10, v[20:21]
	global_load_dwordx4 v[14:17], v[14:15], off
	v_lshl_add_u64 v[18:19], v[18:19], 0, v[20:21]
	global_load_dwordx4 v[18:21], v[18:19], off
	v_lshrrev_b32_e32 v138, 2, v0
	v_and_b32_e32 v141, 48, v138
	v_and_b32_e32 v92, 0x3f0, v1
	v_mov_b32_e32 v23, v91
	v_lshl_or_b32 v22, v141, 10, v92
	s_movk_i32 s16, 0x2000
	v_lshl_add_u64 v[26:27], s[6:7], 0, v[22:23]
	v_add_co_u32_e32 v28, vcc, s16, v26
	global_load_dwordx4 v[74:77], v22, s[6:7]
	global_load_dwordx4 v[70:73], v22, s[6:7] offset:1024
	global_load_dwordx4 v[66:69], v22, s[6:7] offset:2048
	global_load_dwordx4 v[62:65], v22, s[6:7] offset:3072
	v_addc_co_u32_e32 v29, vcc, 0, v27, vcc
	v_cmp_lt_i32_e32 vcc, -1, v24
	global_load_dwordx4 v[50:53], v[28:29], off offset:-4096
	s_movk_i32 s3, 0x1000
	s_movk_i32 s17, 0x3000
	v_or_b32_e32 v139, 0x3c00, v1
	v_lshl_or_b32 v1, v138, 10, v139
	v_lshlrev_b32_e32 v33, 3, v0
	v_or_b32_e32 v90, 0xa500, v90
	v_and_b32_e32 v140, 15, v0
	v_and_b32_e32 v142, 48, v0
	s_movk_i32 s18, 0xc0
	v_lshlrev_b32_e32 v132, 6, v0
	v_lshlrev_b32_e32 v133, 5, v0
	s_waitcnt vmcnt(9)
	v_cndmask_b32_e32 v34, 0, v2, vcc
	v_cndmask_b32_e32 v35, 0, v3, vcc
	v_cndmask_b32_e32 v36, 0, v4, vcc
	v_cndmask_b32_e32 v37, 0, v5, vcc
	v_cmp_lt_i32_e32 vcc, -1, v25
	v_add_co_u32_e64 v2, s[4:5], s3, v26
	s_waitcnt vmcnt(8)
	v_cndmask_b32_e32 v46, 0, v6, vcc
	v_cndmask_b32_e32 v47, 0, v7, vcc
	v_cndmask_b32_e32 v48, 0, v8, vcc
	v_cndmask_b32_e32 v49, 0, v9, vcc
	v_cmp_lt_i32_e32 vcc, -1, v30
	v_addc_co_u32_e64 v3, s[4:5], 0, v27, s[4:5]
	global_load_dwordx4 v[78:81], v[2:3], off offset:1024
	global_load_dwordx4 v[82:85], v[2:3], off offset:2048
	global_load_dwordx4 v[86:89], v[2:3], off offset:3072
	s_movk_i32 s4, 0x110
	s_waitcnt vmcnt(10)
	v_cndmask_b32_e32 v94, 0, v10, vcc
	v_cndmask_b32_e32 v95, 0, v11, vcc
	v_cndmask_b32_e32 v96, 0, v12, vcc
	v_cndmask_b32_e32 v97, 0, v13, vcc
	v_cmp_lt_i32_e32 vcc, -1, v31
	v_mad_u32_u24 v106, v134, s4, v90
	v_mad_u32_u24 v130, v140, s4, v142
	s_waitcnt vmcnt(9)
	v_cndmask_b32_e32 v98, 0, v14, vcc
	v_cndmask_b32_e32 v99, 0, v15, vcc
	v_cndmask_b32_e32 v100, 0, v16, vcc
	v_cndmask_b32_e32 v101, 0, v17, vcc
	v_cmp_lt_i32_e32 vcc, -1, v32
	s_waitcnt vmcnt(8)
	s_nop 0
	v_cndmask_b32_e32 v102, 0, v18, vcc
	v_cndmask_b32_e32 v103, 0, v19, vcc
	v_cndmask_b32_e32 v104, 0, v20, vcc
	v_cndmask_b32_e32 v105, 0, v21, vcc
	v_add_co_u32_e32 v6, vcc, s17, v26
	global_load_dwordx4 v[58:61], v[28:29], off
	global_load_dwordx4 v[54:57], v[28:29], off offset:1024
	global_load_dwordx4 v[22:25], v[28:29], off offset:2048
	global_load_dwordx4 v[18:21], v[28:29], off offset:3072
	v_addc_co_u32_e32 v7, vcc, 0, v27, vcc
	global_load_dwordx4 v[14:17], v[6:7], off
	global_load_dwordx4 v[10:13], v[6:7], off offset:1024
	global_load_dwordx4 v[2:5], v[6:7], off offset:2048
	s_nop 0
	global_load_dwordx4 v[6:9], v1, s[6:7]
	v_and_b32_e32 v1, 0xf8, v33
	v_lshlrev_b32_e32 v26, 4, v1
	global_load_dwordx4 v[122:125], v26, s[8:9] offset:32
	global_load_dwordx4 v[38:41], v26, s[8:9] offset:48
	global_load_dwordx4 v[126:129], v26, s[8:9]
	global_load_dwordx4 v[42:45], v26, s[8:9] offset:16
	v_or_b32_e32 v30, 64, v26
	global_load_dwordx4 v[114:117], v30, s[8:9] offset:32
	global_load_dwordx4 v[26:29], v30, s[8:9] offset:48
	global_load_dwordx4 v[144:147], v30, s[8:9]
	s_nop 0
	global_load_dwordx4 v[30:33], v30, s[8:9] offset:16
	ds_write_b128 v106, v[34:37]
	v_mad_u32_u24 v34, v135, s4, v90
	ds_write_b128 v34, v[46:49]
	v_mad_u32_u24 v34, v136, s4, v90
	ds_write_b128 v34, v[94:97]
	v_mad_u32_u24 v34, v137, s4, v90
	v_lshlrev_b32_e32 v93, 2, v1
	ds_write_b128 v34, v[98:101]
	ds_write_b128 v106, v[102:105] offset:17408
	global_load_dwordx4 v[34:37], v93, s[10:11] offset:16
	global_load_dwordx4 v[46:49], v93, s[10:11]
	s_waitcnt lgkmcnt(0)
	s_barrier
	ds_read_b128 v[94:97], v130 offset:42240
	ds_read_b128 v[98:101], v130 offset:42304
	s_waitcnt vmcnt(25) lgkmcnt(1)
	v_mfma_f32_16x16x32_f16 a[0:3], v[74:77], v[94:97], 0
	ds_read_b128 v[102:105], v130 offset:42368
	ds_read_b128 v[106:109], v130 offset:42432
	v_and_b32_e32 v90, 12, v138
	v_and_or_b32 v90, v0, s18, v90
	s_waitcnt vmcnt(21)
	v_mfma_f32_16x16x32_f16 a[4:7], v[50:53], v[94:97], 0
	v_mul_u32_u24_e32 v93, 0x210, v140
	v_lshl_add_u32 v131, v90, 1, v93
	v_and_b32_e32 v93, 56, v138
	s_waitcnt vmcnt(17)
	v_mfma_f32_16x16x32_f16 a[8:11], v[58:61], v[94:97], 0
	v_mul_u32_u24_e32 v93, 0x210, v93
	v_lshl_add_u32 v93, v1, 1, v93
	s_load_dwordx8 s[4:11], s[0:1], 0x20
	s_waitcnt vmcnt(13)
	v_mfma_f32_16x16x32_f16 a[12:15], v[14:17], v[94:97], 0
	v_lshlrev_b32_e32 v90, 2, v0
	s_mov_b32 s18, 0xbfb8aa3b
	s_waitcnt lgkmcnt(0)
	v_mfma_f32_16x16x32_f16 a[0:3], v[70:73], v[98:101], a[0:3]
	v_mfma_f32_16x16x32_f16 a[4:7], v[78:81], v[98:101], a[4:7]
	v_mfma_f32_16x16x32_f16 a[8:11], v[54:57], v[98:101], a[8:11]
	s_waitcnt vmcnt(12)
	v_mfma_f32_16x16x32_f16 a[12:15], v[10:13], v[98:101], a[12:15]
	s_waitcnt vmcnt(9)
	v_mov_b32_e32 v98, v122
	s_waitcnt vmcnt(8)
	v_mov_b32_e32 v99, v38
	v_mov_b32_e32 v38, v123
	v_mfma_f32_16x16x32_f16 a[0:3], v[66:69], v[102:105], a[0:3]
	v_mov_b32_e32 v100, v124
	v_mov_b32_e32 v101, v40
	v_mov_b32_e32 v40, v125
	v_mfma_f32_16x16x32_f16 a[4:7], v[82:85], v[102:105], a[4:7]
	v_mfma_f32_16x16x32_f16 a[8:11], v[22:25], v[102:105], a[8:11]
	v_mfma_f32_16x16x32_f16 a[12:15], v[2:5], v[102:105], a[12:15]
	s_waitcnt vmcnt(7)
	v_mov_b32_e32 v102, v126
	s_waitcnt vmcnt(6)
	v_mov_b32_e32 v103, v42
	v_mov_b32_e32 v42, v127
	v_mfma_f32_16x16x32_f16 a[0:3], v[62:65], v[106:109], a[0:3]
	v_mov_b32_e32 v104, v128
	v_mov_b32_e32 v105, v44
	v_mov_b32_e32 v44, v129
	v_mfma_f32_16x16x32_f16 a[4:7], v[86:89], v[106:109], a[4:7]
	v_mfma_f32_16x16x32_f16 a[8:11], v[18:21], v[106:109], a[8:11]
	s_nop 2
	v_accvgpr_read_b32 v1, a0
	v_accvgpr_read_b32 v126, a1
	v_accvgpr_read_b32 v127, a2
	v_mfma_f32_16x16x32_f16 a[12:15], v[6:9], v[106:109], a[12:15]
	ds_read_b128 v[94:97], v130 offset:46592
	ds_read_b128 v[106:109], v130 offset:46656
	ds_read_b128 v[110:113], v130 offset:46720
	ds_read_b128 v[118:121], v130 offset:46784
	v_accvgpr_read_b32 v128, a3
	s_waitcnt lgkmcnt(3)
	v_mfma_f32_16x16x32_f16 a[16:19], v[74:77], v[94:97], 0
	v_cvt_pk_f16_f32 v127, v127, v128
	v_cvt_pk_f16_f32 v126, v1, v126
	v_accvgpr_read_b32 v1, a4
	v_mfma_f32_16x16x32_f16 a[20:23], v[50:53], v[94:97], 0
	v_accvgpr_read_b32 v128, a5
	v_accvgpr_read_b32 v129, a6
	v_accvgpr_read_b32 v143, a7
	v_mfma_f32_16x16x32_f16 a[24:27], v[58:61], v[94:97], 0
	v_cvt_pk_f16_f32 v129, v129, v143
	v_cvt_pk_f16_f32 v128, v1, v128
	ds_write2_b64 v131, v[126:127], v[128:129] offset1:4
	v_mfma_f32_16x16x32_f16 a[28:31], v[14:17], v[94:97], 0
	v_accvgpr_read_b32 v1, a8
	v_accvgpr_read_b32 v126, a9
	v_accvgpr_read_b32 v127, a10
	s_waitcnt lgkmcnt(3)
	v_mfma_f32_16x16x32_f16 a[16:19], v[70:73], v[106:109], a[16:19]
	v_accvgpr_read_b32 v128, a11
	ds_read_b128 v[122:125], v130 offset:51136
	v_cvt_pk_f16_f32 v127, v127, v128
	v_mfma_f32_16x16x32_f16 a[20:23], v[78:81], v[106:109], a[20:23]
	v_cvt_pk_f16_f32 v126, v1, v126
	v_accvgpr_read_b32 v1, a12
	v_accvgpr_read_b32 v128, a13
	v_mfma_f32_16x16x32_f16 a[24:27], v[54:57], v[106:109], a[24:27]
	v_accvgpr_read_b32 v129, a14
	v_accvgpr_read_b32 v143, a15
	v_cvt_pk_f16_f32 v129, v129, v143
	v_mfma_f32_16x16x32_f16 a[28:31], v[10:13], v[106:109], a[28:31]
	ds_read_b128 v[106:109], v130 offset:50944
	v_cvt_pk_f16_f32 v128, v1, v128
	ds_write2_b64 v131, v[126:127], v[128:129] offset0:8 offset1:12
	s_waitcnt lgkmcnt(5)
	v_mfma_f32_16x16x32_f16 a[16:19], v[66:69], v[110:113], a[16:19]
	s_waitcnt vmcnt(3)
	v_mov_b32_e32 v94, v144
	s_waitcnt vmcnt(2)
	v_mov_b32_e32 v95, v30
	v_mov_b32_e32 v30, v145
	v_mfma_f32_16x16x32_f16 a[20:23], v[82:85], v[110:113], a[20:23]
	v_mov_b32_e32 v96, v146
	v_mov_b32_e32 v97, v32
	v_mov_b32_e32 v32, v147
	v_mfma_f32_16x16x32_f16 a[24:27], v[22:25], v[110:113], a[24:27]
	v_mfma_f32_16x16x32_f16 a[28:31], v[2:5], v[110:113], a[28:31]
	ds_read_b128 v[110:113], v130 offset:51008
	s_waitcnt lgkmcnt(2)
	v_mfma_f32_16x16x32_f16 a[32:35], v[74:77], v[106:109], 0
	v_mfma_f32_16x16x32_f16 a[0:3], v[50:53], v[106:109], 0
	v_mfma_f32_16x16x32_f16 a[16:19], v[62:65], v[118:121], a[16:19]
	v_mfma_f32_16x16x32_f16 a[20:23], v[86:89], v[118:121], a[20:23]
	v_mfma_f32_16x16x32_f16 a[24:27], v[18:21], v[118:121], a[24:27]
	s_nop 5
	v_accvgpr_read_b32 v1, a16
	v_accvgpr_read_b32 v126, a17
	v_accvgpr_read_b32 v127, a18
	v_mfma_f32_16x16x32_f16 a[28:31], v[6:9], v[118:121], a[28:31]
	ds_read_b128 v[118:121], v130 offset:51072
	v_accvgpr_read_b32 v128, a19
	v_cvt_pk_f16_f32 v126, v1, v126
	v_mfma_f32_16x16x32_f16 a[4:7], v[58:61], v[106:109], 0
	v_accvgpr_read_b32 v1, a20
	v_cvt_pk_f16_f32 v127, v127, v128
	v_accvgpr_read_b32 v128, a25
	s_waitcnt lgkmcnt(1)
	v_mfma_f32_16x16x32_f16 a[32:35], v[70:73], v[110:113], a[32:35]
	v_accvgpr_read_b32 v129, a27
	v_accvgpr_read_b32 v143, a29
	v_accvgpr_read_b32 v144, a31
	v_mfma_f32_16x16x32_f16 a[8:11], v[14:17], v[106:109], 0
	v_accvgpr_read_b32 v106, a21
	v_accvgpr_read_b32 v107, a22
	v_accvgpr_read_b32 v108, a23
	v_mfma_f32_16x16x32_f16 a[0:3], v[78:81], v[110:113], a[0:3]
	v_mfma_f32_16x16x32_f16 a[4:7], v[54:57], v[110:113], a[4:7]
	s_waitcnt lgkmcnt(0)
	v_mfma_f32_16x16x32_f16 a[32:35], v[66:69], v[118:121], a[32:35]
	v_mfma_f32_16x16x32_f16 a[8:11], v[10:13], v[110:113], a[8:11]
	v_cvt_pk_f16_f32 v111, v107, v108
	v_cvt_pk_f16_f32 v110, v1, v106
	v_add_u32_e32 v1, 0x2000, v131
	v_mfma_f32_16x16x32_f16 a[0:3], v[82:85], v[118:121], a[0:3]
	ds_write2_b64 v1, v[126:127], v[110:111] offset0:32 offset1:36
	v_accvgpr_read_b32 v126, a24
	v_accvgpr_read_b32 v127, a26
	v_mfma_f32_16x16x32_f16 a[4:7], v[22:25], v[118:121], a[4:7]
	ds_read_b128 v[106:109], v130 offset:55296
	ds_read_b128 v[110:113], v130 offset:55360
	v_cvt_pk_f16_f32 v127, v127, v129
	v_mfma_f32_16x16x32_f16 a[32:35], v[62:65], v[122:125], a[32:35]
	v_cvt_pk_f16_f32 v126, v126, v128
	v_accvgpr_read_b32 v128, a28
	v_accvgpr_read_b32 v129, a30
	v_mfma_f32_16x16x32_f16 a[8:11], v[2:5], v[118:121], a[8:11]
	v_cvt_pk_f16_f32 v129, v129, v144
	v_cvt_pk_f16_f32 v128, v128, v143
	ds_write2_b64 v1, v[126:127], v[128:129] offset0:40 offset1:44
	v_mfma_f32_16x16x32_f16 a[0:3], v[86:89], v[122:125], a[0:3]
	v_accvgpr_read_b32 v1, a32
	v_accvgpr_read_b32 v126, a33
	v_accvgpr_read_b32 v127, a34
	v_mfma_f32_16x16x32_f16 a[4:7], v[18:21], v[122:125], a[4:7]
	v_accvgpr_read_b32 v128, a35
	v_cvt_pk_f16_f32 v127, v127, v128
	v_cvt_pk_f16_f32 v126, v1, v126
	v_mfma_f32_16x16x32_f16 a[8:11], v[6:9], v[122:125], a[8:11]
	v_accvgpr_read_b32 v1, a0
	v_accvgpr_read_b32 v128, a1
	v_accvgpr_read_b32 v129, a2
	v_accvgpr_read_b32 v143, a3
	v_cvt_pk_f16_f32 v129, v129, v143
	v_cvt_pk_f16_f32 v128, v1, v128
	v_add_u32_e32 v1, 0x4000, v131
	s_waitcnt lgkmcnt(2)
	v_mfma_f32_16x16x32_f16 a[12:15], v[74:77], v[106:109], 0
	ds_write2_b64 v1, v[126:127], v[128:129] offset0:64 offset1:68
	v_accvgpr_read_b32 v126, a4
	v_accvgpr_read_b32 v128, a5
	v_mfma_f32_16x16x32_f16 a[16:19], v[50:53], v[106:109], 0
	v_accvgpr_read_b32 v127, a6
	v_accvgpr_read_b32 v129, a7
	v_cvt_pk_f16_f32 v126, v126, v128
	v_mfma_f32_16x16x32_f16 a[20:23], v[58:61], v[106:109], 0
	v_accvgpr_read_b32 v128, a8
	v_cvt_pk_f16_f32 v127, v127, v129
	ds_read_b128 v[118:121], v130 offset:55424
	ds_read_b128 v[122:125], v130 offset:55488
	v_mfma_f32_16x16x32_f16 a[4:7], v[14:17], v[106:109], 0
	v_accvgpr_read_b32 v106, a9
	v_accvgpr_read_b32 v107, a10
	v_accvgpr_read_b32 v108, a11
	v_cvt_pk_f16_f32 v107, v107, v108
	v_cvt_pk_f16_f32 v106, v128, v106
	ds_write2_b64 v1, v[126:127], v[106:107] offset0:72 offset1:76
	ds_read_b128 v[106:109], v130 offset:59648
	s_waitcnt lgkmcnt(6)
	v_mfma_f32_16x16x32_f16 a[12:15], v[70:73], v[110:113], a[12:15]
	v_mfma_f32_16x16x32_f16 a[16:19], v[78:81], v[110:113], a[16:19]
	v_mfma_f32_16x16x32_f16 a[0:3], v[54:57], v[110:113], a[20:23]
	v_mfma_f32_16x16x32_f16 a[4:7], v[10:13], v[110:113], a[4:7]
	ds_read_b128 v[110:113], v130 offset:59712
	s_waitcnt lgkmcnt(4)
	v_mfma_f32_16x16x32_f16 a[12:15], v[66:69], v[118:121], a[12:15]
	s_waitcnt lgkmcnt(1)
	v_mfma_f32_16x16x32_f16 a[8:11], v[74:77], v[106:109], 0
	ds_read_b128 v[74:77], v130 offset:59776
	v_mfma_f32_16x16x32_f16 a[0:3], v[22:25], v[118:121], a[0:3]
	v_mfma_f32_16x16x32_f16 a[12:15], v[62:65], v[122:125], a[12:15]
	v_mfma_f32_16x16x32_f16 a[4:7], v[2:5], v[118:121], a[4:7]
	s_waitcnt lgkmcnt(1)
	v_mfma_f32_16x16x32_f16 a[8:11], v[70:73], v[110:113], a[8:11]
	ds_read_b128 v[70:73], v130 offset:59840
	s_nop 3
	v_accvgpr_read_b32 v1, a12
	v_mfma_f32_16x16x32_f16 a[0:3], v[18:21], v[122:125], a[0:3]
	v_mfma_f32_16x16x32_f16 a[16:19], v[82:85], v[118:121], a[16:19]
	v_accvgpr_read_b32 v118, a13
	v_accvgpr_read_b32 v119, a14
	v_accvgpr_read_b32 v120, a15
	v_mfma_f32_16x16x32_f16 a[4:7], v[6:9], v[122:125], a[4:7]
	v_cvt_pk_f16_f32 v119, v119, v120
	v_cvt_pk_f16_f32 v118, v1, v118
	s_waitcnt lgkmcnt(1)
	v_mfma_f32_16x16x32_f16 a[8:11], v[66:69], v[74:77], a[8:11]
	v_mfma_f32_16x16x32_f16 a[12:15], v[50:53], v[106:109], 0
	v_accvgpr_read_b32 v50, a0
	v_accvgpr_read_b32 v52, a1
	v_accvgpr_read_b32 v51, a2
	v_accvgpr_read_b32 v53, a3
	s_waitcnt lgkmcnt(0)
	v_mfma_f32_16x16x32_f16 a[8:11], v[62:65], v[70:73], a[8:11]
	v_cvt_pk_f16_f32 v51, v51, v53
	v_cvt_pk_f16_f32 v50, v50, v52
	v_accvgpr_read_b32 v52, a4
	v_mfma_f32_16x16x32_f16 a[12:15], v[78:81], v[110:113], a[12:15]
	v_accvgpr_read_b32 v62, a5
	v_accvgpr_read_b32 v53, a6
	v_accvgpr_read_b32 v63, a7
	v_mfma_f32_16x16x32_f16 a[4:7], v[58:61], v[106:109], 0
	v_cvt_pk_f16_f32 v53, v53, v63
	v_cvt_pk_f16_f32 v52, v52, v62
	v_mfma_f32_16x16x32_f16 a[0:3], v[82:85], v[74:77], a[12:15]
	v_mfma_f32_16x16x32_f16 a[4:7], v[54:57], v[110:113], a[4:7]
	v_mfma_f32_16x16x32_f16 a[16:19], v[86:89], v[122:125], a[16:19]
	v_mfma_f32_16x16x32_f16 a[0:3], v[86:89], v[70:73], a[0:3]
	v_mfma_f32_16x16x32_f16 a[4:7], v[22:25], v[74:77], a[4:7]
	s_nop 5
	v_accvgpr_read_b32 v1, a16
	v_accvgpr_read_b32 v120, a17
	v_accvgpr_read_b32 v66, a18
	v_accvgpr_read_b32 v67, a19
	v_cvt_pk_f16_f32 v67, v66, v67
	v_cvt_pk_f16_f32 v66, v1, v120
	v_add_u32_e32 v1, 0x6000, v131
	ds_write2_b64 v1, v[118:119], v[66:67] offset0:96 offset1:100
	ds_write2_b64 v1, v[50:51], v[52:53] offset0:104 offset1:108
	v_accvgpr_read_b32 v1, a8
	v_accvgpr_read_b32 v50, a9
	v_cvt_pk_f16_f32 v50, v1, v50
	v_accvgpr_read_b32 v1, a0
	v_accvgpr_read_b32 v22, a1
	v_mfma_f32_16x16x32_f16 a[4:7], v[18:21], v[70:73], a[4:7]
	v_accvgpr_read_b32 v18, a2
	v_accvgpr_read_b32 v19, a3
	v_accvgpr_read_b32 v51, a10
	v_mfma_f32_16x16x32_f16 a[0:3], v[14:17], v[106:109], 0
	v_accvgpr_read_b32 v52, a11
	v_cvt_pk_f16_f32 v51, v51, v52
	v_cvt_pk_f16_f32 v19, v18, v19
	v_mfma_f32_16x16x32_f16 a[0:3], v[10:13], v[110:113], a[0:3]
	v_accvgpr_read_b32 v10, a4
	v_accvgpr_read_b32 v11, a5
	v_accvgpr_read_b32 v12, a6
	v_mfma_f32_16x16x32_f16 a[0:3], v[2:5], v[74:77], a[0:3]
	v_accvgpr_read_b32 v2, a7
	v_cvt_pk_f16_f32 v18, v1, v22
	v_add_u32_e32 v1, 0x8000, v131
	v_mfma_f32_16x16x32_f16 a[0:3], v[6:9], v[70:73], a[0:3]
	v_cvt_pk_f16_f32 v3, v12, v2
	v_cvt_pk_f16_f32 v2, v10, v11
	ds_write2_b64 v1, v[50:51], v[18:19] offset0:128 offset1:132
	s_nop 4
	v_accvgpr_read_b32 v4, a0
	v_accvgpr_read_b32 v6, a1
	v_accvgpr_read_b32 v5, a2
	v_accvgpr_read_b32 v7, a3
	v_cvt_pk_f16_f32 v5, v5, v7
	v_cvt_pk_f16_f32 v4, v4, v6
	ds_write2_b64 v1, v[2:3], v[4:5] offset0:136 offset1:140
	global_load_dwordx4 v[2:5], v132, s[10:11] offset:48
	global_load_dwordx4 v[6:9], v132, s[10:11] offset:32
	global_load_dwordx4 v[10:13], v132, s[10:11] offset:16
	global_load_dwordx4 v[14:17], v132, s[10:11]
	global_load_dwordx4 v[18:21], v133, s[6:7] offset:16
	global_load_dwordx4 v[22:25], v133, s[6:7]
	global_load_dword v1, v90, s[8:9]
	s_waitcnt lgkmcnt(0)
	s_barrier
	ds_read_b128 v[50:53], v93 offset:6864
	ds_read_b128 v[82:85], v93 offset:7392
	ds_read_b128 v[106:109], v93 offset:7920
	ds_read_b128 v[118:121], v93 offset:8448
	ds_read_b128 v[62:65], v93 offset:8976
	ds_read_b128 v[70:73], v93 offset:9504
	ds_read_b128 v[78:81], v93 offset:10032
	ds_read_b128 v[74:77], v93 offset:10560
	s_waitcnt lgkmcnt(7)
	v_cvt_f32_f16_e32 v54, v50
	v_cvt_f32_f16_sdwa v55, v50 dst_sel:DWORD dst_unused:UNUSED_PAD src0_sel:WORD_1
	s_waitcnt lgkmcnt(6)
	v_cvt_f32_f16_e32 v122, v82
	v_cvt_f32_f16_sdwa v123, v82 dst_sel:DWORD dst_unused:UNUSED_PAD src0_sel:WORD_1
	s_waitcnt lgkmcnt(5)
	v_cvt_f32_f16_e32 v110, v106
	v_cvt_f32_f16_sdwa v111, v106 dst_sel:DWORD dst_unused:UNUSED_PAD src0_sel:WORD_1
	s_waitcnt lgkmcnt(4)
	v_cvt_f32_f16_e32 v86, v118
	v_cvt_f32_f16_sdwa v87, v118 dst_sel:DWORD dst_unused:UNUSED_PAD src0_sel:WORD_1
	s_waitcnt vmcnt(7)
	v_pk_fma_f32 v[54:55], v[102:103], v[54:55], v[46:47]
	v_cvt_f32_f16_e32 v126, v83
	v_pk_fma_f32 v[54:55], v[42:43], v[122:123], v[54:55]
	v_cvt_f32_f16_sdwa v127, v83 dst_sel:DWORD dst_unused:UNUSED_PAD src0_sel:WORD_1
	v_pk_fma_f32 v[54:55], v[104:105], v[110:111], v[54:55]
	v_cvt_f32_f16_e32 v112, v107
	v_pk_fma_f32 v[124:125], v[44:45], v[86:87], v[54:55]
	v_cvt_f32_f16_sdwa v55, v51 dst_sel:DWORD dst_unused:UNUSED_PAD src0_sel:WORD_1
	v_mul_f32_e32 v54, 0xbfb8aa3b, v125
	v_exp_f32_e32 v54, v54
	v_cvt_f32_f16_sdwa v113, v107 dst_sel:DWORD dst_unused:UNUSED_PAD src0_sel:WORD_1
	v_cvt_f32_f16_e32 v88, v119
	v_cvt_f32_f16_sdwa v89, v119 dst_sel:DWORD dst_unused:UNUSED_PAD src0_sel:WORD_1
	v_add_f32_e32 v56, 1.0, v54
	v_cvt_f32_f16_e32 v54, v51
	v_mul_f32_e32 v50, 0xbfb8aa3b, v124
	v_exp_f32_e32 v50, v50
	v_cvt_f32_f16_e32 v118, v52
	v_pk_fma_f32 v[54:55], v[98:99], v[54:55], v[48:49]
	v_cvt_f32_f16_sdwa v119, v52 dst_sel:DWORD dst_unused:UNUSED_PAD src0_sel:WORD_1
	v_pk_fma_f32 v[54:55], v[38:39], v[126:127], v[54:55]
	v_add_f32_e32 v50, 1.0, v50
	v_pk_fma_f32 v[54:55], v[100:101], v[112:113], v[54:55]
	v_rcp_f32_e32 v50, v50
	v_pk_fma_f32 v[82:83], v[40:41], v[88:89], v[54:55]
	v_cvt_f32_f16_e32 v144, v108
	v_mul_f32_e32 v51, 0xbfb8aa3b, v82
	v_exp_f32_e32 v54, v51
	v_mul_f32_e32 v51, 0xbfb8aa3b, v83
	v_exp_f32_e32 v55, v51
	v_rcp_f32_e32 v51, v56
	v_add_f32_e32 v54, 1.0, v54
	v_rcp_f32_e32 v106, v54
	v_add_f32_e32 v54, 1.0, v55
	v_rcp_f32_e32 v107, v54
	v_pk_mul_f32 v[50:51], v[124:125], v[50:51]
	v_cvt_f32_f16_e32 v124, v84
	v_cvt_f32_f16_sdwa v125, v84 dst_sel:DWORD dst_unused:UNUSED_PAD src0_sel:WORD_1
	v_cvt_f32_f16_sdwa v145, v108 dst_sel:DWORD dst_unused:UNUSED_PAD src0_sel:WORD_1
	v_pk_mul_f32 v[82:83], v[82:83], v[106:107]
	v_cvt_f32_f16_e32 v106, v120
	v_cvt_f32_f16_sdwa v107, v120 dst_sel:DWORD dst_unused:UNUSED_PAD src0_sel:WORD_1
	v_pk_fma_f32 v[118:119], v[94:95], v[118:119], v[34:35]
	v_cvt_pk_f16_f32 v50, v50, v51
	v_pk_fma_f32 v[118:119], v[30:31], v[124:125], v[118:119]
	v_cvt_f32_f16_e32 v146, v85
	v_pk_fma_f32 v[118:119], v[96:97], v[144:145], v[118:119]
	v_cvt_f32_f16_sdwa v147, v85 dst_sel:DWORD dst_unused:UNUSED_PAD src0_sel:WORD_1
	v_pk_fma_f32 v[118:119], v[32:33], v[106:107], v[118:119]
	v_cvt_f32_f16_e32 v108, v121
	v_mul_f32_e32 v51, 0xbfb8aa3b, v118
	v_exp_f32_e32 v52, v51
	v_mul_f32_e32 v51, 0xbfb8aa3b, v119
	v_exp_f32_e32 v84, v51
	v_cvt_pk_f16_f32 v51, v82, v83
	v_add_f32_e32 v52, 1.0, v52
	v_rcp_f32_e32 v128, v52
	v_add_f32_e32 v52, 1.0, v84
	v_rcp_f32_e32 v129, v52
	v_cvt_f32_f16_e32 v52, v53
	v_cvt_f32_f16_sdwa v53, v53 dst_sel:DWORD dst_unused:UNUSED_PAD src0_sel:WORD_1
	v_mov_b32_e32 v82, v114
	v_mov_b32_e32 v83, v26
	v_mov_b32_e32 v26, v115
	v_cvt_f32_f16_e32 v114, v109
	v_cvt_f32_f16_sdwa v115, v109 dst_sel:DWORD dst_unused:UNUSED_PAD src0_sel:WORD_1
	v_cvt_f32_f16_sdwa v109, v121 dst_sel:DWORD dst_unused:UNUSED_PAD src0_sel:WORD_1
	v_pk_fma_f32 v[52:53], v[82:83], v[52:53], v[36:37]
	v_mov_b32_e32 v84, v116
	v_pk_fma_f32 v[52:53], v[26:27], v[146:147], v[52:53]
	v_mov_b32_e32 v85, v28
	v_pk_fma_f32 v[52:53], v[84:85], v[114:115], v[52:53]
	v_mov_b32_e32 v28, v117
	v_pk_fma_f32 v[116:117], v[28:29], v[108:109], v[52:53]
	s_waitcnt lgkmcnt(3)
	v_cvt_f32_f16_e32 v132, v62
	v_mul_f32_e32 v52, 0xbfb8aa3b, v116
	v_exp_f32_e32 v120, v52
	v_mul_f32_e32 v52, 0xbfb8aa3b, v117
	v_exp_f32_e32 v121, v52
	v_cvt_f32_f16_sdwa v133, v62 dst_sel:DWORD dst_unused:UNUSED_PAD src0_sel:WORD_1
	v_pk_mul_f32 v[52:53], v[118:119], v[128:129]
	v_add_f32_e32 v118, 1.0, v120
	v_add_f32_e32 v119, 1.0, v121
	v_pk_fma_f32 v[120:121], v[102:103], v[122:123], v[46:47]
	v_rcp_f32_e32 v118, v118
	v_pk_fma_f32 v[120:121], v[42:43], v[110:111], v[120:121]
	v_rcp_f32_e32 v119, v119
	v_pk_fma_f32 v[120:121], v[104:105], v[86:87], v[120:121]
	v_cvt_f32_f16_e32 v130, v63
	v_pk_fma_f32 v[120:121], v[44:45], v[132:133], v[120:121]
	v_cvt_f32_f16_sdwa v131, v63 dst_sel:DWORD dst_unused:UNUSED_PAD src0_sel:WORD_1
	v_mul_f32_e32 v62, 0xbfb8aa3b, v120
	v_exp_f32_e32 v62, v62
	v_mul_f32_e32 v122, 0xbfb8aa3b, v121
	v_exp_f32_e32 v123, v122
	v_pk_mul_f32 v[116:117], v[116:117], v[118:119]
	v_add_f32_e32 v62, 1.0, v62
	v_rcp_f32_e32 v122, v62
	v_add_f32_e32 v62, 1.0, v123
	v_rcp_f32_e32 v123, v62
	v_pk_fma_f32 v[62:63], v[98:99], v[126:127], v[48:49]
	v_cvt_pk_f16_f32 v52, v52, v53
	v_pk_fma_f32 v[62:63], v[38:39], v[112:113], v[62:63]
	v_cvt_pk_f16_f32 v53, v116, v117
	v_pk_fma_f32 v[62:63], v[100:101], v[88:89], v[62:63]
	v_pk_mul_f32 v[116:117], v[120:121], v[122:123]
	v_pk_fma_f32 v[118:119], v[40:41], v[130:131], v[62:63]
	v_cvt_f32_f16_e32 v128, v64
	v_mul_f32_e32 v62, 0xbfb8aa3b, v118
	v_exp_f32_e32 v63, v62
	v_mul_f32_e32 v62, 0xbfb8aa3b, v119
	v_exp_f32_e32 v120, v62
	v_cvt_f32_f16_sdwa v129, v64 dst_sel:DWORD dst_unused:UNUSED_PAD src0_sel:WORD_1
	v_add_f32_e32 v63, 1.0, v63
	v_cvt_pk_f16_f32 v62, v116, v117
	v_rcp_f32_e32 v116, v63
	v_add_f32_e32 v63, 1.0, v120
	v_pk_fma_f32 v[120:121], v[94:95], v[124:125], v[34:35]
	v_rcp_f32_e32 v117, v63
	v_pk_fma_f32 v[120:121], v[30:31], v[144:145], v[120:121]
	v_cvt_f32_f16_e32 v126, v65
	v_pk_fma_f32 v[120:121], v[96:97], v[106:107], v[120:121]
	v_cvt_f32_f16_sdwa v127, v65 dst_sel:DWORD dst_unused:UNUSED_PAD src0_sel:WORD_1
	v_pk_fma_f32 v[120:121], v[32:33], v[128:129], v[120:121]
	v_pk_mul_f32 v[116:117], v[118:119], v[116:117]
	v_mul_f32_e32 v63, 0xbfb8aa3b, v120
	v_exp_f32_e32 v63, v63
	v_mul_f32_e32 v64, 0xbfb8aa3b, v121
	v_pk_fma_f32 v[118:119], v[82:83], v[146:147], v[36:37]
	v_exp_f32_e32 v122, v64
	v_pk_fma_f32 v[118:119], v[26:27], v[114:115], v[118:119]
	v_add_f32_e32 v63, 1.0, v63
	v_pk_fma_f32 v[118:119], v[84:85], v[108:109], v[118:119]
	v_rcp_f32_e32 v64, v63
	v_pk_fma_f32 v[118:119], v[28:29], v[126:127], v[118:119]
	v_add_f32_e32 v63, 1.0, v122
	v_mul_f32_e32 v65, 0xbfb8aa3b, v118
	v_exp_f32_e32 v122, v65
	v_mul_f32_e32 v65, 0xbfb8aa3b, v119
	v_exp_f32_e32 v123, v65
	v_rcp_f32_e32 v65, v63
	s_waitcnt lgkmcnt(2)
	v_cvt_f32_f16_e32 v124, v70
	v_cvt_f32_f16_sdwa v125, v70 dst_sel:DWORD dst_unused:UNUSED_PAD src0_sel:WORD_1
	v_add_f32_e32 v63, 1.0, v122
	v_pk_fma_f32 v[110:111], v[102:103], v[110:111], v[46:47]
	v_rcp_f32_e32 v122, v63
	v_add_f32_e32 v63, 1.0, v123
	v_pk_fma_f32 v[110:111], v[42:43], v[86:87], v[110:111]
	v_rcp_f32_e32 v123, v63
	v_pk_fma_f32 v[110:111], v[104:105], v[132:133], v[110:111]
	v_pk_mul_f32 v[64:65], v[120:121], v[64:65]
	v_pk_fma_f32 v[110:111], v[44:45], v[124:125], v[110:111]
	v_cvt_pk_f16_f32 v64, v64, v65
	v_mul_f32_e32 v65, 0xbfb8aa3b, v110
	v_exp_f32_e32 v70, v65
	v_mul_f32_e32 v65, 0xbfb8aa3b, v111
	v_cvt_pk_f16_f32 v63, v116, v117
	v_pk_mul_f32 v[116:117], v[118:119], v[122:123]
	v_exp_f32_e32 v118, v65
	v_add_f32_e32 v70, 1.0, v70
	v_cvt_pk_f16_f32 v65, v116, v117
	v_rcp_f32_e32 v116, v70
	v_add_f32_e32 v70, 1.0, v118
	v_cvt_f32_f16_e32 v122, v71
	v_cvt_f32_f16_sdwa v123, v71 dst_sel:DWORD dst_unused:UNUSED_PAD src0_sel:WORD_1
	v_rcp_f32_e32 v117, v70
	v_pk_fma_f32 v[70:71], v[98:99], v[112:113], v[48:49]
	v_cvt_f32_f16_e32 v120, v72
	v_pk_fma_f32 v[70:71], v[38:39], v[88:89], v[70:71]
	v_cvt_f32_f16_sdwa v121, v72 dst_sel:DWORD dst_unused:UNUSED_PAD src0_sel:WORD_1
	v_pk_fma_f32 v[70:71], v[100:101], v[130:131], v[70:71]
	v_pk_fma_f32 v[86:87], v[102:103], v[86:87], v[46:47]
	v_pk_fma_f32 v[112:113], v[40:41], v[122:123], v[70:71]
	v_pk_fma_f32 v[86:87], v[42:43], v[132:133], v[86:87]
	v_mul_f32_e32 v70, 0xbfb8aa3b, v112
	v_exp_f32_e32 v118, v70
	v_mul_f32_e32 v70, 0xbfb8aa3b, v113
	v_exp_f32_e32 v119, v70
	v_pk_mul_f32 v[70:71], v[110:111], v[116:117]
	v_pk_fma_f32 v[116:117], v[94:95], v[144:145], v[34:35]
	v_add_f32_e32 v110, 1.0, v118
	v_pk_fma_f32 v[116:117], v[30:31], v[106:107], v[116:117]
	v_add_f32_e32 v111, 1.0, v119
	v_pk_fma_f32 v[116:117], v[96:97], v[128:129], v[116:117]
	v_rcp_f32_e32 v110, v110
	v_pk_fma_f32 v[116:117], v[32:33], v[120:121], v[116:117]
	v_rcp_f32_e32 v111, v111
	v_mul_f32_e32 v72, 0xbfb8aa3b, v116
	v_exp_f32_e32 v72, v72
	v_mul_f32_e32 v118, 0xbfb8aa3b, v117
	v_exp_f32_e32 v119, v118
	v_pk_mul_f32 v[110:111], v[112:113], v[110:111]
	v_add_f32_e32 v72, 1.0, v72
	v_rcp_f32_e32 v118, v72
	v_add_f32_e32 v72, 1.0, v119
	v_rcp_f32_e32 v119, v72
	v_cvt_pk_f16_f32 v70, v70, v71
	v_cvt_pk_f16_f32 v71, v110, v111
	v_pk_fma_f32 v[86:87], v[104:105], v[124:125], v[86:87]
	v_pk_mul_f32 v[110:111], v[116:117], v[118:119]
	v_cvt_f32_f16_e32 v118, v73
	v_cvt_f32_f16_sdwa v119, v73 dst_sel:DWORD dst_unused:UNUSED_PAD src0_sel:WORD_1
	v_pk_fma_f32 v[72:73], v[82:83], v[114:115], v[36:37]
	s_waitcnt lgkmcnt(1)
	v_cvt_f32_f16_e32 v116, v78
	v_pk_fma_f32 v[72:73], v[26:27], v[108:109], v[72:73]
	v_cvt_f32_f16_sdwa v117, v78 dst_sel:DWORD dst_unused:UNUSED_PAD src0_sel:WORD_1
	v_pk_fma_f32 v[72:73], v[84:85], v[126:127], v[72:73]
	v_cvt_f32_f16_sdwa v115, v79 dst_sel:DWORD dst_unused:UNUSED_PAD src0_sel:WORD_1
	v_pk_fma_f32 v[112:113], v[28:29], v[118:119], v[72:73]
	v_pk_fma_f32 v[86:87], v[44:45], v[116:117], v[86:87]
	v_mul_f32_e32 v72, 0xbfb8aa3b, v112
	v_exp_f32_e32 v73, v72
	v_mul_f32_e32 v72, 0xbfb8aa3b, v113
	v_exp_f32_e32 v114, v72
	v_cvt_pk_f16_f32 v72, v110, v111
	v_add_f32_e32 v73, 1.0, v73
	v_rcp_f32_e32 v110, v73
	v_add_f32_e32 v73, 1.0, v114
	v_rcp_f32_e32 v111, v73
	v_mul_f32_e32 v73, 0xbfb8aa3b, v86
	v_exp_f32_e32 v73, v73
	v_mul_f32_e32 v78, 0xbfb8aa3b, v87
	v_exp_f32_e32 v114, v78
	v_pk_fma_f32 v[88:89], v[98:99], v[88:89], v[48:49]
	v_add_f32_e32 v73, 1.0, v73
	v_rcp_f32_e32 v78, v73
	v_add_f32_e32 v73, 1.0, v114
	v_cvt_f32_f16_e32 v114, v79
	v_pk_fma_f32 v[88:89], v[38:39], v[130:131], v[88:89]
	v_pk_mul_f32 v[110:111], v[112:113], v[110:111]
	v_pk_fma_f32 v[88:89], v[100:101], v[122:123], v[88:89]
	ds_read_b128 v[66:69], v93 offset:11088
	ds_read_b128 v[58:61], v93 offset:11616
	v_pk_fma_f32 v[88:89], v[40:41], v[114:115], v[88:89]
	ds_read_b128 v[54:57], v93 offset:12144
	v_mul_f32_e32 v79, 0xbfb8aa3b, v88
	v_exp_f32_e32 v112, v79
	v_mul_f32_e32 v79, 0xbfb8aa3b, v89
	v_exp_f32_e32 v113, v79
	v_rcp_f32_e32 v79, v73
	v_add_f32_e32 v73, 1.0, v112
	v_rcp_f32_e32 v112, v73
	v_add_f32_e32 v73, 1.0, v113
	v_rcp_f32_e32 v113, v73
	v_pk_mul_f32 v[78:79], v[86:87], v[78:79]
	v_cvt_pk_f16_f32 v73, v110, v111
	v_cvt_pk_f16_f32 v78, v78, v79
	v_pk_mul_f32 v[86:87], v[88:89], v[112:113]
	v_cvt_f32_f16_e32 v112, v80
	v_cvt_f32_f16_sdwa v113, v80 dst_sel:DWORD dst_unused:UNUSED_PAD src0_sel:WORD_1
	v_pk_fma_f32 v[88:89], v[94:95], v[106:107], v[34:35]
	v_cvt_f32_f16_e32 v110, v81
	v_pk_fma_f32 v[88:89], v[30:31], v[128:129], v[88:89]
	v_cvt_f32_f16_sdwa v111, v81 dst_sel:DWORD dst_unused:UNUSED_PAD src0_sel:WORD_1
	v_pk_fma_f32 v[88:89], v[96:97], v[120:121], v[88:89]
	v_pk_fma_f32 v[128:129], v[94:95], v[128:129], v[34:35]
	v_pk_fma_f32 v[88:89], v[32:33], v[112:113], v[88:89]
	v_pk_fma_f32 v[128:129], v[30:31], v[120:121], v[128:129]
	v_mul_f32_e32 v79, 0xbfb8aa3b, v88
	v_exp_f32_e32 v80, v79
	v_mul_f32_e32 v79, 0xbfb8aa3b, v89
	v_exp_f32_e32 v106, v79
	v_cvt_pk_f16_f32 v79, v86, v87
	v_add_f32_e32 v80, 1.0, v80
	v_rcp_f32_e32 v86, v80
	v_add_f32_e32 v80, 1.0, v106
	v_rcp_f32_e32 v87, v80
	v_pk_fma_f32 v[80:81], v[82:83], v[108:109], v[36:37]
	v_pk_fma_f32 v[128:129], v[96:97], v[112:113], v[128:129]
	v_pk_fma_f32 v[80:81], v[26:27], v[126:127], v[80:81]
	v_pk_fma_f32 v[126:127], v[82:83], v[126:127], v[36:37]
	v_pk_fma_f32 v[80:81], v[84:85], v[118:119], v[80:81]
	v_pk_fma_f32 v[126:127], v[26:27], v[118:119], v[126:127]
	v_pk_fma_f32 v[106:107], v[28:29], v[110:111], v[80:81]
	v_pk_fma_f32 v[126:127], v[84:85], v[110:111], v[126:127]
	v_mul_f32_e32 v80, 0xbfb8aa3b, v106
	v_exp_f32_e32 v108, v80
	v_mul_f32_e32 v80, 0xbfb8aa3b, v107
	v_exp_f32_e32 v109, v80
	v_pk_mul_f32 v[80:81], v[88:89], v[86:87]
	v_add_f32_e32 v86, 1.0, v108
	s_waitcnt lgkmcnt(3)
	v_cvt_f32_f16_e32 v108, v74
	v_add_f32_e32 v87, 1.0, v109
	v_cvt_f32_f16_sdwa v109, v74 dst_sel:DWORD dst_unused:UNUSED_PAD src0_sel:WORD_1
	v_pk_fma_f32 v[88:89], v[102:103], v[132:133], v[46:47]
	v_rcp_f32_e32 v86, v86
	v_pk_fma_f32 v[88:89], v[42:43], v[124:125], v[88:89]
	v_rcp_f32_e32 v87, v87
	v_pk_fma_f32 v[88:89], v[104:105], v[116:117], v[88:89]
	v_cvt_pk_f16_f32 v80, v80, v81
	v_pk_fma_f32 v[88:89], v[44:45], v[108:109], v[88:89]
	v_pk_mul_f32 v[86:87], v[106:107], v[86:87]
	v_mul_f32_e32 v74, 0xbfb8aa3b, v88
	v_exp_f32_e32 v74, v74
	v_mul_f32_e32 v132, 0xbfb8aa3b, v89
	v_exp_f32_e32 v133, v132
	v_cvt_f32_f16_e32 v106, v75
	v_add_f32_e32 v74, 1.0, v74
	v_rcp_f32_e32 v132, v74
	v_add_f32_e32 v74, 1.0, v133
	v_cvt_f32_f16_sdwa v107, v75 dst_sel:DWORD dst_unused:UNUSED_PAD src0_sel:WORD_1
	v_rcp_f32_e32 v133, v74
	v_pk_fma_f32 v[74:75], v[98:99], v[130:131], v[48:49]
	v_cvt_pk_f16_f32 v81, v86, v87
	v_pk_fma_f32 v[74:75], v[38:39], v[122:123], v[74:75]
	v_pk_mul_f32 v[86:87], v[88:89], v[132:133]
	v_pk_fma_f32 v[74:75], v[100:101], v[114:115], v[74:75]
	v_cvt_f32_f16_sdwa v89, v76 dst_sel:DWORD dst_unused:UNUSED_PAD src0_sel:WORD_1
	v_pk_fma_f32 v[130:131], v[40:41], v[106:107], v[74:75]
	v_pk_fma_f32 v[124:125], v[102:103], v[124:125], v[46:47]
	v_mul_f32_e32 v74, 0xbfb8aa3b, v130
	v_exp_f32_e32 v75, v74
	v_mul_f32_e32 v74, 0xbfb8aa3b, v131
	v_exp_f32_e32 v88, v74
	v_cvt_pk_f16_f32 v74, v86, v87
	v_add_f32_e32 v75, 1.0, v75
	v_rcp_f32_e32 v86, v75
	v_add_f32_e32 v75, 1.0, v88
	v_cvt_f32_f16_e32 v88, v76
	v_rcp_f32_e32 v87, v75
	v_pk_fma_f32 v[124:125], v[42:43], v[116:117], v[124:125]
	v_pk_fma_f32 v[120:121], v[94:95], v[120:121], v[34:35]
	v_pk_fma_f32 v[128:129], v[32:33], v[88:89], v[128:129]
	v_pk_mul_f32 v[130:131], v[130:131], v[86:87]
	v_mul_f32_e32 v75, 0xbfb8aa3b, v128
	v_cvt_f32_f16_e32 v86, v77
	v_cvt_f32_f16_sdwa v87, v77 dst_sel:DWORD dst_unused:UNUSED_PAD src0_sel:WORD_1
	v_exp_f32_e32 v75, v75
	v_mul_f32_e32 v76, 0xbfb8aa3b, v129
	v_exp_f32_e32 v132, v76
	v_pk_fma_f32 v[126:127], v[28:29], v[86:87], v[126:127]
	v_add_f32_e32 v75, 1.0, v75
	v_mul_f32_e32 v77, 0xbfb8aa3b, v126
	v_rcp_f32_e32 v76, v75
	v_add_f32_e32 v75, 1.0, v132
	v_exp_f32_e32 v132, v77
	v_mul_f32_e32 v77, 0xbfb8aa3b, v127
	v_exp_f32_e32 v133, v77
	v_rcp_f32_e32 v77, v75
	v_pk_fma_f32 v[124:125], v[104:105], v[108:109], v[124:125]
	v_add_f32_e32 v75, 1.0, v132
	v_rcp_f32_e32 v132, v75
	v_pk_mul_f32 v[76:77], v[128:129], v[76:77]
	s_waitcnt lgkmcnt(2)
	v_cvt_f32_f16_e32 v128, v66
	v_cvt_f32_f16_sdwa v129, v66 dst_sel:DWORD dst_unused:UNUSED_PAD src0_sel:WORD_1
	v_add_f32_e32 v75, 1.0, v133
	v_rcp_f32_e32 v133, v75
	v_cvt_pk_f16_f32 v76, v76, v77
	v_pk_fma_f32 v[124:125], v[44:45], v[128:129], v[124:125]
	v_cvt_pk_f16_f32 v75, v130, v131
	v_mul_f32_e32 v66, 0xbfb8aa3b, v124
	v_exp_f32_e32 v66, v66
	v_mul_f32_e32 v77, 0xbfb8aa3b, v125
	v_exp_f32_e32 v130, v77
	v_pk_mul_f32 v[126:127], v[126:127], v[132:133]
	v_add_f32_e32 v66, 1.0, v66
	v_cvt_pk_f16_f32 v77, v126, v127
	v_rcp_f32_e32 v126, v66
	v_add_f32_e32 v66, 1.0, v130
	v_cvt_f32_f16_e32 v130, v67
	v_cvt_f32_f16_sdwa v131, v67 dst_sel:DWORD dst_unused:UNUSED_PAD src0_sel:WORD_1
	v_rcp_f32_e32 v127, v66
	v_pk_fma_f32 v[66:67], v[98:99], v[122:123], v[48:49]
	v_pk_fma_f32 v[120:121], v[30:31], v[112:113], v[120:121]
	v_pk_fma_f32 v[66:67], v[38:39], v[114:115], v[66:67]
	v_pk_fma_f32 v[120:121], v[96:97], v[88:89], v[120:121]
	v_pk_fma_f32 v[66:67], v[100:101], v[106:107], v[66:67]
	v_pk_fma_f32 v[116:117], v[102:103], v[116:117], v[46:47]
	v_pk_fma_f32 v[122:123], v[40:41], v[130:131], v[66:67]
	v_pk_fma_f32 v[116:117], v[42:43], v[108:109], v[116:117]
	v_mul_f32_e32 v66, 0xbfb8aa3b, v122
	v_exp_f32_e32 v132, v66
	v_mul_f32_e32 v66, 0xbfb8aa3b, v123
	v_exp_f32_e32 v133, v66
	v_pk_mul_f32 v[66:67], v[124:125], v[126:127]
	v_cvt_f32_f16_e32 v126, v68
	v_cvt_f32_f16_sdwa v127, v68 dst_sel:DWORD dst_unused:UNUSED_PAD src0_sel:WORD_1
	v_add_f32_e32 v124, 1.0, v132
	v_add_f32_e32 v125, 1.0, v133
	v_rcp_f32_e32 v124, v124
	v_pk_fma_f32 v[120:121], v[32:33], v[126:127], v[120:121]
	v_rcp_f32_e32 v125, v125
	v_mul_f32_e32 v68, 0xbfb8aa3b, v120
	v_exp_f32_e32 v68, v68
	v_mul_f32_e32 v132, 0xbfb8aa3b, v121
	v_exp_f32_e32 v133, v132
	v_pk_mul_f32 v[122:123], v[122:123], v[124:125]
	v_add_f32_e32 v68, 1.0, v68
	v_rcp_f32_e32 v132, v68
	v_add_f32_e32 v68, 1.0, v133
	v_cvt_pk_f16_f32 v66, v66, v67
	v_cvt_pk_f16_f32 v67, v122, v123
	v_cvt_f32_f16_e32 v122, v69
	v_cvt_f32_f16_sdwa v123, v69 dst_sel:DWORD dst_unused:UNUSED_PAD src0_sel:WORD_1
	v_rcp_f32_e32 v133, v68
	v_pk_fma_f32 v[68:69], v[82:83], v[118:119], v[36:37]
	s_waitcnt lgkmcnt(1)
	v_cvt_f32_f16_sdwa v125, v58 dst_sel:DWORD dst_unused:UNUSED_PAD src0_sel:WORD_1
	v_pk_fma_f32 v[68:69], v[26:27], v[110:111], v[68:69]
	v_pk_mul_f32 v[120:121], v[120:121], v[132:133]
	v_pk_fma_f32 v[68:69], v[84:85], v[86:87], v[68:69]
	v_pk_fma_f32 v[116:117], v[104:105], v[128:129], v[116:117]
	v_pk_fma_f32 v[118:119], v[28:29], v[122:123], v[68:69]
	v_pk_fma_f32 v[114:115], v[98:99], v[114:115], v[48:49]
	v_mul_f32_e32 v68, 0xbfb8aa3b, v118
	v_exp_f32_e32 v69, v68
	v_mul_f32_e32 v68, 0xbfb8aa3b, v119
	v_exp_f32_e32 v124, v68
	v_cvt_pk_f16_f32 v68, v120, v121
	v_add_f32_e32 v69, 1.0, v69
	v_rcp_f32_e32 v120, v69
	v_add_f32_e32 v69, 1.0, v124
	v_rcp_f32_e32 v121, v69
	v_cvt_f32_f16_e32 v124, v58
	v_pk_fma_f32 v[114:115], v[38:39], v[106:107], v[114:115]
	v_pk_fma_f32 v[112:113], v[94:95], v[112:113], v[34:35]
	v_pk_mul_f32 v[118:119], v[118:119], v[120:121]
	v_pk_fma_f32 v[116:117], v[44:45], v[124:125], v[116:117]
	v_cvt_f32_f16_e32 v120, v59
	v_cvt_f32_f16_sdwa v121, v59 dst_sel:DWORD dst_unused:UNUSED_PAD src0_sel:WORD_1
	v_mul_f32_e32 v58, 0xbfb8aa3b, v116
	v_mul_f32_e32 v69, 0xbfb8aa3b, v117
	v_exp_f32_e32 v58, v58
	v_exp_f32_e32 v69, v69
	v_pk_fma_f32 v[114:115], v[100:101], v[130:131], v[114:115]
	v_pk_fma_f32 v[112:113], v[30:31], v[88:89], v[112:113]
	v_pk_fma_f32 v[114:115], v[40:41], v[120:121], v[114:115]
	v_add_f32_e32 v58, 1.0, v58
	v_mul_f32_e32 v59, 0xbfb8aa3b, v114
	v_add_f32_e32 v69, 1.0, v69
	v_exp_f32_e32 v132, v59
	v_mul_f32_e32 v59, 0xbfb8aa3b, v115
	v_rcp_f32_e32 v58, v58
	v_exp_f32_e32 v133, v59
	v_rcp_f32_e32 v59, v69
	v_pk_fma_f32 v[112:113], v[96:97], v[126:127], v[112:113]
	v_add_f32_e32 v69, 1.0, v132
	v_rcp_f32_e32 v132, v69
	v_pk_mul_f32 v[58:59], v[116:117], v[58:59]
	v_cvt_f32_f16_e32 v116, v60
	v_cvt_f32_f16_sdwa v117, v60 dst_sel:DWORD dst_unused:UNUSED_PAD src0_sel:WORD_1
	v_add_f32_e32 v69, 1.0, v133
	v_cvt_pk_f16_f32 v58, v58, v59
	v_rcp_f32_e32 v133, v69
	v_pk_fma_f32 v[112:113], v[32:33], v[116:117], v[112:113]
	v_cvt_pk_f16_f32 v69, v118, v119
	v_mul_f32_e32 v59, 0xbfb8aa3b, v112
	v_exp_f32_e32 v60, v59
	v_mul_f32_e32 v59, 0xbfb8aa3b, v113
	v_exp_f32_e32 v118, v59
	v_pk_mul_f32 v[114:115], v[114:115], v[132:133]
	v_add_f32_e32 v60, 1.0, v60
	v_cvt_pk_f16_f32 v59, v114, v115
	v_rcp_f32_e32 v114, v60
	v_add_f32_e32 v60, 1.0, v118
	v_cvt_f32_f16_e32 v118, v61
	v_cvt_f32_f16_sdwa v119, v61 dst_sel:DWORD dst_unused:UNUSED_PAD src0_sel:WORD_1
	v_rcp_f32_e32 v115, v60
	v_pk_fma_f32 v[60:61], v[82:83], v[110:111], v[36:37]
	v_pk_fma_f32 v[46:47], v[102:103], v[108:109], v[46:47]
	v_pk_fma_f32 v[60:61], v[26:27], v[86:87], v[60:61]
	v_pk_fma_f32 v[42:43], v[42:43], v[128:129], v[46:47]
	v_pk_fma_f32 v[60:61], v[84:85], v[122:123], v[60:61]
	v_pk_fma_f32 v[42:43], v[104:105], v[124:125], v[42:43]
	v_pk_fma_f32 v[110:111], v[28:29], v[118:119], v[60:61]
	v_pk_fma_f32 v[34:35], v[94:95], v[88:89], v[34:35]
	v_mul_f32_e32 v60, 0xbfb8aa3b, v110
	v_exp_f32_e32 v132, v60
	v_mul_f32_e32 v60, 0xbfb8aa3b, v111
	v_exp_f32_e32 v133, v60
	v_pk_mul_f32 v[60:61], v[112:113], v[114:115]
	s_waitcnt lgkmcnt(0)
	v_cvt_f32_f16_e32 v114, v54
	v_cvt_f32_f16_sdwa v115, v54 dst_sel:DWORD dst_unused:UNUSED_PAD src0_sel:WORD_1
	v_add_f32_e32 v112, 1.0, v132
	v_add_f32_e32 v113, 1.0, v133
	v_rcp_f32_e32 v112, v112
	v_pk_fma_f32 v[42:43], v[44:45], v[114:115], v[42:43]
	v_rcp_f32_e32 v113, v113
	v_mul_f32_e32 v44, 0xbfb8aa3b, v42
	v_mul_f32_e32 v45, 0xbfb8aa3b, v43
	v_exp_f32_e32 v44, v44
	v_exp_f32_e32 v45, v45
	v_pk_mul_f32 v[46:47], v[110:111], v[112:113]
	v_cvt_pk_f16_f32 v60, v60, v61
	v_add_f32_e32 v44, 1.0, v44
	v_add_f32_e32 v45, 1.0, v45
	v_rcp_f32_e32 v44, v44
	v_rcp_f32_e32 v45, v45
	v_cvt_pk_f16_f32 v61, v46, v47
	v_pk_fma_f32 v[46:47], v[98:99], v[106:107], v[48:49]
	v_pk_fma_f32 v[30:31], v[30:31], v[126:127], v[34:35]
	v_pk_mul_f32 v[42:43], v[42:43], v[44:45]
	v_cvt_f32_f16_e32 v44, v55
	v_cvt_f32_f16_sdwa v45, v55 dst_sel:DWORD dst_unused:UNUSED_PAD src0_sel:WORD_1
	v_pk_fma_f32 v[38:39], v[38:39], v[130:131], v[46:47]
	v_pk_fma_f32 v[30:31], v[96:97], v[116:117], v[30:31]
	v_pk_fma_f32 v[38:39], v[100:101], v[120:121], v[38:39]
	v_pk_fma_f32 v[36:37], v[82:83], v[86:87], v[36:37]
	v_pk_fma_f32 v[40:41], v[40:41], v[44:45], v[38:39]
	v_cvt_f32_f16_sdwa v45, v56 dst_sel:DWORD dst_unused:UNUSED_PAD src0_sel:WORD_1
	v_mul_f32_e32 v38, 0xbfb8aa3b, v40
	v_exp_f32_e32 v39, v38
	v_mul_f32_e32 v38, 0xbfb8aa3b, v41
	v_exp_f32_e32 v44, v38
	v_cvt_pk_f16_f32 v38, v42, v43
	v_add_f32_e32 v39, 1.0, v39
	v_rcp_f32_e32 v42, v39
	v_add_f32_e32 v39, 1.0, v44
	v_cvt_f32_f16_e32 v44, v56
	v_rcp_f32_e32 v43, v39
	v_pk_fma_f32 v[26:27], v[26:27], v[122:123], v[36:37]
	v_pk_fma_f32 v[30:31], v[32:33], v[44:45], v[30:31]
	v_pk_fma_f32 v[26:27], v[84:85], v[118:119], v[26:27]
	v_mul_f32_e32 v32, 0xbfb8aa3b, v30
	v_exp_f32_e32 v34, v32
	v_mul_f32_e32 v32, 0xbfb8aa3b, v31
	v_exp_f32_e32 v35, v32
	v_pk_mul_f32 v[32:33], v[40:41], v[42:43]
	v_cvt_f32_f16_e32 v40, v57
	v_cvt_f32_f16_sdwa v41, v57 dst_sel:DWORD dst_unused:UNUSED_PAD src0_sel:WORD_1
	v_add_f32_e32 v34, 1.0, v34
	v_add_f32_e32 v35, 1.0, v35
	v_rcp_f32_e32 v34, v34
	v_pk_fma_f32 v[26:27], v[28:29], v[40:41], v[26:27]
	v_rcp_f32_e32 v35, v35
	v_mul_f32_e32 v28, 0xbfb8aa3b, v26
	v_mul_f32_e32 v29, 0xbfb8aa3b, v27
	v_exp_f32_e32 v28, v28
	v_exp_f32_e32 v29, v29
	v_pk_mul_f32 v[30:31], v[30:31], v[34:35]
	v_cvt_pk_f16_f32 v39, v32, v33
	v_add_f32_e32 v28, 1.0, v28
	v_add_f32_e32 v29, 1.0, v29
	v_rcp_f32_e32 v28, v28
	v_rcp_f32_e32 v29, v29
	v_cvt_pk_f16_f32 v40, v30, v31
	s_barrier
	v_pk_mul_f32 v[26:27], v[26:27], v[28:29]
	v_or_b32_e32 v34, v141, v140
	v_cvt_pk_f16_f32 v41, v26, v27
	ds_write_b128 v93, v[50:53] offset:8448
	ds_write_b128 v93, v[62:65] offset:8976
	ds_write_b128 v93, v[70:73] offset:9504
	ds_write_b128 v93, v[78:81] offset:10032
	ds_write_b128 v93, v[74:77] offset:10560
	ds_write_b128 v93, v[66:69] offset:11088
	ds_write_b128 v93, v[58:61] offset:11616
	ds_write_b128 v93, v[38:41] offset:12144
	v_mov_b32_e32 v93, v91
	v_lshl_add_u64 v[58:59], s[4:5], 0, v[92:93]
	v_add_co_u32_e32 v60, vcc, s17, v58
	s_waitcnt lgkmcnt(0)
	s_nop 0
	v_addc_co_u32_e32 v61, vcc, 0, v59, vcc
	s_barrier
	global_load_dwordx4 v[26:29], v92, s[4:5]
	global_load_dwordx4 v[30:33], v[60:61], off offset:-4096
	s_movk_i32 s6, 0x210
	v_add_u32_e32 v34, 16, v34
	v_mad_u32_u24 v66, v34, s6, v142
	ds_read_b128 v[34:37], v66
	s_movk_i32 s6, 0x5000
	v_add_co_u32_e32 v62, vcc, s6, v58
	s_waitcnt vmcnt(1) lgkmcnt(0)
	v_mfma_f32_16x16x32_f16 a[0:3], v[34:37], v[26:29], 0
	v_addc_co_u32_e32 v63, vcc, 0, v59, vcc
	global_load_dwordx4 v[38:41], v[62:63], off offset:-4096
	global_load_dwordx4 v[42:45], v92, s[4:5] offset:1024
	v_add_co_u32_e32 v54, vcc, s16, v58
	global_load_dwordx4 v[26:29], v[60:61], off
	s_nop 0
	v_addc_co_u32_e32 v55, vcc, 0, v59, vcc
	s_waitcnt vmcnt(3)
	v_mfma_f32_16x16x32_f16 a[4:7], v[34:37], v[30:33], 0
	global_load_dwordx4 v[30:33], v[54:55], off offset:1024
	ds_read_b128 v[46:49], v66 offset:64
	s_movk_i32 s6, 0x4000
	v_add_co_u32_e32 v64, vcc, s6, v58
	global_load_dwordx4 v[50:53], v[62:63], off
	s_nop 0
	v_addc_co_u32_e32 v65, vcc, 0, v59, vcc
	s_waitcnt vmcnt(4)
	v_mfma_f32_16x16x32_f16 a[8:11], v[34:37], v[38:41], 0
	global_load_dwordx4 v[34:37], v[64:65], off offset:1024
	global_load_dwordx4 v[38:41], v[54:55], off offset:2048
	v_add_co_u32_e32 v58, vcc, s3, v58
	s_waitcnt vmcnt(5) lgkmcnt(0)
	v_mfma_f32_16x16x32_f16 a[0:3], v[46:49], v[42:45], a[0:3]
	v_addc_co_u32_e32 v59, vcc, 0, v59, vcc
	s_load_dwordx2 s[16:17], s[0:1], 0x60
	s_waitcnt vmcnt(3)
	v_mfma_f32_16x16x32_f16 a[4:7], v[46:49], v[30:33], a[4:7]
	global_load_dwordx4 v[30:33], v92, s[4:5] offset:2048
	global_load_dwordx4 v[42:45], v[54:55], off offset:3072
	s_mov_b32 s3, 4
	s_waitcnt vmcnt(3)
	v_mfma_f32_16x16x32_f16 a[8:11], v[46:49], v[34:37], a[8:11]
	ds_read_b128 v[34:37], v66 offset:128
	ds_read_b128 v[46:49], v66 offset:192
	global_load_dwordx4 v[54:57], v92, s[4:5] offset:3072
	s_waitcnt vmcnt(2) lgkmcnt(0)
	v_mfma_f32_16x16x32_f16 a[0:3], v[34:37], v[30:33], a[0:3]
	global_load_dwordx4 v[30:33], v[64:65], off offset:2048
	v_mfma_f32_16x16x32_f16 a[4:7], v[34:37], v[38:41], a[4:7]
	global_load_dwordx4 v[38:41], v[64:65], off offset:3072
	s_waitcnt vmcnt(3)
	v_mfma_f32_16x16x32_f16 a[4:7], v[46:49], v[42:45], a[4:7]
	global_load_dwordx4 v[42:45], v[60:61], off offset:1024
	s_waitcnt vmcnt(2)
	v_mfma_f32_16x16x32_f16 a[8:11], v[34:37], v[30:33], a[8:11]
	global_load_dwordx4 v[30:33], v[58:59], off
	global_load_dwordx4 v[34:37], v[58:59], off offset:1024
	v_mfma_f32_16x16x32_f16 a[0:3], v[46:49], v[54:57], a[0:3]
	s_waitcnt vmcnt(3)
	v_mfma_f32_16x16x32_f16 a[8:11], v[46:49], v[38:41], a[8:11]
	ds_read_b128 v[38:41], v66 offset:256
	ds_read_b128 v[46:49], v66 offset:320
	s_waitcnt vmcnt(1) lgkmcnt(1)
	v_mfma_f32_16x16x32_f16 a[0:3], v[38:41], v[30:33], a[0:3]
	global_load_dwordx4 v[30:33], v[62:63], off offset:1024
	v_mfma_f32_16x16x32_f16 a[4:7], v[38:41], v[26:29], a[4:7]
	global_load_dwordx4 v[26:29], v[58:59], off offset:2048
	v_mfma_f32_16x16x32_f16 a[8:11], v[38:41], v[50:53], a[8:11]
	global_load_dwordx4 v[38:41], v[60:61], off offset:2048
	s_waitcnt vmcnt(3) lgkmcnt(0)
	v_mfma_f32_16x16x32_f16 a[0:3], v[46:49], v[34:37], a[0:3]
	global_load_dwordx4 v[34:37], v[62:63], off offset:2048
	v_mfma_f32_16x16x32_f16 a[4:7], v[46:49], v[42:45], a[4:7]
	global_load_dwordx4 v[42:45], v[58:59], off offset:3072
	s_waitcnt vmcnt(4)
	v_mfma_f32_16x16x32_f16 a[8:11], v[46:49], v[30:33], a[8:11]
	ds_read_b128 v[30:33], v66 offset:384
	ds_read_b128 v[46:49], v66 offset:448
	s_waitcnt vmcnt(3) lgkmcnt(1)
	v_mfma_f32_16x16x32_f16 a[0:3], v[30:33], v[26:29], a[0:3]
	global_load_dwordx4 v[26:29], v139, s[4:5]
	s_load_dwordx8 s[4:11], s[0:1], 0x40
	s_movk_i32 s0, 0xd0
	s_waitcnt vmcnt(3)
	v_mfma_f32_16x16x32_f16 a[4:7], v[30:33], v[38:41], a[4:7]
	v_mov_b32_e32 v40, v91
	v_mov_b32_e32 v41, v91
	v_mov_b32_e32 v38, v91
	s_waitcnt vmcnt(2)
	v_mfma_f32_16x16x32_f16 a[8:11], v[30:33], v[34:37], a[8:11]
	global_load_dwordx4 v[30:33], v[62:63], off offset:3072
	v_lshlrev_b32_e32 v34, 2, v140
	v_or_b32_e32 v35, 0xfa00, v34
	s_waitcnt vmcnt(2) lgkmcnt(0)
	v_mfma_f32_16x16x32_f16 a[0:3], v[46:49], v[42:45], a[0:3]
	v_mov_b32_e32 v42, v91
	v_mov_b32_e32 v43, v91
	v_mov_b32_e32 v39, v91
	s_waitcnt vmcnt(1)
	v_mfma_f32_16x16x32_f16 a[4:7], v[46:49], v[26:29], a[4:7]
	v_bitop3_b32 v26, v138, 12, 48 bitop3:0xe0
	v_mad_u32_u24 v26, v26, s0, v35
	v_or_b32_e32 v28, s14, v134
	s_waitcnt vmcnt(0)
	v_mfma_f32_16x16x32_f16 a[8:11], v[46:49], v[30:33], a[8:11]
	ds_write_b32 v26, a0
	ds_write_b32 v26, a1 offset:208
	ds_write_b32 v26, a2 offset:416
	ds_write_b32 v26, a3 offset:624
	ds_write_b32 v26, a4 offset:64
	ds_write_b32 v26, a5 offset:272
	ds_write_b32 v26, a6 offset:480
	ds_write_b32 v26, a7 offset:688
	ds_write_b32 v26, a8 offset:128
	ds_write_b32 v26, a9 offset:336
	ds_write_b32 v26, a10 offset:544
	ds_write_b32 v26, a11 offset:752
	v_mad_u32_u24 v26, v134, s0, v35
	s_waitcnt lgkmcnt(0)
	s_barrier
	ds_read2_b32 v[26:27], v26 offset0:8 offset1:24
	v_mov_b32_e32 v29, s15
	v_lshlrev_b64 v[30:31], 6, v[28:29]
	v_or_b32_e32 v30, v30, v34
	v_lshl_add_u64 v[32:33], s[6:7], 0, v[30:31]
	s_waitcnt lgkmcnt(0)
	global_store_dword v[32:33], v26, off sc1
	v_lshl_add_u64 v[30:31], s[8:9], 0, v[30:31]
	v_mad_u32_u24 v26, v135, s0, v35
	global_store_dword v[30:31], v27, off sc1
	ds_read2_b32 v[26:27], v26 offset0:8 offset1:24
	v_or_b32_e32 v28, s14, v135
	v_lshlrev_b64 v[30:31], 6, v[28:29]
	v_or_b32_e32 v30, v30, v34
	v_lshl_add_u64 v[32:33], s[6:7], 0, v[30:31]
	s_waitcnt lgkmcnt(0)
	global_store_dword v[32:33], v26, off sc1
	v_lshl_add_u64 v[30:31], s[8:9], 0, v[30:31]
	v_mad_u32_u24 v26, v136, s0, v35
	global_store_dword v[30:31], v27, off sc1
	ds_read2_b32 v[26:27], v26 offset0:8 offset1:24
	v_or_b32_e32 v28, s14, v136
	v_lshlrev_b64 v[30:31], 6, v[28:29]
	v_or_b32_e32 v30, v30, v34
	v_lshl_add_u64 v[32:33], s[6:7], 0, v[30:31]
	s_waitcnt lgkmcnt(0)
	global_store_dword v[32:33], v26, off sc1
	v_lshl_add_u64 v[30:31], s[8:9], 0, v[30:31]
	v_mad_u32_u24 v26, v137, s0, v35
	global_store_dword v[30:31], v27, off sc1
	ds_read2_b32 v[30:31], v26 offset0:8 offset1:24
	v_or_b32_e32 v28, s14, v137
	v_lshlrev_b64 v[32:33], 6, v[28:29]
	ds_read_b128 v[26:29], v91 offset:64000
	v_or_b32_e32 v32, v32, v34
	v_lshl_add_u64 v[34:35], s[6:7], 0, v[32:33]
	v_lshl_add_u64 v[32:33], s[8:9], 0, v[32:33]
	s_waitcnt lgkmcnt(1)
	global_store_dword v[34:35], v30, off sc1
	global_store_dword v[32:33], v31, off sc1
	ds_read_b128 v[30:33], v91 offset:64016
	v_lshlrev_b32_e32 v46, 1, v0
	ds_read_u16 v48, v46 offset:8448
	s_waitcnt lgkmcnt(2)
	v_fma_f32 v26, v22, v26, v1
	v_fmac_f32_e32 v26, v24, v28
	v_mul_f32_e32 v28, v25, v29
	v_fmac_f32_e32 v28, v23, v27
	s_waitcnt lgkmcnt(1)
	v_fmac_f32_e32 v26, v18, v30
	v_fmac_f32_e32 v28, v19, v31
	v_fmac_f32_e32 v26, v20, v32
	v_fmac_f32_e32 v28, v21, v33
	v_add_f32_e32 v28, v26, v28
	v_mul_f32_e64 v26, |v28|, s18
	v_exp_f32_e32 v26, v26
	s_lshl_b64 s[0:1], s[14:15], 10
	s_add_u32 s0, s4, s0
	s_addc_u32 s1, s5, s1
	v_add_f32_e32 v26, 1.0, v26
	v_log_f32_e32 v29, v26
	v_max_f32_e32 v49, 0, v28
	v_lshl_add_u64 v[26:27], s[0:1], 0, v[90:91]
	v_mul_u32_u24_e32 v164, 12, v0
	v_mov_b32_e32 v165, 0
	v_lshl_add_u64 v[26:27], v[26:27], 0, v[164:165]
	s_mov_b32 s4, 0x3f317218
	v_fmac_f32_e32 v49, 0x3f317218, v29
	v_add_u32_e32 v47, 0x2310, v46
	s_mov_b64 s[0:1], 0
	s_mov_b32 s5, 0xfa20
	v_mov_b32_e32 v28, v91
	v_mov_b32_e32 v29, v91
	v_mov_b32_e32 v36, v91
	v_mov_b32_e32 v37, v91
	v_mov_b32_e32 v34, v91
	v_mov_b32_e32 v35, v91
	v_mov_b32_e32 v32, v91
	v_mov_b32_e32 v33, v91
	v_mov_b32_e32 v30, v91
	v_mov_b32_e32 v31, v91
.LBB1_1:
	v_cvt_f16_f32_e32 v49, v49
	s_cmpk_lg_u32 s0, 0xf000
	v_mov_b32_e32 v90, s5
	s_cselect_b32 s6, s3, 63
	ds_read_u16 v149, v47
	ds_read_u16 v150, v47 offset:528
	ds_read_u16 v151, v47 offset:1056
	ds_read_b128 v[50:53], v90 offset:176
	ds_read_b128 v[54:57], v90 offset:192
	ds_read_b128 v[58:61], v90
	ds_read_b128 v[62:65], v90 offset:16
	ds_read_b128 v[66:69], v90 offset:32
	ds_read_b128 v[70:73], v90 offset:48
	ds_read_b128 v[74:77], v90 offset:384
	ds_read_b128 v[78:81], v90 offset:400
	ds_read_b128 v[82:85], v90 offset:208
	ds_read_b128 v[86:89], v90 offset:224
	ds_read_b128 v[92:95], v90 offset:240
	ds_read_b128 v[96:99], v90 offset:256
	ds_read_b128 v[100:103], v90 offset:592
	ds_read_b128 v[104:107], v90 offset:608
	ds_read_b128 v[108:111], v90 offset:416
	ds_read_b128 v[112:115], v90 offset:432
	ds_read_b128 v[116:119], v90 offset:448
	ds_read_b128 v[120:123], v90 offset:464
	s_mul_i32 s7, s6, 0xd0
	s_waitcnt lgkmcnt(14)
	v_lshlrev_b32_e32 v140, 16, v48
	v_cvt_f32_f16_e32 v148, v48
	s_mulk_i32 s6, 0x210
	v_mov_b32_e32 v48, s7
	v_fma_f32 v50, v22, v50, v1
	v_mul_f32_e32 v51, v23, v51
	ds_read_b128 v[124:127], v90 offset:624
	ds_read_b128 v[128:131], v90 offset:640
	ds_read_b128 v[132:135], v90 offset:656
	ds_read_b128 v[136:139], v90 offset:672
	v_add_u32_e32 v152, s6, v46
	v_or_b32_e32 v164, v140, v49
	ds_read_b128 v[140:143], v48 offset:64000
	ds_read_b128 v[144:147], v48 offset:64016
	ds_read_u16 v48, v152 offset:8448
	s_waitcnt lgkmcnt(14)
	v_fma_f32 v74, v22, v74, v1
	v_mul_f32_e32 v75, v23, v75
	s_waitcnt lgkmcnt(12)
	v_fma_f32 v100, v22, v100, v1
	v_mul_f32_e32 v101, v23, v101
	v_pk_fma_f32 v[50:51], v[24:25], v[52:53], v[50:51]
	v_cvt_f32_f16_e32 v90, v49
	v_pk_fma_f32 v[52:53], v[24:25], v[76:77], v[74:75]
	v_pk_fma_f32 v[74:75], v[24:25], v[102:103], v[100:101]
	v_pk_fma_f32 v[50:51], v[18:19], v[54:55], v[50:51]
	v_pk_fma_f32 v[52:53], v[18:19], v[78:79], v[52:53]
	s_waitcnt lgkmcnt(11)
	v_pk_fma_f32 v[74:75], v[18:19], v[104:105], v[74:75]
	v_pk_fma_f32 v[50:51], v[20:21], v[56:57], v[50:51]
	v_pk_fma_f32 v[52:53], v[20:21], v[80:81], v[52:53]
	v_pk_fma_f32 v[74:75], v[20:21], v[106:107], v[74:75]
	s_waitcnt lgkmcnt(2)
	v_fma_f32 v80, v22, v140, v1
	v_mul_f32_e32 v81, v23, v141
	v_add_f32_e32 v49, v50, v51
	v_lshl_add_u64 v[44:45], v[26:27], 0, s[0:1]
	v_add_f32_e32 v52, v52, v53
	v_add_f32_e32 v53, v74, v75
	v_pk_fma_f32 v[50:51], v[24:25], v[142:143], v[80:81]
	v_mul_f32_e64 v74, |v49|, s18
	v_lshlrev_b32_e32 v158, 16, v149
	v_cvt_f32_f16_e32 v159, v149
	v_lshlrev_b32_e32 v160, 16, v150
	v_cvt_f32_f16_e32 v161, v150
	v_lshlrev_b32_e32 v162, 16, v151
	v_cvt_f32_f16_e32 v163, v151
	v_mul_f32_e32 v54, v90, v148
	v_pk_mul_f32 v[76:77], v[90:91], v[14:15] op_sel_hi:[0,1]
	v_pk_mul_f32 v[100:101], v[90:91], v[16:17] op_sel_hi:[0,1]
	v_pk_mul_f32 v[102:103], v[90:91], v[10:11] op_sel_hi:[0,1]
	v_pk_mul_f32 v[148:149], v[90:91], v[12:13] op_sel_hi:[0,1]
	v_pk_mul_f32 v[150:151], v[90:91], v[6:7] op_sel_hi:[0,1]
	v_pk_mul_f32 v[152:153], v[90:91], v[8:9] op_sel_hi:[0,1]
	v_pk_mul_f32 v[154:155], v[90:91], v[2:3] op_sel_hi:[0,1]
	v_pk_mul_f32 v[156:157], v[90:91], v[4:5] op_sel_hi:[0,1]
	v_mul_f32_e64 v80, |v53|, s18
	s_waitcnt lgkmcnt(1)
	v_pk_fma_f32 v[50:51], v[18:19], v[144:145], v[50:51]
	v_exp_f32_e32 v74, v74
	v_add_f32_e32 v55, v91, v90
	v_exp_f32_e32 v56, v76
	v_exp_f32_e32 v57, v77
	v_exp_f32_e32 v76, v100
	v_exp_f32_e32 v77, v101
	v_exp_f32_e32 v78, v102
	v_exp_f32_e32 v79, v103
	v_exp_f32_e32 v90, v148
	v_exp_f32_e32 v91, v149
	v_exp_f32_e32 v100, v150
	v_exp_f32_e32 v101, v151
	v_exp_f32_e32 v102, v152
	v_exp_f32_e32 v103, v153
	v_exp_f32_e32 v104, v154
	v_exp_f32_e32 v105, v155
	v_exp_f32_e32 v148, v156
	v_exp_f32_e32 v149, v157
	v_max_f32_e32 v75, 0, v49
	v_mul_f32_e64 v49, |v52|, s18
	v_exp_f32_e32 v80, v80
	v_pk_fma_f32 v[50:51], v[20:21], v[146:147], v[50:51]
	v_exp_f32_e32 v81, v49
	v_add_f32_e32 v49, v50, v51
	v_mul_f32_e64 v50, |v49|, s18
	v_exp_f32_e32 v50, v50
	v_add_f32_e32 v51, 1.0, v74
	v_pk_mul_f32 v[42:43], v[42:43], v[56:57]
	v_pk_mul_f32 v[40:41], v[40:41], v[76:77]
	v_pk_mul_f32 v[38:39], v[38:39], v[78:79]
	v_pk_mul_f32 v[36:37], v[36:37], v[90:91]
	v_pk_mul_f32 v[34:35], v[34:35], v[100:101]
	v_pk_mul_f32 v[32:33], v[32:33], v[102:103]
	v_pk_mul_f32 v[30:31], v[30:31], v[104:105]
	v_pk_mul_f32 v[28:29], v[28:29], v[148:149]
	v_add_f32_e32 v56, 1.0, v80
	v_log_f32_e32 v51, v51
	v_pk_fma_f32 v[42:43], v[54:55], v[58:59], v[42:43] op_sel_hi:[0,1,1]
	v_pk_fma_f32 v[40:41], v[54:55], v[60:61], v[40:41] op_sel_hi:[0,1,1]
	v_pk_fma_f32 v[38:39], v[54:55], v[62:63], v[38:39] op_sel_hi:[0,1,1]
	v_pk_fma_f32 v[36:37], v[54:55], v[64:65], v[36:37] op_sel_hi:[0,1,1]
	v_pk_fma_f32 v[34:35], v[54:55], v[66:67], v[34:35] op_sel_hi:[0,1,1]
	v_pk_fma_f32 v[32:33], v[54:55], v[68:69], v[32:33] op_sel_hi:[0,1,1]
	v_pk_fma_f32 v[30:31], v[54:55], v[70:71], v[30:31] op_sel_hi:[0,1,1]
	v_pk_fma_f32 v[28:29], v[54:55], v[72:73], v[28:29] op_sel_hi:[0,1,1]
	v_add_f32_e32 v54, 1.0, v81
	v_log_f32_e32 v56, v56
	v_log_f32_e32 v54, v54
	v_add_f32_e32 v50, 1.0, v50
	v_max_f32_e32 v53, 0, v53
	v_log_f32_e32 v57, v50
	v_fma_mixlo_f16 v50, v51, s4, v75
	v_max_f32_e32 v52, 0, v52
	v_fma_mixlo_f16 v53, v56, s4, v53
	v_or_b32_sdwa v165, v158, v50 dst_sel:DWORD dst_unused:UNUSED_PAD src0_sel:DWORD src1_sel:WORD_0
	v_cvt_f32_f16_e32 v50, v50
	v_fma_mixlo_f16 v51, v54, s4, v52
	v_cvt_f32_f16_e32 v52, v51
	v_max_f32_e32 v49, 0, v49
	v_or_b32_sdwa v166, v160, v51 dst_sel:DWORD dst_unused:UNUSED_PAD src0_sel:DWORD src1_sel:WORD_0
	v_or_b32_sdwa v167, v162, v53 dst_sel:DWORD dst_unused:UNUSED_PAD src0_sel:DWORD src1_sel:WORD_0
	v_cvt_f32_f16_e32 v54, v53
	global_store_dwordx4 v[44:45], v[164:167], off sc1
	v_fmac_f32_e32 v49, 0x3f317218, v57
	v_pk_mul_f32 v[56:57], v[50:51], v[14:15] op_sel_hi:[0,1]
	v_pk_mul_f32 v[58:59], v[50:51], v[16:17] op_sel_hi:[0,1]
	v_pk_mul_f32 v[60:61], v[50:51], v[10:11] op_sel_hi:[0,1]
	v_pk_mul_f32 v[62:63], v[50:51], v[12:13] op_sel_hi:[0,1]
	v_pk_mul_f32 v[64:65], v[50:51], v[6:7] op_sel_hi:[0,1]
	v_pk_mul_f32 v[66:67], v[50:51], v[8:9] op_sel_hi:[0,1]
	v_pk_mul_f32 v[68:69], v[50:51], v[2:3] op_sel_hi:[0,1]
	v_pk_mul_f32 v[70:71], v[50:51], v[4:5] op_sel_hi:[0,1]
	v_exp_f32_e32 v56, v56
	v_exp_f32_e32 v57, v57
	v_exp_f32_e32 v58, v58
	v_exp_f32_e32 v59, v59
	v_exp_f32_e32 v60, v60
	v_exp_f32_e32 v61, v61
	v_exp_f32_e32 v62, v62
	v_exp_f32_e32 v63, v63
	v_exp_f32_e32 v64, v64
	v_exp_f32_e32 v65, v65
	v_exp_f32_e32 v66, v66
	v_exp_f32_e32 v67, v67
	v_exp_f32_e32 v68, v68
	v_exp_f32_e32 v69, v69
	v_exp_f32_e32 v70, v70
	v_exp_f32_e32 v71, v71
	v_pk_mul_f32 v[72:73], v[52:53], v[14:15] op_sel_hi:[0,1]
	v_pk_mul_f32 v[74:75], v[52:53], v[16:17] op_sel_hi:[0,1]
	v_pk_mul_f32 v[76:77], v[52:53], v[10:11] op_sel_hi:[0,1]
	v_pk_mul_f32 v[78:79], v[52:53], v[12:13] op_sel_hi:[0,1]
	v_pk_mul_f32 v[80:81], v[52:53], v[6:7] op_sel_hi:[0,1]
	v_pk_mul_f32 v[90:91], v[52:53], v[8:9] op_sel_hi:[0,1]
	v_pk_mul_f32 v[100:101], v[52:53], v[2:3] op_sel_hi:[0,1]
	v_pk_mul_f32 v[102:103], v[52:53], v[4:5] op_sel_hi:[0,1]
	v_exp_f32_e32 v72, v72
	v_exp_f32_e32 v73, v73
	v_exp_f32_e32 v74, v74
	v_exp_f32_e32 v75, v75
	v_exp_f32_e32 v76, v76
	v_exp_f32_e32 v77, v77
	v_exp_f32_e32 v78, v78
	v_exp_f32_e32 v79, v79
	v_exp_f32_e32 v80, v80
	v_exp_f32_e32 v81, v81
	v_exp_f32_e32 v154, v90
	v_exp_f32_e32 v155, v91
	v_exp_f32_e32 v100, v100
	v_exp_f32_e32 v101, v101
	v_exp_f32_e32 v102, v102
	v_exp_f32_e32 v103, v103
	v_add_f32_e32 v45, v55, v50
	v_pk_mul_f32 v[106:107], v[54:55], v[14:15] op_sel_hi:[0,1]
	v_pk_mul_f32 v[140:141], v[54:55], v[16:17] op_sel_hi:[0,1]
	v_pk_mul_f32 v[142:143], v[54:55], v[10:11] op_sel_hi:[0,1]
	v_pk_mul_f32 v[144:145], v[54:55], v[12:13] op_sel_hi:[0,1]
	v_pk_mul_f32 v[146:147], v[54:55], v[6:7] op_sel_hi:[0,1]
	v_pk_mul_f32 v[148:149], v[54:55], v[8:9] op_sel_hi:[0,1]
	v_pk_mul_f32 v[150:151], v[54:55], v[2:3] op_sel_hi:[0,1]
	v_pk_mul_f32 v[152:153], v[54:55], v[4:5] op_sel_hi:[0,1]
	v_mul_f32_e32 v44, v50, v159
	v_mul_f32_e32 v50, v52, v161
	v_add_f32_e32 v45, v45, v52
	v_exp_f32_e32 v52, v106
	v_exp_f32_e32 v53, v107
	v_exp_f32_e32 v106, v140
	v_exp_f32_e32 v107, v141
	v_exp_f32_e32 v140, v142
	v_exp_f32_e32 v141, v143
	v_exp_f32_e32 v142, v144
	v_exp_f32_e32 v143, v145
	v_exp_f32_e32 v144, v146
	v_exp_f32_e32 v145, v147
	v_exp_f32_e32 v146, v148
	v_exp_f32_e32 v147, v149
	v_exp_f32_e32 v148, v150
	v_exp_f32_e32 v149, v151
	v_exp_f32_e32 v150, v152
	v_exp_f32_e32 v151, v153
	v_pk_mul_f32 v[42:43], v[42:43], v[56:57]
	v_pk_mul_f32 v[40:41], v[40:41], v[58:59]
	v_pk_mul_f32 v[38:39], v[38:39], v[60:61]
	v_pk_mul_f32 v[36:37], v[36:37], v[62:63]
	v_pk_mul_f32 v[34:35], v[34:35], v[64:65]
	v_pk_mul_f32 v[32:33], v[32:33], v[66:67]
	v_pk_mul_f32 v[30:31], v[30:31], v[68:69]
	v_pk_mul_f32 v[28:29], v[28:29], v[70:71]
	v_pk_fma_f32 v[42:43], v[44:45], v[82:83], v[42:43] op_sel_hi:[0,1,1]
	v_pk_fma_f32 v[40:41], v[44:45], v[84:85], v[40:41] op_sel_hi:[0,1,1]
	v_pk_fma_f32 v[38:39], v[44:45], v[86:87], v[38:39] op_sel_hi:[0,1,1]
	v_pk_fma_f32 v[36:37], v[44:45], v[88:89], v[36:37] op_sel_hi:[0,1,1]
	v_pk_fma_f32 v[34:35], v[44:45], v[92:93], v[34:35] op_sel_hi:[0,1,1]
	v_pk_fma_f32 v[32:33], v[44:45], v[94:95], v[32:33] op_sel_hi:[0,1,1]
	v_pk_fma_f32 v[30:31], v[44:45], v[96:97], v[30:31] op_sel_hi:[0,1,1]
	v_pk_fma_f32 v[28:29], v[44:45], v[98:99], v[28:29] op_sel_hi:[0,1,1]
	v_pk_mul_f32 v[42:43], v[42:43], v[72:73]
	v_pk_mul_f32 v[40:41], v[40:41], v[74:75]
	v_pk_mul_f32 v[38:39], v[38:39], v[76:77]
	v_pk_mul_f32 v[36:37], v[36:37], v[78:79]
	v_pk_mul_f32 v[34:35], v[34:35], v[80:81]
	v_pk_mul_f32 v[32:33], v[32:33], v[154:155]
	v_pk_mul_f32 v[30:31], v[30:31], v[100:101]
	v_pk_mul_f32 v[28:29], v[28:29], v[102:103]
	s_add_u32 s0, s0, 0x1000
	v_pk_fma_f32 v[42:43], v[50:51], v[108:109], v[42:43] op_sel_hi:[0,1,1]
	v_pk_fma_f32 v[40:41], v[50:51], v[110:111], v[40:41] op_sel_hi:[0,1,1]
	v_pk_fma_f32 v[38:39], v[50:51], v[112:113], v[38:39] op_sel_hi:[0,1,1]
	v_pk_fma_f32 v[36:37], v[50:51], v[114:115], v[36:37] op_sel_hi:[0,1,1]
	v_pk_fma_f32 v[34:35], v[50:51], v[116:117], v[34:35] op_sel_hi:[0,1,1]
	v_pk_fma_f32 v[32:33], v[50:51], v[118:119], v[32:33] op_sel_hi:[0,1,1]
	v_pk_fma_f32 v[30:31], v[50:51], v[120:121], v[30:31] op_sel_hi:[0,1,1]
	v_pk_fma_f32 v[28:29], v[50:51], v[122:123], v[28:29] op_sel_hi:[0,1,1]
	s_addc_u32 s1, s1, 0
	s_add_i32 s3, s3, 4
	s_addk_i32 s5, 0x340
	v_mul_f32_e32 v104, v54, v163
	v_pk_mul_f32 v[42:43], v[42:43], v[52:53]
	v_pk_mul_f32 v[40:41], v[40:41], v[106:107]
	v_pk_mul_f32 v[38:39], v[38:39], v[140:141]
	v_pk_mul_f32 v[36:37], v[36:37], v[142:143]
	v_pk_mul_f32 v[34:35], v[34:35], v[144:145]
	v_pk_mul_f32 v[32:33], v[32:33], v[146:147]
	v_pk_mul_f32 v[30:31], v[30:31], v[148:149]
	v_pk_mul_f32 v[28:29], v[28:29], v[150:151]
	v_add_u32_e32 v47, 0x840, v47
	s_cmp_eq_u32 s0, 0x10000
	v_add_f32_e32 v91, v45, v54
	v_pk_fma_f32 v[42:43], v[104:105], v[124:125], v[42:43] op_sel_hi:[0,1,1]
	v_pk_fma_f32 v[40:41], v[104:105], v[126:127], v[40:41] op_sel_hi:[0,1,1]
	v_pk_fma_f32 v[38:39], v[104:105], v[128:129], v[38:39] op_sel_hi:[0,1,1]
	v_pk_fma_f32 v[36:37], v[104:105], v[130:131], v[36:37] op_sel_hi:[0,1,1]
	v_pk_fma_f32 v[34:35], v[104:105], v[132:133], v[34:35] op_sel_hi:[0,1,1]
	v_pk_fma_f32 v[32:33], v[104:105], v[134:135], v[32:33] op_sel_hi:[0,1,1]
	v_pk_fma_f32 v[30:31], v[104:105], v[136:137], v[30:31] op_sel_hi:[0,1,1]
	v_pk_fma_f32 v[28:29], v[104:105], v[138:139], v[28:29] op_sel_hi:[0,1,1]
	s_cbranch_scc0 .LBB1_1
	s_ashr_i32 s3, s2, 31
	s_lshl_b64 s[0:1], s[12:13], 10
	s_lshl_b64 s[4:5], s[2:3], 4
	s_add_u32 s0, s0, s4
	s_addc_u32 s1, s1, s5
	s_lshl_b64 s[0:1], s[0:1], 10
	s_add_u32 s0, s10, s0
	s_addc_u32 s1, s11, s1
	v_lshlrev_b32_e32 v0, 2, v0
	v_mov_b32_e32 v1, 0
	v_lshl_add_u64 v[2:3], s[0:1], 0, v[0:1]
	global_store_dword v0, v42, s[0:1] sc1
	global_store_dword v0, v43, s[0:1] offset:1024 sc1
	global_store_dword v0, v40, s[0:1] offset:2048 sc1
	global_store_dword v0, v41, s[0:1] offset:3072 sc1
	s_movk_i32 s0, 0x1000
	v_add_co_u32_e32 v4, vcc, s0, v2
	s_movk_i32 s0, 0x2000
	s_nop 0
	v_addc_co_u32_e32 v5, vcc, 0, v3, vcc
	v_add_co_u32_e32 v6, vcc, s0, v2
	s_movk_i32 s0, 0x3000
	s_nop 0
	v_addc_co_u32_e32 v7, vcc, 0, v3, vcc
	v_add_co_u32_e32 v2, vcc, s0, v2
	s_lshl_b64 s[0:1], s[12:13], 16
	s_add_u32 s4, s16, s0
	s_addc_u32 s5, s17, s1
	s_lshl_b64 s[0:1], s[2:3], 10
	s_add_u32 s0, s4, s0
	v_addc_co_u32_e32 v3, vcc, 0, v3, vcc
	s_addc_u32 s1, s5, s1
	global_store_dword v[6:7], v38, off offset:-4096 sc1
	global_store_dword v[4:5], v39, off offset:1024 sc1
	global_store_dword v[4:5], v36, off offset:2048 sc1
	global_store_dword v[4:5], v37, off offset:3072 sc1
	global_store_dword v[6:7], v34, off sc1
	global_store_dword v[6:7], v35, off offset:1024 sc1
	global_store_dword v[6:7], v32, off offset:2048 sc1
	global_store_dword v[6:7], v33, off offset:3072 sc1
	global_store_dword v[2:3], v30, off sc1
	global_store_dword v[2:3], v31, off offset:1024 sc1
	global_store_dword v[2:3], v28, off offset:2048 sc1
	global_store_dword v[2:3], v29, off offset:3072 sc1
	global_store_dword v0, v91, s[0:1] sc1
	s_endpgm

_Z7k_scan2PKfPfS0_:
	s_load_dwordx4 s[4:7], s[0:1], 0x0
	s_load_dwordx2 s[10:11], s[0:1], 0x10
	s_lshl_b32 s1, s2, 6
	s_and_b32 s1, s1, 0xc0
	s_lshr_b32 s0, s2, 2
	v_or_b32_e32 v4, s1, v0
	s_mov_b32 s8, s3
	v_lshl_add_u32 v2, v4, 4, s0
	s_mov_b32 s1, 0
	v_mov_b32_e32 v3, 0
	s_ashr_i32 s9, s3, 31
	s_waitcnt lgkmcnt(0)
	v_lshl_add_u64 v[0:1], v[2:3], 2, s[4:5]
	s_lshl_b64 s[2:3], s[8:9], 6
	s_lshl_b64 s[4:5], s[0:1], 10
	s_add_u32 s4, s6, s4
	s_addc_u32 s5, s7, s5
	v_lshlrev_b32_e32 v2, 2, v4
	v_lshl_add_u64 v[4:5], s[4:5], 0, v[2:3]
	s_lshl_b64 s[4:5], s[8:9], 20
	global_load_dword v63, v[0:1], off
	v_lshl_add_u64 v[0:1], s[10:11], 0, v[2:3]
	v_lshl_add_u64 v[6:7], v[4:5], 0, s[4:5]
	s_lshl_b64 s[4:5], s[8:9], 16
	global_load_dword v74, v[6:7], off
	v_lshl_add_u64 v[6:7], v[0:1], 0, s[4:5]
	s_or_b32 s4, s2, 1
	s_mov_b32 s5, s3
	s_lshl_b64 s[10:11], s[4:5], 14
	global_load_dword v116, v[6:7], off
	v_lshl_add_u64 v[6:7], v[4:5], 0, s[10:11]
	s_lshl_b64 s[4:5], s[4:5], 10
	global_load_dword v72, v[6:7], off
	v_lshl_add_u64 v[6:7], v[0:1], 0, s[4:5]
	s_or_b32 s4, s2, 2
	s_mov_b32 s5, s3
	s_lshl_b64 s[10:11], s[4:5], 14
	global_load_dword v78, v[6:7], off
	v_lshl_add_u64 v[6:7], v[4:5], 0, s[10:11]
	s_lshl_b64 s[4:5], s[4:5], 10
	global_load_dword v71, v[6:7], off
	v_lshl_add_u64 v[6:7], v[0:1], 0, s[4:5]
	s_or_b32 s4, s2, 3
	s_mov_b32 s5, s3
	s_lshl_b64 s[10:11], s[4:5], 14
	global_load_dword v77, v[6:7], off
	v_lshl_add_u64 v[6:7], v[4:5], 0, s[10:11]
	s_lshl_b64 s[4:5], s[4:5], 10
	global_load_dword v65, v[6:7], off
	v_lshl_add_u64 v[6:7], v[0:1], 0, s[4:5]
	s_or_b32 s4, s2, 4
	s_mov_b32 s5, s3
	s_lshl_b64 s[10:11], s[4:5], 14
	global_load_dword v75, v[6:7], off
	v_lshl_add_u64 v[6:7], v[4:5], 0, s[10:11]
	s_lshl_b64 s[4:5], s[4:5], 10
	global_load_dword v66, v[6:7], off
	v_lshl_add_u64 v[6:7], v[0:1], 0, s[4:5]
	s_or_b32 s4, s2, 5
	s_mov_b32 s5, s3
	s_lshl_b64 s[10:11], s[4:5], 14
	global_load_dword v67, v[6:7], off
	v_lshl_add_u64 v[6:7], v[4:5], 0, s[10:11]
	s_lshl_b64 s[4:5], s[4:5], 10
	global_load_dword v64, v[6:7], off
	v_lshl_add_u64 v[6:7], v[0:1], 0, s[4:5]
	s_or_b32 s4, s2, 6
	s_mov_b32 s5, s3
	s_lshl_b64 s[10:11], s[4:5], 14
	global_load_dword v68, v[6:7], off
	v_lshl_add_u64 v[6:7], v[4:5], 0, s[10:11]
	s_lshl_b64 s[4:5], s[4:5], 10
	global_load_dword v61, v[6:7], off
	v_lshl_add_u64 v[6:7], v[0:1], 0, s[4:5]
	s_or_b32 s4, s2, 7
	s_mov_b32 s5, s3
	s_lshl_b64 s[10:11], s[4:5], 14
	global_load_dword v69, v[6:7], off
	v_lshl_add_u64 v[6:7], v[4:5], 0, s[10:11]
	s_lshl_b64 s[4:5], s[4:5], 10
	global_load_dword v58, v[6:7], off
	v_lshl_add_u64 v[6:7], v[0:1], 0, s[4:5]
	s_or_b32 s4, s2, 8
	s_mov_b32 s5, s3
	s_lshl_b64 s[10:11], s[4:5], 14
	global_load_dword v70, v[6:7], off
	v_lshl_add_u64 v[6:7], v[4:5], 0, s[10:11]
	s_lshl_b64 s[4:5], s[4:5], 10
	global_load_dword v54, v[6:7], off
	v_lshl_add_u64 v[6:7], v[0:1], 0, s[4:5]
	s_or_b32 s4, s2, 9
	s_mov_b32 s5, s3
	s_lshl_b64 s[10:11], s[4:5], 14
	global_load_dword v73, v[6:7], off
	v_lshl_add_u64 v[6:7], v[4:5], 0, s[10:11]
	s_lshl_b64 s[4:5], s[4:5], 10
	global_load_dword v62, v[6:7], off
	v_lshl_add_u64 v[6:7], v[0:1], 0, s[4:5]
	s_or_b32 s4, s2, 10
	s_mov_b32 s5, s3
	s_lshl_b64 s[10:11], s[4:5], 14
	global_load_dword v76, v[6:7], off
	v_lshl_add_u64 v[6:7], v[4:5], 0, s[10:11]
	s_lshl_b64 s[4:5], s[4:5], 10
	global_load_dword v59, v[6:7], off
	v_lshl_add_u64 v[6:7], v[0:1], 0, s[4:5]
	s_or_b32 s4, s2, 11
	s_mov_b32 s5, s3
	s_lshl_b64 s[10:11], s[4:5], 14
	global_load_dword v79, v[6:7], off
	v_lshl_add_u64 v[6:7], v[4:5], 0, s[10:11]
	s_lshl_b64 s[4:5], s[4:5], 10
	global_load_dword v56, v[6:7], off
	v_lshl_add_u64 v[6:7], v[0:1], 0, s[4:5]
	s_or_b32 s4, s2, 12
	s_mov_b32 s5, s3
	s_lshl_b64 s[10:11], s[4:5], 14
	global_load_dword v80, v[6:7], off
	v_lshl_add_u64 v[6:7], v[4:5], 0, s[10:11]
	s_lshl_b64 s[4:5], s[4:5], 10
	global_load_dword v53, v[6:7], off
	v_lshl_add_u64 v[6:7], v[0:1], 0, s[4:5]
	s_or_b32 s4, s2, 13
	s_mov_b32 s5, s3
	s_lshl_b64 s[10:11], s[4:5], 14
	global_load_dword v81, v[6:7], off
	v_lshl_add_u64 v[6:7], v[4:5], 0, s[10:11]
	s_lshl_b64 s[4:5], s[4:5], 10
	global_load_dword v60, v[6:7], off
	v_lshl_add_u64 v[6:7], v[0:1], 0, s[4:5]
	s_or_b32 s4, s2, 14
	s_mov_b32 s5, s3
	s_lshl_b64 s[10:11], s[4:5], 14
	global_load_dword v82, v[6:7], off
	v_lshl_add_u64 v[6:7], v[4:5], 0, s[10:11]
	s_lshl_b64 s[4:5], s[4:5], 10
	global_load_dword v57, v[6:7], off
	v_lshl_add_u64 v[6:7], v[0:1], 0, s[4:5]
	s_or_b32 s4, s2, 15
	s_mov_b32 s5, s3
	s_lshl_b64 s[10:11], s[4:5], 14
	global_load_dword v83, v[6:7], off
	v_lshl_add_u64 v[6:7], v[4:5], 0, s[10:11]
	s_lshl_b64 s[4:5], s[4:5], 10
	global_load_dword v55, v[6:7], off
	v_lshl_add_u64 v[6:7], v[0:1], 0, s[4:5]
	s_or_b32 s4, s2, 16
	s_mov_b32 s5, s3
	s_lshl_b64 s[10:11], s[4:5], 14
	global_load_dword v84, v[6:7], off
	v_lshl_add_u64 v[6:7], v[4:5], 0, s[10:11]
	s_lshl_b64 s[4:5], s[4:5], 10
	global_load_dword v52, v[6:7], off
	v_lshl_add_u64 v[6:7], v[0:1], 0, s[4:5]
	s_or_b32 s4, s2, 17
	s_mov_b32 s5, s3
	s_lshl_b64 s[10:11], s[4:5], 14
	global_load_dword v85, v[6:7], off
	v_lshl_add_u64 v[6:7], v[4:5], 0, s[10:11]
	s_lshl_b64 s[4:5], s[4:5], 10
	global_load_dword v30, v[6:7], off
	v_lshl_add_u64 v[6:7], v[0:1], 0, s[4:5]
	s_or_b32 s4, s2, 18
	s_mov_b32 s5, s3
	s_lshl_b64 s[10:11], s[4:5], 14
	global_load_dword v86, v[6:7], off
	v_lshl_add_u64 v[6:7], v[4:5], 0, s[10:11]
	s_lshl_b64 s[4:5], s[4:5], 10
	global_load_dword v29, v[6:7], off
	v_lshl_add_u64 v[6:7], v[0:1], 0, s[4:5]
	s_or_b32 s4, s2, 19
	s_mov_b32 s5, s3
	s_lshl_b64 s[10:11], s[4:5], 14
	global_load_dword v87, v[6:7], off
	v_lshl_add_u64 v[6:7], v[4:5], 0, s[10:11]
	s_lshl_b64 s[4:5], s[4:5], 10
	global_load_dword v28, v[6:7], off
	v_lshl_add_u64 v[6:7], v[0:1], 0, s[4:5]
	s_or_b32 s4, s2, 20
	s_mov_b32 s5, s3
	s_lshl_b64 s[10:11], s[4:5], 14
	global_load_dword v88, v[6:7], off
	v_lshl_add_u64 v[6:7], v[4:5], 0, s[10:11]
	s_lshl_b64 s[4:5], s[4:5], 10
	global_load_dword v27, v[6:7], off
	v_lshl_add_u64 v[6:7], v[0:1], 0, s[4:5]
	s_or_b32 s4, s2, 21
	s_mov_b32 s5, s3
	s_lshl_b64 s[10:11], s[4:5], 14
	global_load_dword v89, v[6:7], off
	v_lshl_add_u64 v[6:7], v[4:5], 0, s[10:11]
	s_lshl_b64 s[4:5], s[4:5], 10
	global_load_dword v25, v[6:7], off
	v_lshl_add_u64 v[6:7], v[0:1], 0, s[4:5]
	s_or_b32 s4, s2, 22
	s_mov_b32 s5, s3
	s_lshl_b64 s[10:11], s[4:5], 14
	global_load_dword v90, v[6:7], off
	v_lshl_add_u64 v[6:7], v[4:5], 0, s[10:11]
	s_lshl_b64 s[4:5], s[4:5], 10
	global_load_dword v24, v[6:7], off
	v_lshl_add_u64 v[6:7], v[0:1], 0, s[4:5]
	s_or_b32 s4, s2, 23
	s_mov_b32 s5, s3
	s_lshl_b64 s[10:11], s[4:5], 14
	global_load_dword v91, v[6:7], off
	v_lshl_add_u64 v[6:7], v[4:5], 0, s[10:11]
	s_lshl_b64 s[4:5], s[4:5], 10
	global_load_dword v22, v[6:7], off
	v_lshl_add_u64 v[6:7], v[0:1], 0, s[4:5]
	s_or_b32 s4, s2, 24
	s_mov_b32 s5, s3
	s_lshl_b64 s[10:11], s[4:5], 14
	global_load_dword v92, v[6:7], off
	v_lshl_add_u64 v[6:7], v[4:5], 0, s[10:11]
	s_lshl_b64 s[4:5], s[4:5], 10
	global_load_dword v20, v[6:7], off
	v_lshl_add_u64 v[6:7], v[0:1], 0, s[4:5]
	s_or_b32 s4, s2, 25
	s_mov_b32 s5, s3
	s_lshl_b64 s[10:11], s[4:5], 14
	global_load_dword v93, v[6:7], off
	v_lshl_add_u64 v[6:7], v[4:5], 0, s[10:11]
	s_lshl_b64 s[4:5], s[4:5], 10
	global_load_dword v18, v[6:7], off
	v_lshl_add_u64 v[6:7], v[0:1], 0, s[4:5]
	s_or_b32 s4, s2, 26
	s_mov_b32 s5, s3
	s_lshl_b64 s[10:11], s[4:5], 14
	global_load_dword v94, v[6:7], off
	v_lshl_add_u64 v[6:7], v[4:5], 0, s[10:11]
	s_lshl_b64 s[4:5], s[4:5], 10
	global_load_dword v16, v[6:7], off
	v_lshl_add_u64 v[6:7], v[0:1], 0, s[4:5]
	s_or_b32 s4, s2, 27
	s_mov_b32 s5, s3
	s_lshl_b64 s[10:11], s[4:5], 14
	global_load_dword v95, v[6:7], off
	v_lshl_add_u64 v[6:7], v[4:5], 0, s[10:11]
	s_lshl_b64 s[4:5], s[4:5], 10
	global_load_dword v13, v[6:7], off
	v_lshl_add_u64 v[6:7], v[0:1], 0, s[4:5]
	s_or_b32 s4, s2, 28
	s_mov_b32 s5, s3
	s_lshl_b64 s[10:11], s[4:5], 14
	global_load_dword v96, v[6:7], off
	v_lshl_add_u64 v[6:7], v[4:5], 0, s[10:11]
	s_lshl_b64 s[4:5], s[4:5], 10
	global_load_dword v14, v[6:7], off
	v_lshl_add_u64 v[6:7], v[0:1], 0, s[4:5]
	s_or_b32 s4, s2, 29
	s_mov_b32 s5, s3
	s_lshl_b64 s[10:11], s[4:5], 14
	global_load_dword v97, v[6:7], off
	v_lshl_add_u64 v[6:7], v[4:5], 0, s[10:11]
	s_lshl_b64 s[4:5], s[4:5], 10
	global_load_dword v15, v[6:7], off
	v_lshl_add_u64 v[6:7], v[0:1], 0, s[4:5]
	s_or_b32 s4, s2, 30
	s_mov_b32 s5, s3
	s_lshl_b64 s[10:11], s[4:5], 14
	global_load_dword v98, v[6:7], off
	v_lshl_add_u64 v[6:7], v[4:5], 0, s[10:11]
	s_lshl_b64 s[4:5], s[4:5], 10
	global_load_dword v17, v[6:7], off
	v_lshl_add_u64 v[6:7], v[0:1], 0, s[4:5]
	s_or_b32 s4, s2, 31
	s_mov_b32 s5, s3
	s_lshl_b64 s[10:11], s[4:5], 14
	global_load_dword v99, v[6:7], off
	v_lshl_add_u64 v[6:7], v[4:5], 0, s[10:11]
	s_lshl_b64 s[4:5], s[4:5], 10
	global_load_dword v19, v[6:7], off
	v_lshl_add_u64 v[6:7], v[0:1], 0, s[4:5]
	s_or_b32 s4, s2, 32
	s_mov_b32 s5, s3
	s_lshl_b64 s[10:11], s[4:5], 14
	global_load_dword v100, v[6:7], off
	v_lshl_add_u64 v[6:7], v[4:5], 0, s[10:11]
	s_lshl_b64 s[4:5], s[4:5], 10
	global_load_dword v21, v[6:7], off
	v_lshl_add_u64 v[6:7], v[0:1], 0, s[4:5]
	s_or_b32 s4, s2, 33
	s_mov_b32 s5, s3
	s_lshl_b64 s[10:11], s[4:5], 14
	global_load_dword v101, v[6:7], off
	v_lshl_add_u64 v[6:7], v[4:5], 0, s[10:11]
	s_lshl_b64 s[4:5], s[4:5], 10
	global_load_dword v23, v[6:7], off
	v_lshl_add_u64 v[6:7], v[0:1], 0, s[4:5]
	s_or_b32 s4, s2, 34
	s_mov_b32 s5, s3
	s_lshl_b64 s[10:11], s[4:5], 14
	s_lshl_b64 s[4:5], s[4:5], 10
	v_lshl_add_u64 v[8:9], v[0:1], 0, s[4:5]
	s_or_b32 s4, s2, 35
	s_mov_b32 s5, s3
	global_load_dword v102, v[6:7], off
	global_load_dword v103, v[8:9], off
	v_lshl_add_u64 v[6:7], v[4:5], 0, s[10:11]
	s_lshl_b64 s[10:11], s[4:5], 14
	v_lshl_add_u64 v[8:9], v[4:5], 0, s[10:11]
	s_lshl_b64 s[4:5], s[4:5], 10
	global_load_dword v6, v[6:7], off
	s_lshl_b64 s[8:9], s[8:9], 10
	global_load_dword v7, v[8:9], off
	v_lshl_add_u64 v[8:9], v[0:1], 0, s[4:5]
	s_or_b32 s4, s2, 36
	s_mov_b32 s5, s3
	s_lshl_b64 s[10:11], s[4:5], 14
	s_lshl_b64 s[4:5], s[4:5], 10
	v_lshl_add_u64 v[10:11], v[0:1], 0, s[4:5]
	s_or_b32 s4, s2, 37
	s_mov_b32 s5, s3
	global_load_dword v104, v[8:9], off
	global_load_dword v105, v[10:11], off
	v_lshl_add_u64 v[8:9], v[4:5], 0, s[10:11]
	s_lshl_b64 s[10:11], s[4:5], 14
	v_lshl_add_u64 v[10:11], v[4:5], 0, s[10:11]
	s_lshl_b64 s[4:5], s[4:5], 10
	global_load_dword v8, v[8:9], off
	s_waitcnt vmcnt(62)
	v_mul_f32_e32 v78, v63, v78
	global_load_dword v9, v[10:11], off
	v_lshl_add_u64 v[10:11], v[0:1], 0, s[4:5]
	s_or_b32 s4, s2, 38
	s_mov_b32 s5, s3
	s_lshl_b64 s[10:11], s[4:5], 14
	s_lshl_b64 s[4:5], s[4:5], 10
	v_lshl_add_u64 v[32:33], v[0:1], 0, s[4:5]
	s_or_b32 s4, s2, 39
	s_mov_b32 s5, s3
	global_load_dword v106, v[10:11], off
	global_load_dword v107, v[32:33], off
	v_lshl_add_u64 v[10:11], v[4:5], 0, s[10:11]
	s_lshl_b64 s[10:11], s[4:5], 14
	v_lshl_add_u64 v[32:33], v[4:5], 0, s[10:11]
	s_lshl_b64 s[4:5], s[4:5], 10
	global_load_dword v10, v[10:11], off
	v_exp_f32_e32 v78, v78
	global_load_dword v11, v[32:33], off
	v_lshl_add_u64 v[32:33], v[0:1], 0, s[4:5]
	s_or_b32 s4, s2, 40
	s_mov_b32 s5, s3
	s_lshl_b64 s[10:11], s[4:5], 14
	global_load_dword v108, v[32:33], off
	v_lshl_add_u64 v[32:33], v[4:5], 0, s[10:11]
	s_lshl_b64 s[4:5], s[4:5], 10
	global_load_dword v12, v[32:33], off
	v_lshl_add_u64 v[32:33], v[0:1], 0, s[4:5]
	s_or_b32 s4, s2, 41
	s_mov_b32 s5, s3
	s_lshl_b64 s[10:11], s[4:5], 14
	global_load_dword v109, v[32:33], off
	v_lshl_add_u64 v[32:33], v[4:5], 0, s[10:11]
	s_lshl_b64 s[4:5], s[4:5], 10
	global_load_dword v26, v[32:33], off
	v_lshl_add_u64 v[32:33], v[0:1], 0, s[4:5]
	s_or_b32 s4, s2, 42
	s_mov_b32 s5, s3
	s_lshl_b64 s[10:11], s[4:5], 14
	global_load_dword v110, v[32:33], off
	v_lshl_add_u64 v[32:33], v[4:5], 0, s[10:11]
	s_lshl_b64 s[4:5], s[4:5], 10
	global_load_dword v31, v[32:33], off
	v_lshl_add_u64 v[32:33], v[0:1], 0, s[4:5]
	s_or_b32 s4, s2, 43
	s_mov_b32 s5, s3
	s_lshl_b64 s[10:11], s[4:5], 14
	global_load_dword v111, v[32:33], off
	v_lshl_add_u64 v[32:33], v[4:5], 0, s[10:11]
	s_lshl_b64 s[4:5], s[4:5], 10
	global_load_dword v36, v[32:33], off
	v_lshl_add_u64 v[32:33], v[0:1], 0, s[4:5]
	s_or_b32 s4, s2, 44
	s_mov_b32 s5, s3
	s_lshl_b64 s[10:11], s[4:5], 14
	global_load_dword v112, v[32:33], off
	v_lshl_add_u64 v[32:33], v[4:5], 0, s[10:11]
	s_lshl_b64 s[4:5], s[4:5], 10
	global_load_dword v37, v[32:33], off
	v_lshl_add_u64 v[32:33], v[0:1], 0, s[4:5]
	s_or_b32 s4, s2, 45
	s_mov_b32 s5, s3
	s_lshl_b64 s[10:11], s[4:5], 14
	global_load_dword v113, v[32:33], off
	v_lshl_add_u64 v[32:33], v[4:5], 0, s[10:11]
	s_lshl_b64 s[4:5], s[4:5], 10
	global_load_dword v38, v[32:33], off
	v_lshl_add_u64 v[32:33], v[0:1], 0, s[4:5]
	s_or_b32 s4, s2, 46
	s_mov_b32 s5, s3
	s_lshl_b64 s[10:11], s[4:5], 14
	global_load_dword v114, v[32:33], off
	v_lshl_add_u64 v[32:33], v[4:5], 0, s[10:11]
	s_lshl_b64 s[4:5], s[4:5], 10
	global_load_dword v39, v[32:33], off
	v_lshl_add_u64 v[32:33], v[0:1], 0, s[4:5]
	s_or_b32 s4, s2, 47
	s_mov_b32 s5, s3
	s_lshl_b64 s[10:11], s[4:5], 14
	s_lshl_b64 s[34:35], s[4:5], 10
	s_or_b32 s4, s2, 48
	global_load_dword v115, v[32:33], off
	v_lshl_add_u64 v[32:33], v[4:5], 0, s[10:11]
	s_lshl_b64 s[10:11], s[4:5], 14
	s_lshl_b64 s[28:29], s[4:5], 10
	s_or_b32 s4, s2, 49
	global_load_dword v40, v[32:33], off
	v_lshl_add_u64 v[32:33], v[4:5], 0, s[10:11]
	s_lshl_b64 s[10:11], s[4:5], 14
	s_lshl_b64 s[30:31], s[4:5], 10
	s_or_b32 s4, s2, 50
	global_load_dword v41, v[32:33], off
	v_lshl_add_u64 v[32:33], v[4:5], 0, s[10:11]
	s_lshl_b64 s[10:11], s[4:5], 14
	s_lshl_b64 s[18:19], s[4:5], 10
	s_or_b32 s4, s2, 51
	global_load_dword v42, v[32:33], off
	v_lshl_add_u64 v[32:33], v[4:5], 0, s[10:11]
	s_lshl_b64 s[10:11], s[4:5], 14
	s_lshl_b64 s[26:27], s[4:5], 10
	s_or_b32 s4, s2, 52
	global_load_dword v43, v[32:33], off
	v_lshl_add_u64 v[32:33], v[4:5], 0, s[10:11]
	s_lshl_b64 s[10:11], s[4:5], 14
	s_lshl_b64 s[14:15], s[4:5], 10
	s_or_b32 s4, s2, 53
	global_load_dword v44, v[32:33], off
	v_lshl_add_u64 v[32:33], v[4:5], 0, s[10:11]
	s_lshl_b64 s[10:11], s[4:5], 14
	s_lshl_b64 s[16:17], s[4:5], 10
	s_or_b32 s4, s2, 54
	global_load_dword v45, v[32:33], off
	v_lshl_add_u64 v[32:33], v[4:5], 0, s[10:11]
	s_lshl_b64 s[10:11], s[4:5], 14
	global_load_dword v46, v[32:33], off
	v_lshl_add_u64 v[32:33], v[4:5], 0, s[10:11]
	s_or_b32 s10, s2, 55
	s_mov_b32 s11, s3
	s_lshl_b64 s[12:13], s[10:11], 14
	s_lshl_b64 s[20:21], s[10:11], 10
	s_or_b32 s10, s2, 56
	global_load_dword v47, v[32:33], off
	v_lshl_add_u64 v[32:33], v[4:5], 0, s[12:13]
	s_lshl_b64 s[12:13], s[10:11], 14
	global_load_dword v48, v[32:33], off
	v_lshl_add_u64 v[32:33], v[4:5], 0, s[12:13]
	s_or_b32 s12, s2, 57
	s_mov_b32 s13, s3
	s_lshl_b64 s[22:23], s[12:13], 14
	global_load_dword v49, v[32:33], off
	v_lshl_add_u64 v[32:33], v[4:5], 0, s[22:23]
	s_lshl_b64 s[22:23], s[12:13], 10
	s_or_b32 s12, s2, 58
	s_lshl_b64 s[24:25], s[12:13], 14
	global_load_dword v50, v[32:33], off
	v_lshl_add_u64 v[32:33], v[4:5], 0, s[24:25]
	s_or_b32 s24, s2, 59
	s_mov_b32 s25, s3
	s_lshl_b64 s[36:37], s[24:25], 14
	global_load_dword v51, v[32:33], off
	v_lshl_add_u64 v[32:33], v[4:5], 0, s[36:37]
	s_or_b32 s36, s2, 60
	s_mov_b32 s37, s3
	s_lshl_b64 s[38:39], s[36:37], 14
	global_load_dword v35, v[32:33], off
	v_lshl_add_u64 v[32:33], v[4:5], 0, s[38:39]
	s_or_b32 s38, s2, 61
	s_mov_b32 s39, s3
	s_lshl_b64 s[40:41], s[38:39], 14
	s_or_b32 s2, s2, 62
	s_lshl_b64 s[4:5], s[4:5], 10
	s_lshl_b64 s[10:11], s[10:11], 10
	s_lshl_b64 s[12:13], s[12:13], 10
	s_lshl_b64 s[24:25], s[24:25], 10
	global_load_dword v34, v[32:33], off
	s_lshl_b64 s[36:37], s[36:37], 10
	v_lshl_add_u64 v[32:33], v[4:5], 0, s[40:41]
	s_lshl_b64 s[38:39], s[38:39], 10
	s_lshl_b64 s[40:41], s[2:3], 14
	s_lshl_b64 s[2:3], s[2:3], 10
	v_lshl_add_u64 v[4:5], v[4:5], 0, s[40:41]
	s_add_u32 s0, s8, s0
	global_load_dword v32, v[32:33], off
	s_addc_u32 s1, s9, 0
	global_load_dword v33, v[4:5], off
	v_mul_f32_e32 v4, v63, v116
	v_exp_f32_e32 v116, v4
	v_lshl_add_u64 v[4:5], s[6:7], 0, v[2:3]
	s_lshl_b64 s[0:1], s[0:1], 10
	v_lshl_add_u64 v[4:5], v[4:5], 0, s[0:1]
	global_store_dword v[4:5], v3, off sc1
	v_lshl_add_u64 v[2:3], v[0:1], 0, s[34:35]
	s_movk_i32 s0, 0x4000
	global_load_dword v117, v[2:3], off
	v_add_co_u32_e32 v2, vcc, s0, v4
	v_fmac_f32_e32 v74, 0, v116
	s_nop 0
	v_addc_co_u32_e32 v3, vcc, 0, v5, vcc
	global_store_dword v[2:3], v74, off sc1
	v_lshl_add_u64 v[2:3], v[0:1], 0, s[28:29]
	global_load_dword v116, v[2:3], off
	v_lshl_add_u64 v[2:3], v[0:1], 0, s[30:31]
	v_fmac_f32_e32 v72, v74, v78
	s_mov_b32 s0, 0x8000
	v_mul_f32_e32 v74, v63, v77
	global_load_dword v118, v[2:3], off
	v_add_co_u32_e32 v2, vcc, s0, v4
	v_exp_f32_e32 v74, v74
	s_nop 0
	v_addc_co_u32_e32 v3, vcc, 0, v5, vcc
	global_store_dword v[2:3], v72, off sc1
	v_lshl_add_u64 v[2:3], v[0:1], 0, s[18:19]
	global_load_dword v77, v[2:3], off
	v_lshl_add_u64 v[2:3], v[0:1], 0, s[26:27]
	s_mov_b32 s0, 0xc000
	global_load_dword v78, v[2:3], off
	v_fmac_f32_e32 v71, v72, v74
	v_add_co_u32_e32 v2, vcc, s0, v4
	v_mul_f32_e32 v72, v63, v75
	s_nop 0
	v_addc_co_u32_e32 v3, vcc, 0, v5, vcc
	v_exp_f32_e32 v72, v72
	global_store_dword v[2:3], v71, off sc1
	v_lshl_add_u64 v[2:3], v[0:1], 0, s[14:15]
	global_load_dword v74, v[2:3], off
	v_lshl_add_u64 v[2:3], v[0:1], 0, s[16:17]
	global_load_dword v75, v[2:3], off
	v_lshl_add_u64 v[2:3], v[0:1], 0, s[4:5]
	v_fmac_f32_e32 v65, v71, v72
	global_load_dword v71, v[2:3], off
	v_lshl_add_u64 v[2:3], v[0:1], 0, s[20:21]
	global_load_dword v72, v[2:3], off
	v_lshl_add_u64 v[2:3], v[0:1], 0, s[10:11]
	global_load_dword v119, v[2:3], off
	v_lshl_add_u64 v[2:3], v[0:1], 0, s[22:23]
	global_load_dword v120, v[2:3], off
	v_lshl_add_u64 v[2:3], v[0:1], 0, s[12:13]
	global_load_dword v121, v[2:3], off
	v_lshl_add_u64 v[2:3], v[0:1], 0, s[24:25]
	global_load_dword v122, v[2:3], off
	v_lshl_add_u64 v[2:3], v[0:1], 0, s[36:37]
	global_load_dword v123, v[2:3], off
	v_lshl_add_u64 v[2:3], v[0:1], 0, s[38:39]
	v_lshl_add_u64 v[0:1], v[0:1], 0, s[2:3]
	global_load_dword v2, v[2:3], off
	s_mov_b32 s0, 0x10000
	global_load_dword v3, v[0:1], off
	v_mul_f32_e32 v0, v63, v67
	v_exp_f32_e32 v67, v0
	v_add_co_u32_e32 v0, vcc, s0, v4
	s_mov_b32 s0, 0x14000
	s_nop 0
	v_addc_co_u32_e32 v1, vcc, 0, v5, vcc
	global_store_dword v[0:1], v65, off sc1
	v_mul_f32_e32 v0, v63, v68
	v_fmac_f32_e32 v66, v65, v67
	v_exp_f32_e32 v65, v0
	v_add_co_u32_e32 v0, vcc, s0, v4
	s_mov_b32 s0, 0x18000
	s_nop 0
	v_addc_co_u32_e32 v1, vcc, 0, v5, vcc
	global_store_dword v[0:1], v66, off sc1
	v_add_co_u32_e32 v0, vcc, s0, v4
	v_fmac_f32_e32 v64, v66, v65
	s_nop 0
	v_addc_co_u32_e32 v1, vcc, 0, v5, vcc
	global_store_dword v[0:1], v64, off sc1
	s_waitcnt vmcnt(62)
	v_mul_f32_e32 v0, v63, v69
	v_exp_f32_e32 v126, v0
	v_mul_f32_e32 v1, v63, v70
	v_mul_f32_e32 v68, v63, v80
	v_mul_f32_e32 v80, v63, v86
	v_mul_f32_e32 v86, v63, v92
	v_mul_f32_e32 v92, v63, v98
	v_exp_f32_e32 v127, v1
	s_mov_b32 s0, 0x1c000
	v_mul_f32_e32 v65, v63, v73
	v_mul_f32_e32 v69, v63, v81
	v_mul_f32_e32 v81, v63, v87
	v_mul_f32_e32 v87, v63, v93
	v_mul_f32_e32 v93, v63, v99
	v_exp_f32_e32 v148, v92
	v_add_co_u32_e32 v92, vcc, s0, v4
	v_exp_f32_e32 v128, v65
	v_exp_f32_e32 v149, v93
	v_fmac_f32_e32 v61, v64, v126
	v_addc_co_u32_e32 v93, vcc, 0, v5, vcc
	s_mov_b32 s0, 0x20000
	v_mul_f32_e32 v66, v63, v76
	global_store_dword v[92:93], v61, off sc1
	v_add_co_u32_e32 v92, vcc, s0, v4
	v_exp_f32_e32 v129, v66
	v_fmac_f32_e32 v58, v61, v127
	v_addc_co_u32_e32 v93, vcc, 0, v5, vcc
	s_mov_b32 s0, 0x24000
	global_store_dword v[92:93], v58, off sc1
	v_add_co_u32_e32 v92, vcc, s0, v4
	v_mul_f32_e32 v67, v63, v79
	v_fmac_f32_e32 v54, v58, v128
	v_addc_co_u32_e32 v93, vcc, 0, v5, vcc
	s_mov_b32 s0, 0x28000
	v_exp_f32_e32 v130, v67
	global_store_dword v[92:93], v54, off sc1
	v_add_co_u32_e32 v92, vcc, s0, v4
	v_exp_f32_e32 v131, v68
	v_fmac_f32_e32 v62, v54, v129
	v_addc_co_u32_e32 v93, vcc, 0, v5, vcc
	s_mov_b32 s0, 0x2c000
	global_store_dword v[92:93], v62, off sc1
	v_add_co_u32_e32 v92, vcc, s0, v4
	v_exp_f32_e32 v132, v69
	s_nop 0
	v_addc_co_u32_e32 v93, vcc, 0, v5, vcc
	s_mov_b32 s0, 0x30000
	v_mul_f32_e32 v70, v63, v82
	v_fmac_f32_e32 v59, v62, v130
	v_add_co_u32_e32 v58, vcc, s0, v4
	v_exp_f32_e32 v133, v70
	global_store_dword v[92:93], v59, off sc1
	v_fmac_f32_e32 v56, v59, v131
	v_addc_co_u32_e32 v59, vcc, 0, v5, vcc
	s_mov_b32 s0, 0x34000
	global_store_dword v[58:59], v56, off sc1
	v_add_co_u32_e32 v58, vcc, s0, v4
	v_mul_f32_e32 v73, v63, v83
	v_fmac_f32_e32 v53, v56, v132
	v_addc_co_u32_e32 v59, vcc, 0, v5, vcc
	s_mov_b32 s0, 0x38000
	v_mul_f32_e32 v76, v63, v84
	v_exp_f32_e32 v134, v73
	global_store_dword v[58:59], v53, off sc1
	v_add_co_u32_e32 v58, vcc, s0, v4
	v_exp_f32_e32 v135, v76
	v_fmac_f32_e32 v60, v53, v133
	v_addc_co_u32_e32 v59, vcc, 0, v5, vcc
	s_mov_b32 s0, 0x3c000
	v_mul_f32_e32 v79, v63, v85
	global_store_dword v[58:59], v60, off sc1
	v_add_co_u32_e32 v58, vcc, s0, v4
	v_exp_f32_e32 v136, v79
	s_nop 0
	v_addc_co_u32_e32 v59, vcc, 0, v5, vcc
	s_mov_b32 s0, 0x40000
	v_exp_f32_e32 v137, v80
	v_fmac_f32_e32 v57, v60, v134
	v_add_co_u32_e32 v56, vcc, s0, v4
	global_store_dword v[58:59], v57, off sc1
	v_fmac_f32_e32 v55, v57, v135
	v_addc_co_u32_e32 v57, vcc, 0, v5, vcc
	s_mov_b32 s0, 0x44000
	v_add_co_u32_e32 v54, vcc, s0, v4
	v_exp_f32_e32 v138, v81
	global_store_dword v[56:57], v55, off sc1
	v_fmac_f32_e32 v52, v55, v136
	v_addc_co_u32_e32 v55, vcc, 0, v5, vcc
	s_mov_b32 s0, 0x48000
	v_mul_f32_e32 v82, v63, v88
	global_store_dword v[54:55], v52, off sc1
	v_fmac_f32_e32 v30, v52, v137
	v_add_co_u32_e32 v52, vcc, s0, v4
	v_mul_f32_e32 v83, v63, v89
	v_exp_f32_e32 v139, v82
	v_addc_co_u32_e32 v53, vcc, 0, v5, vcc
	s_mov_b32 s0, 0x4c000
	v_exp_f32_e32 v140, v83
	global_store_dword v[52:53], v30, off sc1
	v_add_co_u32_e32 v52, vcc, s0, v4
	v_fmac_f32_e32 v29, v30, v138
	s_nop 0
	v_addc_co_u32_e32 v53, vcc, 0, v5, vcc
	s_mov_b32 s0, 0x50000
	v_mul_f32_e32 v84, v63, v90
	global_store_dword v[52:53], v29, off sc1
	v_add_co_u32_e32 v52, vcc, s0, v4
	v_exp_f32_e32 v141, v84
	v_fmac_f32_e32 v28, v29, v139
	v_addc_co_u32_e32 v53, vcc, 0, v5, vcc
	s_mov_b32 s0, 0x54000
	v_mul_f32_e32 v85, v63, v91
	global_store_dword v[52:53], v28, off sc1
	v_fmac_f32_e32 v27, v28, v140
	v_add_co_u32_e32 v28, vcc, s0, v4
	v_exp_f32_e32 v142, v85
	s_nop 0
	v_addc_co_u32_e32 v29, vcc, 0, v5, vcc
	s_mov_b32 s0, 0x58000
	v_exp_f32_e32 v143, v86
	global_store_dword v[28:29], v27, off sc1
	v_add_co_u32_e32 v28, vcc, s0, v4
	v_fmac_f32_e32 v25, v27, v141
	s_nop 0
	v_addc_co_u32_e32 v29, vcc, 0, v5, vcc
	s_mov_b32 s0, 0x5c000
	global_store_dword v[28:29], v25, off sc1
	v_add_co_u32_e32 v28, vcc, s0, v4
	v_exp_f32_e32 v144, v87
	v_fmac_f32_e32 v24, v25, v142
	v_addc_co_u32_e32 v29, vcc, 0, v5, vcc
	s_mov_b32 s0, 0x60000
	v_mul_f32_e32 v88, v63, v94
	global_store_dword v[28:29], v24, off sc1
	v_fmac_f32_e32 v22, v24, v143
	v_add_co_u32_e32 v24, vcc, s0, v4
	v_exp_f32_e32 v145, v88
	s_nop 0
	v_addc_co_u32_e32 v25, vcc, 0, v5, vcc
	s_mov_b32 s0, 0x64000
	v_mul_f32_e32 v89, v63, v95
	global_store_dword v[24:25], v22, off sc1
	v_add_co_u32_e32 v24, vcc, s0, v4
	v_exp_f32_e32 v146, v89
	v_fmac_f32_e32 v20, v22, v144
	v_addc_co_u32_e32 v25, vcc, 0, v5, vcc
	s_mov_b32 s0, 0x68000
	v_mul_f32_e32 v90, v63, v96
	global_store_dword v[24:25], v20, off sc1
	v_add_co_u32_e32 v24, vcc, s0, v4
	v_exp_f32_e32 v147, v90
	v_fmac_f32_e32 v18, v20, v145
	v_addc_co_u32_e32 v25, vcc, 0, v5, vcc
	s_mov_b32 s0, 0x6c000
	v_mul_f32_e32 v91, v63, v97
	global_store_dword v[24:25], v18, off sc1
	v_add_co_u32_e32 v24, vcc, s0, v4
	v_exp_f32_e32 v91, v91
	v_fmac_f32_e32 v16, v18, v146
	v_addc_co_u32_e32 v25, vcc, 0, v5, vcc
	s_mov_b32 s0, 0x70000
	global_store_dword v[24:25], v16, off sc1
	v_add_co_u32_e32 v24, vcc, s0, v4
	v_fmac_f32_e32 v13, v16, v147
	s_nop 0
	v_addc_co_u32_e32 v25, vcc, 0, v5, vcc
	s_mov_b32 s0, 0x74000
	global_store_dword v[24:25], v13, off sc1
	v_add_co_u32_e32 v24, vcc, s0, v4
	v_fmac_f32_e32 v14, v13, v91
	s_nop 0
	v_addc_co_u32_e32 v25, vcc, 0, v5, vcc
	s_mov_b32 s0, 0x78000
	v_mul_f32_e32 v94, v63, v100
	global_store_dword v[24:25], v14, off sc1
	v_add_co_u32_e32 v24, vcc, s0, v4
	v_exp_f32_e32 v94, v94
	s_nop 0
	v_addc_co_u32_e32 v25, vcc, 0, v5, vcc
	s_mov_b32 s0, 0x7c000
	v_mul_f32_e32 v95, v63, v101
	v_fmac_f32_e32 v15, v14, v148
	v_add_co_u32_e32 v14, vcc, s0, v4
	v_exp_f32_e32 v90, v95
	global_store_dword v[24:25], v15, off sc1
	v_fmac_f32_e32 v17, v15, v149
	v_addc_co_u32_e32 v15, vcc, 0, v5, vcc
	s_mov_b32 s0, 0x80000
	v_mul_f32_e32 v96, v63, v102
	global_store_dword v[14:15], v17, off sc1
	v_add_co_u32_e32 v14, vcc, s0, v4
	v_exp_f32_e32 v89, v96
	v_fmac_f32_e32 v19, v17, v94
	v_addc_co_u32_e32 v15, vcc, 0, v5, vcc
	s_mov_b32 s0, 0x84000
	v_mul_f32_e32 v97, v63, v103
	global_store_dword v[14:15], v19, off sc1
	v_add_co_u32_e32 v14, vcc, s0, v4
	v_exp_f32_e32 v88, v97
	v_fmac_f32_e32 v21, v19, v90
	v_addc_co_u32_e32 v15, vcc, 0, v5, vcc
	s_mov_b32 s0, 0x88000
	global_store_dword v[14:15], v21, off sc1
	v_add_co_u32_e32 v14, vcc, s0, v4
	s_waitcnt vmcnt(62)
	v_mul_f32_e32 v98, v63, v104
	v_fmac_f32_e32 v23, v21, v89
	v_addc_co_u32_e32 v15, vcc, 0, v5, vcc
	s_mov_b32 s0, 0x8c000
	v_mul_f32_e32 v99, v63, v105
	v_exp_f32_e32 v87, v98
	global_store_dword v[14:15], v23, off sc1
	v_add_co_u32_e32 v14, vcc, s0, v4
	v_exp_f32_e32 v86, v99
	v_fmac_f32_e32 v6, v23, v88
	v_addc_co_u32_e32 v15, vcc, 0, v5, vcc
	s_mov_b32 s0, 0x90000
	v_mul_f32_e32 v100, v63, v106
	global_store_dword v[14:15], v6, off sc1
	v_add_co_u32_e32 v14, vcc, s0, v4
	v_exp_f32_e32 v85, v100
	s_nop 0
	v_addc_co_u32_e32 v15, vcc, 0, v5, vcc
	s_mov_b32 s0, 0x94000
	v_mul_f32_e32 v101, v63, v107
	v_fmac_f32_e32 v7, v6, v87
	v_add_co_u32_e32 v6, vcc, s0, v4
	v_exp_f32_e32 v84, v101
	global_store_dword v[14:15], v7, off sc1
	v_fmac_f32_e32 v8, v7, v86
	v_addc_co_u32_e32 v7, vcc, 0, v5, vcc
	s_mov_b32 s0, 0x98000
	v_mul_f32_e32 v102, v63, v108
	global_store_dword v[6:7], v8, off sc1
	v_add_co_u32_e32 v6, vcc, s0, v4
	v_exp_f32_e32 v83, v102
	v_fmac_f32_e32 v9, v8, v85
	v_addc_co_u32_e32 v7, vcc, 0, v5, vcc
	s_mov_b32 s0, 0x9c000
	v_mul_f32_e32 v103, v63, v109
	global_store_dword v[6:7], v9, off sc1
	v_add_co_u32_e32 v6, vcc, s0, v4
	v_exp_f32_e32 v82, v103
	v_fmac_f32_e32 v10, v9, v84
	v_addc_co_u32_e32 v7, vcc, 0, v5, vcc
	s_mov_b32 s0, 0xa0000
	v_mul_f32_e32 v104, v63, v110
	global_store_dword v[6:7], v10, off sc1
	v_add_co_u32_e32 v6, vcc, s0, v4
	v_exp_f32_e32 v81, v104
	v_fmac_f32_e32 v11, v10, v83
	v_addc_co_u32_e32 v7, vcc, 0, v5, vcc
	s_mov_b32 s0, 0xa4000
	v_mul_f32_e32 v105, v63, v111
	global_store_dword v[6:7], v11, off sc1
	v_add_co_u32_e32 v6, vcc, s0, v4
	v_exp_f32_e32 v80, v105
	v_fmac_f32_e32 v12, v11, v82
	v_addc_co_u32_e32 v7, vcc, 0, v5, vcc
	s_mov_b32 s0, 0xa8000
	v_mul_f32_e32 v106, v63, v112
	global_store_dword v[6:7], v12, off sc1
	v_add_co_u32_e32 v6, vcc, s0, v4
	v_exp_f32_e32 v79, v106
	v_fmac_f32_e32 v26, v12, v81
	v_addc_co_u32_e32 v7, vcc, 0, v5, vcc
	s_mov_b32 s0, 0xac000
	v_mul_f32_e32 v107, v63, v113
	global_store_dword v[6:7], v26, off sc1
	v_add_co_u32_e32 v6, vcc, s0, v4
	v_mul_f32_e32 v108, v63, v114
	s_waitcnt vmcnt(51)
	v_mul_f32_e32 v114, v63, v78
	v_exp_f32_e32 v78, v107
	v_fmac_f32_e32 v31, v26, v80
	v_addc_co_u32_e32 v7, vcc, 0, v5, vcc
	s_mov_b32 s0, 0xb0000
	global_store_dword v[6:7], v31, off sc1
	v_add_co_u32_e32 v6, vcc, s0, v4
	v_mul_f32_e32 v113, v63, v77
	v_exp_f32_e32 v77, v108
	v_fmac_f32_e32 v36, v31, v79
	v_addc_co_u32_e32 v7, vcc, 0, v5, vcc
	s_mov_b32 s0, 0xb4000
	v_mul_f32_e32 v109, v63, v115
	global_store_dword v[6:7], v36, off sc1
	v_add_co_u32_e32 v6, vcc, s0, v4
	v_exp_f32_e32 v76, v109
	v_fmac_f32_e32 v37, v36, v78
	v_addc_co_u32_e32 v7, vcc, 0, v5, vcc
	s_mov_b32 s0, 0xb8000
	v_mul_f32_e32 v110, v63, v117
	global_store_dword v[6:7], v37, off sc1
	v_add_co_u32_e32 v6, vcc, s0, v4
	v_mul_f32_e32 v111, v63, v116
	s_waitcnt vmcnt(51)
	v_mul_f32_e32 v116, v63, v75
	v_exp_f32_e32 v75, v110
	v_fmac_f32_e32 v38, v37, v77
	v_addc_co_u32_e32 v7, vcc, 0, v5, vcc
	s_mov_b32 s0, 0xbc000
	global_store_dword v[6:7], v38, off sc1
	v_add_co_u32_e32 v6, vcc, s0, v4
	v_mul_f32_e32 v115, v63, v74
	v_exp_f32_e32 v74, v111
	v_fmac_f32_e32 v39, v38, v76
	v_addc_co_u32_e32 v7, vcc, 0, v5, vcc
	s_mov_b32 s0, 0xc0000
	v_mul_f32_e32 v112, v63, v118
	global_store_dword v[6:7], v39, off sc1
	v_add_co_u32_e32 v6, vcc, s0, v4
	v_exp_f32_e32 v73, v112
	v_fmac_f32_e32 v40, v39, v75
	v_addc_co_u32_e32 v7, vcc, 0, v5, vcc
	s_mov_b32 s0, 0xc4000
	global_store_dword v[6:7], v40, off sc1
	v_add_co_u32_e32 v6, vcc, s0, v4
	s_waitcnt vmcnt(52)
	v_mul_f32_e32 v118, v63, v72
	v_exp_f32_e32 v72, v113
	v_fmac_f32_e32 v41, v40, v74
	v_addc_co_u32_e32 v7, vcc, 0, v5, vcc
	s_mov_b32 s0, 0xc8000
	global_store_dword v[6:7], v41, off sc1
	v_add_co_u32_e32 v6, vcc, s0, v4
	v_mul_f32_e32 v117, v63, v71
	v_exp_f32_e32 v71, v114
	v_fmac_f32_e32 v42, v41, v73
	v_addc_co_u32_e32 v7, vcc, 0, v5, vcc
	s_mov_b32 s0, 0xcc000
	global_store_dword v[6:7], v42, off sc1
	v_add_co_u32_e32 v6, vcc, s0, v4
	v_exp_f32_e32 v70, v115
	v_fmac_f32_e32 v43, v42, v72
	v_addc_co_u32_e32 v7, vcc, 0, v5, vcc
	s_mov_b32 s0, 0xd0000
	global_store_dword v[6:7], v43, off sc1
	v_add_co_u32_e32 v6, vcc, s0, v4
	v_exp_f32_e32 v69, v116
	v_fmac_f32_e32 v44, v43, v71
	v_addc_co_u32_e32 v7, vcc, 0, v5, vcc
	s_mov_b32 s0, 0xd4000
	global_store_dword v[6:7], v44, off sc1
	v_add_co_u32_e32 v6, vcc, s0, v4
	v_exp_f32_e32 v68, v117
	v_fmac_f32_e32 v45, v44, v70
	v_addc_co_u32_e32 v7, vcc, 0, v5, vcc
	s_mov_b32 s0, 0xd8000
	global_store_dword v[6:7], v45, off sc1
	v_add_co_u32_e32 v6, vcc, s0, v4
	v_exp_f32_e32 v67, v118
	v_fmac_f32_e32 v46, v45, v69
	v_addc_co_u32_e32 v7, vcc, 0, v5, vcc
	s_mov_b32 s0, 0xdc000
	s_waitcnt vmcnt(56)
	v_mul_f32_e32 v119, v63, v119
	global_store_dword v[6:7], v46, off sc1
	v_add_co_u32_e32 v6, vcc, s0, v4
	v_exp_f32_e32 v66, v119
	v_fmac_f32_e32 v47, v46, v68
	v_addc_co_u32_e32 v7, vcc, 0, v5, vcc
	s_mov_b32 s0, 0xe0000
	s_waitcnt vmcnt(56)
	v_mul_f32_e32 v120, v63, v120
	global_store_dword v[6:7], v47, off sc1
	v_add_co_u32_e32 v6, vcc, s0, v4
	v_exp_f32_e32 v65, v120
	v_fmac_f32_e32 v48, v47, v67
	v_addc_co_u32_e32 v7, vcc, 0, v5, vcc
	s_mov_b32 s0, 0xe4000
	s_waitcnt vmcnt(56)
	v_mul_f32_e32 v121, v63, v121
	global_store_dword v[6:7], v48, off sc1
	v_add_co_u32_e32 v6, vcc, s0, v4
	s_waitcnt vmcnt(56)
	v_mul_f32_e32 v122, v63, v122
	s_waitcnt vmcnt(55)
	v_mul_f32_e32 v123, v63, v123
	s_waitcnt vmcnt(54)
	v_mul_f32_e32 v124, v63, v2
	s_waitcnt vmcnt(53)
	v_mul_f32_e32 v125, v63, v3
	v_exp_f32_e32 v63, v121
	v_fmac_f32_e32 v49, v48, v66
	v_addc_co_u32_e32 v7, vcc, 0, v5, vcc
	s_mov_b32 s0, 0xe8000
	global_store_dword v[6:7], v49, off sc1
	v_add_co_u32_e32 v6, vcc, s0, v4
	v_exp_f32_e32 v3, v122
	v_fmac_f32_e32 v50, v49, v65
	v_addc_co_u32_e32 v7, vcc, 0, v5, vcc
	s_mov_b32 s0, 0xec000
	v_exp_f32_e32 v2, v123
	global_store_dword v[6:7], v50, off sc1
	v_add_co_u32_e32 v6, vcc, s0, v4
	v_fmac_f32_e32 v51, v50, v63
	s_nop 0
	v_addc_co_u32_e32 v7, vcc, 0, v5, vcc
	s_mov_b32 s0, 0xf0000
	global_store_dword v[6:7], v51, off sc1
	v_add_co_u32_e32 v6, vcc, s0, v4
	v_exp_f32_e32 v1, v124
	v_fmac_f32_e32 v35, v51, v3
	v_addc_co_u32_e32 v7, vcc, 0, v5, vcc
	s_mov_b32 s0, 0xf4000
	v_exp_f32_e32 v0, v125
	v_fmac_f32_e32 v34, v35, v2
	v_add_co_u32_e32 v2, vcc, s0, v4
	v_fmac_f32_e32 v32, v34, v1
	s_nop 0
	v_addc_co_u32_e32 v3, vcc, 0, v5, vcc
	global_store_dword v[2:3], v34, off sc1
	v_add_co_u32_e32 v2, vcc, 0xf8000, v4
	v_fmac_f32_e32 v33, v32, v0
	s_nop 0
	v_addc_co_u32_e32 v3, vcc, 0, v5, vcc
	v_add_co_u32_e32 v0, vcc, 0xfc000, v4
	global_store_dword v[6:7], v35, off sc1
	s_nop 0
	v_addc_co_u32_e32 v1, vcc, 0, v5, vcc
	global_store_dword v[2:3], v32, off sc1
	global_store_dword v[0:1], v33, off sc1
	s_endpgm

.Lsc3_loop:
	s_waitcnt lgkmcnt(0)
	ds_read_b128 v[196:199], v57 offset:64
	ds_read_b128 v[200:203], v57 offset:80
	ds_read_b128 v[204:207], v57 offset:96
	ds_read_b128 v[208:211], v57 offset:112
	ds_read_b128 v[212:215], v57 offset:4160
	ds_read_b128 v[216:219], v57 offset:4176
	ds_read_b128 v[220:223], v57 offset:4192
	ds_read_b128 v[224:227], v57 offset:4208
	v_cvt_f32_f16_e32 v46, v181
	v_cvt_f32_f16_e32 v53, v52
	ds_read_u16 v52, v19 offset:528
	v_pk_mul_f32 v[94:95], v[94:95], v[20:21]
	v_pk_mul_f32 v[20:21], v[46:47], v[14:15] op_sel_hi:[0,1]
	v_mul_f32_e32 v55, 0xbfb8aa3b, v53
	v_pk_mul_f32 v[102:103], v[102:103], v[22:23]
	v_exp_f32_e32 v20, v20
	v_pk_mul_f32 v[22:23], v[46:47], v[16:17] op_sel_hi:[0,1]
	v_pk_fma_f32 v[94:95], v[44:45], v[116:117], v[94:95] op_sel_hi:[0,1,1]
	v_exp_f32_e32 v21, v21
	v_pk_mul_f32 v[48:49], v[94:95], v[132:133]
	v_pk_mul_f32 v[88:89], v[88:89], v[24:25]
	v_exp_f32_e32 v22, v22
	v_pk_mul_f32 v[24:25], v[46:47], v[10:11] op_sel_hi:[0,1]
	v_pk_fma_f32 v[102:103], v[44:45], v[118:119], v[102:103] op_sel_hi:[0,1,1]
	v_exp_f32_e32 v23, v23
	v_pk_fma_f32 v[48:49], v[102:103], v[134:135], v[48:49]
	v_exp_f32_e32 v55, v55
	v_pk_mul_f32 v[96:97], v[96:97], v[26:27]
	v_exp_f32_e32 v24, v24
	v_pk_mul_f32 v[26:27], v[46:47], v[12:13] op_sel_hi:[0,1]
	v_pk_fma_f32 v[88:89], v[44:45], v[120:121], v[88:89] op_sel_hi:[0,1,1]
	v_exp_f32_e32 v25, v25
	v_pk_fma_f32 v[48:49], v[88:89], v[136:137], v[48:49]
	v_pk_mul_f32 v[90:91], v[90:91], v[28:29]
	v_exp_f32_e32 v26, v26
	v_pk_mul_f32 v[28:29], v[46:47], v[6:7] op_sel_hi:[0,1]
	v_pk_fma_f32 v[96:97], v[44:45], v[122:123], v[96:97] op_sel_hi:[0,1,1]
	v_exp_f32_e32 v27, v27
	v_pk_fma_f32 v[48:49], v[96:97], v[138:139], v[48:49]
	v_add_f32_e32 v55, 1.0, v55
	v_pk_mul_f32 v[92:93], v[92:93], v[30:31]
	v_exp_f32_e32 v28, v28
	v_pk_mul_f32 v[30:31], v[46:47], v[8:9] op_sel_hi:[0,1]
	v_pk_fma_f32 v[90:91], v[44:45], v[124:125], v[90:91] op_sel_hi:[0,1,1]
	v_exp_f32_e32 v29, v29
	v_pk_fma_f32 v[48:49], v[90:91], v[140:141], v[48:49]
	v_pk_mul_f32 v[98:99], v[98:99], v[32:33]
	v_exp_f32_e32 v30, v30
	v_pk_mul_f32 v[32:33], v[46:47], v[2:3] op_sel_hi:[0,1]
	v_pk_fma_f32 v[92:93], v[44:45], v[126:127], v[92:93] op_sel_hi:[0,1,1]
	v_exp_f32_e32 v31, v31
	v_pk_fma_f32 v[48:49], v[92:93], v[142:143], v[48:49]
	v_rcp_f32_e32 v55, v55
	v_pk_mul_f32 v[100:101], v[100:101], v[34:35]
	v_exp_f32_e32 v32, v32
	v_pk_mul_f32 v[34:35], v[46:47], v[4:5] op_sel_hi:[0,1]
	v_pk_fma_f32 v[98:99], v[44:45], v[128:129], v[98:99] op_sel_hi:[0,1,1]
	v_exp_f32_e32 v33, v33
	v_pk_fma_f32 v[48:49], v[98:99], v[144:145], v[48:49]
	v_exp_f32_e32 v34, v34
	v_pk_fma_f32 v[100:101], v[44:45], v[130:131], v[100:101] op_sel_hi:[0,1,1]
	v_exp_f32_e32 v35, v35
	v_pk_fma_f32 v[48:49], v[100:101], v[146:147], v[48:49]
	v_add_f32_e32 v54, v48, v49
	v_fma_mix_f32 v54, v87, v180, v54 op_sel:[0,1,0] op_sel_hi:[0,1,0]
	v_mul_f32_e32 v54, v54, v53
	v_fma_mix_f32 v44, v181, v181, 0 op_sel:[0,1,0] op_sel_hi:[1,1,0]
	v_fma_mixlo_f16 v56, v54, v55, 0
	ds_write_b16 v19, v56
	v_add_u32_e32 v19, 0x210, v19
	s_waitcnt lgkmcnt(1)
	ds_read_b128 v[116:119], v57 offset:128
	ds_read_b128 v[120:123], v57 offset:144
	ds_read_b128 v[124:127], v57 offset:160
	ds_read_b128 v[128:131], v57 offset:176
	ds_read_b128 v[132:135], v57 offset:4224
	ds_read_b128 v[136:139], v57 offset:4240
	ds_read_b128 v[140:143], v57 offset:4256
	ds_read_b128 v[144:147], v57 offset:4272
	v_cvt_f32_f16_e32 v46, v182
	v_cvt_f32_f16_e32 v53, v52
	ds_read_u16 v52, v19 offset:528
	v_pk_mul_f32 v[94:95], v[94:95], v[20:21]
	v_pk_mul_f32 v[20:21], v[46:47], v[14:15] op_sel_hi:[0,1]
	v_mul_f32_e32 v55, 0xbfb8aa3b, v53
	v_pk_mul_f32 v[102:103], v[102:103], v[22:23]
	v_exp_f32_e32 v20, v20
	v_pk_mul_f32 v[22:23], v[46:47], v[16:17] op_sel_hi:[0,1]
	v_pk_fma_f32 v[94:95], v[44:45], v[196:197], v[94:95] op_sel_hi:[0,1,1]
	v_exp_f32_e32 v21, v21
	v_pk_mul_f32 v[48:49], v[94:95], v[212:213]
	v_pk_mul_f32 v[88:89], v[88:89], v[24:25]
	v_exp_f32_e32 v22, v22
	v_pk_mul_f32 v[24:25], v[46:47], v[10:11] op_sel_hi:[0,1]
	v_pk_fma_f32 v[102:103], v[44:45], v[198:199], v[102:103] op_sel_hi:[0,1,1]
	v_exp_f32_e32 v23, v23
	v_pk_fma_f32 v[48:49], v[102:103], v[214:215], v[48:49]
	v_exp_f32_e32 v55, v55
	v_pk_mul_f32 v[96:97], v[96:97], v[26:27]
	v_exp_f32_e32 v24, v24
	v_pk_mul_f32 v[26:27], v[46:47], v[12:13] op_sel_hi:[0,1]
	v_pk_fma_f32 v[88:89], v[44:45], v[200:201], v[88:89] op_sel_hi:[0,1,1]
	v_exp_f32_e32 v25, v25
	v_pk_fma_f32 v[48:49], v[88:89], v[216:217], v[48:49]
	v_pk_mul_f32 v[90:91], v[90:91], v[28:29]
	v_exp_f32_e32 v26, v26
	v_pk_mul_f32 v[28:29], v[46:47], v[6:7] op_sel_hi:[0,1]
	v_pk_fma_f32 v[96:97], v[44:45], v[202:203], v[96:97] op_sel_hi:[0,1,1]
	v_exp_f32_e32 v27, v27
	v_pk_fma_f32 v[48:49], v[96:97], v[218:219], v[48:49]
	v_add_f32_e32 v55, 1.0, v55
	v_pk_mul_f32 v[92:93], v[92:93], v[30:31]
	v_exp_f32_e32 v28, v28
	v_pk_mul_f32 v[30:31], v[46:47], v[8:9] op_sel_hi:[0,1]
	v_pk_fma_f32 v[90:91], v[44:45], v[204:205], v[90:91] op_sel_hi:[0,1,1]
	v_exp_f32_e32 v29, v29
	v_pk_fma_f32 v[48:49], v[90:91], v[220:221], v[48:49]
	v_pk_mul_f32 v[98:99], v[98:99], v[32:33]
	v_exp_f32_e32 v30, v30
	v_pk_mul_f32 v[32:33], v[46:47], v[2:3] op_sel_hi:[0,1]
	v_pk_fma_f32 v[92:93], v[44:45], v[206:207], v[92:93] op_sel_hi:[0,1,1]
	v_exp_f32_e32 v31, v31
	v_pk_fma_f32 v[48:49], v[92:93], v[222:223], v[48:49]
	v_rcp_f32_e32 v55, v55
	v_pk_mul_f32 v[100:101], v[100:101], v[34:35]
	v_exp_f32_e32 v32, v32
	v_pk_mul_f32 v[34:35], v[46:47], v[4:5] op_sel_hi:[0,1]
	v_pk_fma_f32 v[98:99], v[44:45], v[208:209], v[98:99] op_sel_hi:[0,1,1]
	v_exp_f32_e32 v33, v33
	v_pk_fma_f32 v[48:49], v[98:99], v[224:225], v[48:49]
	v_exp_f32_e32 v34, v34
	v_pk_fma_f32 v[100:101], v[44:45], v[210:211], v[100:101] op_sel_hi:[0,1,1]
	v_exp_f32_e32 v35, v35
	v_pk_fma_f32 v[48:49], v[100:101], v[226:227], v[48:49]
	v_add_f32_e32 v54, v48, v49
	v_fma_mix_f32 v54, v87, v181, v54 op_sel:[0,1,0] op_sel_hi:[0,1,0]
	v_mul_f32_e32 v54, v54, v53
	v_fma_mix_f32 v44, v182, v182, 0 op_sel:[0,1,0] op_sel_hi:[1,1,0]
	v_fma_mixlo_f16 v56, v54, v55, 0
	ds_write_b16 v19, v56
	v_add_u32_e32 v19, 0x210, v19
	s_waitcnt lgkmcnt(1)
	ds_read_b128 v[196:199], v57 offset:192
	ds_read_b128 v[200:203], v57 offset:208
	ds_read_b128 v[204:207], v57 offset:224
	ds_read_b128 v[208:211], v57 offset:240
	ds_read_b128 v[212:215], v57 offset:4288
	ds_read_b128 v[216:219], v57 offset:4304
	ds_read_b128 v[220:223], v57 offset:4320
	ds_read_b128 v[224:227], v57 offset:4336
	v_cvt_f32_f16_e32 v46, v183
	v_cvt_f32_f16_e32 v53, v52
	ds_read_u16 v52, v19 offset:528
	v_pk_mul_f32 v[94:95], v[94:95], v[20:21]
	v_pk_mul_f32 v[20:21], v[46:47], v[14:15] op_sel_hi:[0,1]
	v_mul_f32_e32 v55, 0xbfb8aa3b, v53
	v_pk_mul_f32 v[102:103], v[102:103], v[22:23]
	v_exp_f32_e32 v20, v20
	v_pk_mul_f32 v[22:23], v[46:47], v[16:17] op_sel_hi:[0,1]
	v_pk_fma_f32 v[94:95], v[44:45], v[116:117], v[94:95] op_sel_hi:[0,1,1]
	v_exp_f32_e32 v21, v21
	v_pk_mul_f32 v[48:49], v[94:95], v[132:133]
	v_pk_mul_f32 v[88:89], v[88:89], v[24:25]
	v_exp_f32_e32 v22, v22
	v_pk_mul_f32 v[24:25], v[46:47], v[10:11] op_sel_hi:[0,1]
	v_pk_fma_f32 v[102:103], v[44:45], v[118:119], v[102:103] op_sel_hi:[0,1,1]
	v_exp_f32_e32 v23, v23
	v_pk_fma_f32 v[48:49], v[102:103], v[134:135], v[48:49]
	v_exp_f32_e32 v55, v55
	v_pk_mul_f32 v[96:97], v[96:97], v[26:27]
	v_exp_f32_e32 v24, v24
	v_pk_mul_f32 v[26:27], v[46:47], v[12:13] op_sel_hi:[0,1]
	v_pk_fma_f32 v[88:89], v[44:45], v[120:121], v[88:89] op_sel_hi:[0,1,1]
	v_exp_f32_e32 v25, v25
	v_pk_fma_f32 v[48:49], v[88:89], v[136:137], v[48:49]
	v_pk_mul_f32 v[90:91], v[90:91], v[28:29]
	v_exp_f32_e32 v26, v26
	v_pk_mul_f32 v[28:29], v[46:47], v[6:7] op_sel_hi:[0,1]
	v_pk_fma_f32 v[96:97], v[44:45], v[122:123], v[96:97] op_sel_hi:[0,1,1]
	v_exp_f32_e32 v27, v27
	v_pk_fma_f32 v[48:49], v[96:97], v[138:139], v[48:49]
	v_add_f32_e32 v55, 1.0, v55
	v_pk_mul_f32 v[92:93], v[92:93], v[30:31]
	v_exp_f32_e32 v28, v28
	v_pk_mul_f32 v[30:31], v[46:47], v[8:9] op_sel_hi:[0,1]
	v_pk_fma_f32 v[90:91], v[44:45], v[124:125], v[90:91] op_sel_hi:[0,1,1]
	v_exp_f32_e32 v29, v29
	v_pk_fma_f32 v[48:49], v[90:91], v[140:141], v[48:49]
	v_pk_mul_f32 v[98:99], v[98:99], v[32:33]
	v_exp_f32_e32 v30, v30
	v_pk_mul_f32 v[32:33], v[46:47], v[2:3] op_sel_hi:[0,1]
	v_pk_fma_f32 v[92:93], v[44:45], v[126:127], v[92:93] op_sel_hi:[0,1,1]
	v_exp_f32_e32 v31, v31
	v_pk_fma_f32 v[48:49], v[92:93], v[142:143], v[48:49]
	v_rcp_f32_e32 v55, v55
	v_pk_mul_f32 v[100:101], v[100:101], v[34:35]
	v_exp_f32_e32 v32, v32
	v_pk_mul_f32 v[34:35], v[46:47], v[4:5] op_sel_hi:[0,1]
	v_pk_fma_f32 v[98:99], v[44:45], v[128:129], v[98:99] op_sel_hi:[0,1,1]
	v_exp_f32_e32 v33, v33
	v_pk_fma_f32 v[48:49], v[98:99], v[144:145], v[48:49]
	v_exp_f32_e32 v34, v34
	v_pk_fma_f32 v[100:101], v[44:45], v[130:131], v[100:101] op_sel_hi:[0,1,1]
	v_exp_f32_e32 v35, v35
	v_pk_fma_f32 v[48:49], v[100:101], v[146:147], v[48:49]
	v_add_f32_e32 v54, v48, v49
	v_fma_mix_f32 v54, v87, v182, v54 op_sel:[0,1,0] op_sel_hi:[0,1,0]
	v_mul_f32_e32 v54, v54, v53
	v_fma_mix_f32 v44, v183, v183, 0 op_sel:[0,1,0] op_sel_hi:[1,1,0]
	v_fma_mixlo_f16 v56, v54, v55, 0
	ds_write_b16 v19, v56
	v_add_u32_e32 v19, 0x210, v19
	s_waitcnt lgkmcnt(1)
	ds_read_b128 v[116:119], v57 offset:256
	ds_read_b128 v[120:123], v57 offset:272
	ds_read_b128 v[124:127], v57 offset:288
	ds_read_b128 v[128:131], v57 offset:304
	ds_read_b128 v[132:135], v57 offset:4352
	ds_read_b128 v[136:139], v57 offset:4368
	ds_read_b128 v[140:143], v57 offset:4384
	ds_read_b128 v[144:147], v57 offset:4400
	s_waitcnt vmcnt(2)
	v_cvt_f32_f16_e32 v46, v184
	v_cvt_f32_f16_e32 v53, v52
	ds_read_u16 v52, v19 offset:528
	v_pk_mul_f32 v[94:95], v[94:95], v[20:21]
	v_pk_mul_f32 v[20:21], v[46:47], v[14:15] op_sel_hi:[0,1]
	v_mul_f32_e32 v55, 0xbfb8aa3b, v53
	v_pk_mul_f32 v[102:103], v[102:103], v[22:23]
	v_exp_f32_e32 v20, v20
	v_pk_mul_f32 v[22:23], v[46:47], v[16:17] op_sel_hi:[0,1]
	v_pk_fma_f32 v[94:95], v[44:45], v[196:197], v[94:95] op_sel_hi:[0,1,1]
	v_exp_f32_e32 v21, v21
	v_pk_mul_f32 v[48:49], v[94:95], v[212:213]
	v_pk_mul_f32 v[88:89], v[88:89], v[24:25]
	v_exp_f32_e32 v22, v22
	v_pk_mul_f32 v[24:25], v[46:47], v[10:11] op_sel_hi:[0,1]
	v_pk_fma_f32 v[102:103], v[44:45], v[198:199], v[102:103] op_sel_hi:[0,1,1]
	v_exp_f32_e32 v23, v23
	v_pk_fma_f32 v[48:49], v[102:103], v[214:215], v[48:49]
	v_exp_f32_e32 v55, v55
	v_pk_mul_f32 v[96:97], v[96:97], v[26:27]
	v_exp_f32_e32 v24, v24
	v_pk_mul_f32 v[26:27], v[46:47], v[12:13] op_sel_hi:[0,1]
	v_pk_fma_f32 v[88:89], v[44:45], v[200:201], v[88:89] op_sel_hi:[0,1,1]
	v_exp_f32_e32 v25, v25
	v_pk_fma_f32 v[48:49], v[88:89], v[216:217], v[48:49]
	v_pk_mul_f32 v[90:91], v[90:91], v[28:29]
	v_exp_f32_e32 v26, v26
	v_pk_mul_f32 v[28:29], v[46:47], v[6:7] op_sel_hi:[0,1]
	v_pk_fma_f32 v[96:97], v[44:45], v[202:203], v[96:97] op_sel_hi:[0,1,1]
	v_exp_f32_e32 v27, v27
	v_pk_fma_f32 v[48:49], v[96:97], v[218:219], v[48:49]
	v_add_f32_e32 v55, 1.0, v55
	v_pk_mul_f32 v[92:93], v[92:93], v[30:31]
	v_exp_f32_e32 v28, v28
	v_pk_mul_f32 v[30:31], v[46:47], v[8:9] op_sel_hi:[0,1]
	v_pk_fma_f32 v[90:91], v[44:45], v[204:205], v[90:91] op_sel_hi:[0,1,1]
	v_exp_f32_e32 v29, v29
	v_pk_fma_f32 v[48:49], v[90:91], v[220:221], v[48:49]
	v_pk_mul_f32 v[98:99], v[98:99], v[32:33]
	v_exp_f32_e32 v30, v30
	v_pk_mul_f32 v[32:33], v[46:47], v[2:3] op_sel_hi:[0,1]
	v_pk_fma_f32 v[92:93], v[44:45], v[206:207], v[92:93] op_sel_hi:[0,1,1]
	v_exp_f32_e32 v31, v31
	v_pk_fma_f32 v[48:49], v[92:93], v[222:223], v[48:49]
	v_rcp_f32_e32 v55, v55
	v_pk_mul_f32 v[100:101], v[100:101], v[34:35]
	v_exp_f32_e32 v32, v32
	v_pk_mul_f32 v[34:35], v[46:47], v[4:5] op_sel_hi:[0,1]
	v_pk_fma_f32 v[98:99], v[44:45], v[208:209], v[98:99] op_sel_hi:[0,1,1]
	v_exp_f32_e32 v33, v33
	v_pk_fma_f32 v[48:49], v[98:99], v[224:225], v[48:49]
	v_exp_f32_e32 v34, v34
	v_pk_fma_f32 v[100:101], v[44:45], v[210:211], v[100:101] op_sel_hi:[0,1,1]
	v_exp_f32_e32 v35, v35
	v_pk_fma_f32 v[48:49], v[100:101], v[226:227], v[48:49]
	v_add_f32_e32 v54, v48, v49
	v_fma_mix_f32 v54, v87, v183, v54 op_sel:[0,1,0] op_sel_hi:[0,1,0]
	v_mul_f32_e32 v54, v54, v53
	v_fma_mix_f32 v44, v184, v184, 0 op_sel:[0,1,0] op_sel_hi:[1,1,0]
	global_load_dwordx4 v[180:183], v[58:59], off offset:-4096
	v_fma_mixlo_f16 v56, v54, v55, 0
	ds_write_b16 v19, v56
	v_add_u32_e32 v19, 0x210, v19
	s_waitcnt lgkmcnt(1)
	ds_read_b128 v[196:199], v57 offset:320
	ds_read_b128 v[200:203], v57 offset:336
	ds_read_b128 v[204:207], v57 offset:352
	ds_read_b128 v[208:211], v57 offset:368
	ds_read_b128 v[212:215], v57 offset:4416
	ds_read_b128 v[216:219], v57 offset:4432
	ds_read_b128 v[220:223], v57 offset:4448
	ds_read_b128 v[224:227], v57 offset:4464
	v_cvt_f32_f16_e32 v46, v185
	v_cvt_f32_f16_e32 v53, v52
	ds_read_u16 v52, v19 offset:528
	v_pk_mul_f32 v[94:95], v[94:95], v[20:21]
	v_pk_mul_f32 v[20:21], v[46:47], v[14:15] op_sel_hi:[0,1]
	v_mul_f32_e32 v55, 0xbfb8aa3b, v53
	v_pk_mul_f32 v[102:103], v[102:103], v[22:23]
	v_exp_f32_e32 v20, v20
	v_pk_mul_f32 v[22:23], v[46:47], v[16:17] op_sel_hi:[0,1]
	v_pk_fma_f32 v[94:95], v[44:45], v[116:117], v[94:95] op_sel_hi:[0,1,1]
	v_exp_f32_e32 v21, v21
	v_pk_mul_f32 v[48:49], v[94:95], v[132:133]
	v_pk_mul_f32 v[88:89], v[88:89], v[24:25]
	v_exp_f32_e32 v22, v22
	v_pk_mul_f32 v[24:25], v[46:47], v[10:11] op_sel_hi:[0,1]
	v_pk_fma_f32 v[102:103], v[44:45], v[118:119], v[102:103] op_sel_hi:[0,1,1]
	v_exp_f32_e32 v23, v23
	v_pk_fma_f32 v[48:49], v[102:103], v[134:135], v[48:49]
	v_exp_f32_e32 v55, v55
	v_pk_mul_f32 v[96:97], v[96:97], v[26:27]
	v_exp_f32_e32 v24, v24
	v_pk_mul_f32 v[26:27], v[46:47], v[12:13] op_sel_hi:[0,1]
	v_pk_fma_f32 v[88:89], v[44:45], v[120:121], v[88:89] op_sel_hi:[0,1,1]
	v_exp_f32_e32 v25, v25
	v_pk_fma_f32 v[48:49], v[88:89], v[136:137], v[48:49]
	v_pk_mul_f32 v[90:91], v[90:91], v[28:29]
	v_exp_f32_e32 v26, v26
	v_pk_mul_f32 v[28:29], v[46:47], v[6:7] op_sel_hi:[0,1]
	v_pk_fma_f32 v[96:97], v[44:45], v[122:123], v[96:97] op_sel_hi:[0,1,1]
	v_exp_f32_e32 v27, v27
	v_pk_fma_f32 v[48:49], v[96:97], v[138:139], v[48:49]
	v_add_f32_e32 v55, 1.0, v55
	v_pk_mul_f32 v[92:93], v[92:93], v[30:31]
	v_exp_f32_e32 v28, v28
	v_pk_mul_f32 v[30:31], v[46:47], v[8:9] op_sel_hi:[0,1]
	v_pk_fma_f32 v[90:91], v[44:45], v[124:125], v[90:91] op_sel_hi:[0,1,1]
	v_exp_f32_e32 v29, v29
	v_pk_fma_f32 v[48:49], v[90:91], v[140:141], v[48:49]
	v_pk_mul_f32 v[98:99], v[98:99], v[32:33]
	v_exp_f32_e32 v30, v30
	v_pk_mul_f32 v[32:33], v[46:47], v[2:3] op_sel_hi:[0,1]
	v_pk_fma_f32 v[92:93], v[44:45], v[126:127], v[92:93] op_sel_hi:[0,1,1]
	v_exp_f32_e32 v31, v31
	v_pk_fma_f32 v[48:49], v[92:93], v[142:143], v[48:49]
	v_rcp_f32_e32 v55, v55
	v_pk_mul_f32 v[100:101], v[100:101], v[34:35]
	v_exp_f32_e32 v32, v32
	v_pk_mul_f32 v[34:35], v[46:47], v[4:5] op_sel_hi:[0,1]
	v_pk_fma_f32 v[98:99], v[44:45], v[128:129], v[98:99] op_sel_hi:[0,1,1]
	v_exp_f32_e32 v33, v33
	v_pk_fma_f32 v[48:49], v[98:99], v[144:145], v[48:49]
	v_exp_f32_e32 v34, v34
	v_pk_fma_f32 v[100:101], v[44:45], v[130:131], v[100:101] op_sel_hi:[0,1,1]
	v_exp_f32_e32 v35, v35
	v_pk_fma_f32 v[48:49], v[100:101], v[146:147], v[48:49]
	v_add_f32_e32 v54, v48, v49
	v_fma_mix_f32 v54, v87, v184, v54 op_sel:[0,1,0] op_sel_hi:[0,1,0]
	v_mul_f32_e32 v54, v54, v53
	v_fma_mix_f32 v44, v185, v185, 0 op_sel:[0,1,0] op_sel_hi:[1,1,0]
	v_fma_mixlo_f16 v56, v54, v55, 0
	ds_write_b16 v19, v56
	v_add_u32_e32 v19, 0x210, v19
	s_waitcnt lgkmcnt(1)
	ds_read_b128 v[116:119], v57 offset:384
	ds_read_b128 v[120:123], v57 offset:400
	ds_read_b128 v[124:127], v57 offset:416
	ds_read_b128 v[128:131], v57 offset:432
	ds_read_b128 v[132:135], v57 offset:4480
	ds_read_b128 v[136:139], v57 offset:4496
	ds_read_b128 v[140:143], v57 offset:4512
	ds_read_b128 v[144:147], v57 offset:4528
	v_cvt_f32_f16_e32 v46, v186
	v_cvt_f32_f16_e32 v53, v52
	ds_read_u16 v52, v19 offset:528
	v_pk_mul_f32 v[94:95], v[94:95], v[20:21]
	v_pk_mul_f32 v[20:21], v[46:47], v[14:15] op_sel_hi:[0,1]
	v_mul_f32_e32 v55, 0xbfb8aa3b, v53
	v_pk_mul_f32 v[102:103], v[102:103], v[22:23]
	v_exp_f32_e32 v20, v20
	v_pk_mul_f32 v[22:23], v[46:47], v[16:17] op_sel_hi:[0,1]
	v_pk_fma_f32 v[94:95], v[44:45], v[196:197], v[94:95] op_sel_hi:[0,1,1]
	v_exp_f32_e32 v21, v21
	v_pk_mul_f32 v[48:49], v[94:95], v[212:213]
	v_pk_mul_f32 v[88:89], v[88:89], v[24:25]
	v_exp_f32_e32 v22, v22
	v_pk_mul_f32 v[24:25], v[46:47], v[10:11] op_sel_hi:[0,1]
	v_pk_fma_f32 v[102:103], v[44:45], v[198:199], v[102:103] op_sel_hi:[0,1,1]
	v_exp_f32_e32 v23, v23
	v_pk_fma_f32 v[48:49], v[102:103], v[214:215], v[48:49]
	v_exp_f32_e32 v55, v55
	v_pk_mul_f32 v[96:97], v[96:97], v[26:27]
	v_exp_f32_e32 v24, v24
	v_pk_mul_f32 v[26:27], v[46:47], v[12:13] op_sel_hi:[0,1]
	v_pk_fma_f32 v[88:89], v[44:45], v[200:201], v[88:89] op_sel_hi:[0,1,1]
	v_exp_f32_e32 v25, v25
	v_pk_fma_f32 v[48:49], v[88:89], v[216:217], v[48:49]
	v_pk_mul_f32 v[90:91], v[90:91], v[28:29]
	v_exp_f32_e32 v26, v26
	v_pk_mul_f32 v[28:29], v[46:47], v[6:7] op_sel_hi:[0,1]
	v_pk_fma_f32 v[96:97], v[44:45], v[202:203], v[96:97] op_sel_hi:[0,1,1]
	v_exp_f32_e32 v27, v27
	v_pk_fma_f32 v[48:49], v[96:97], v[218:219], v[48:49]
	v_add_f32_e32 v55, 1.0, v55
	v_pk_mul_f32 v[92:93], v[92:93], v[30:31]
	v_exp_f32_e32 v28, v28
	v_pk_mul_f32 v[30:31], v[46:47], v[8:9] op_sel_hi:[0,1]
	v_pk_fma_f32 v[90:91], v[44:45], v[204:205], v[90:91] op_sel_hi:[0,1,1]
	v_exp_f32_e32 v29, v29
	v_pk_fma_f32 v[48:49], v[90:91], v[220:221], v[48:49]
	v_pk_mul_f32 v[98:99], v[98:99], v[32:33]
	v_exp_f32_e32 v30, v30
	v_pk_mul_f32 v[32:33], v[46:47], v[2:3] op_sel_hi:[0,1]
	v_pk_fma_f32 v[92:93], v[44:45], v[206:207], v[92:93] op_sel_hi:[0,1,1]
	v_exp_f32_e32 v31, v31
	v_pk_fma_f32 v[48:49], v[92:93], v[222:223], v[48:49]
	v_rcp_f32_e32 v55, v55
	v_pk_mul_f32 v[100:101], v[100:101], v[34:35]
	v_exp_f32_e32 v32, v32
	v_pk_mul_f32 v[34:35], v[46:47], v[4:5] op_sel_hi:[0,1]
	v_pk_fma_f32 v[98:99], v[44:45], v[208:209], v[98:99] op_sel_hi:[0,1,1]
	v_exp_f32_e32 v33, v33
	v_pk_fma_f32 v[48:49], v[98:99], v[224:225], v[48:49]
	v_exp_f32_e32 v34, v34
	v_pk_fma_f32 v[100:101], v[44:45], v[210:211], v[100:101] op_sel_hi:[0,1,1]
	v_exp_f32_e32 v35, v35
	v_pk_fma_f32 v[48:49], v[100:101], v[226:227], v[48:49]
	v_add_f32_e32 v54, v48, v49
	v_fma_mix_f32 v54, v87, v185, v54 op_sel:[0,1,0] op_sel_hi:[0,1,0]
	v_mul_f32_e32 v54, v54, v53
	v_fma_mix_f32 v44, v186, v186, 0 op_sel:[0,1,0] op_sel_hi:[1,1,0]
	v_fma_mixlo_f16 v56, v54, v55, 0
	ds_write_b16 v19, v56
	v_add_u32_e32 v19, 0x210, v19
	s_waitcnt lgkmcnt(1)
	ds_read_b128 v[196:199], v57 offset:448
	ds_read_b128 v[200:203], v57 offset:464
	ds_read_b128 v[204:207], v57 offset:480
	ds_read_b128 v[208:211], v57 offset:496
	ds_read_b128 v[212:215], v57 offset:4544
	ds_read_b128 v[216:219], v57 offset:4560
	ds_read_b128 v[220:223], v57 offset:4576
	ds_read_b128 v[224:227], v57 offset:4592
	v_cvt_f32_f16_e32 v46, v187
	v_cvt_f32_f16_e32 v53, v52
	ds_read_u16 v52, v19 offset:528
	v_pk_mul_f32 v[94:95], v[94:95], v[20:21]
	v_pk_mul_f32 v[20:21], v[46:47], v[14:15] op_sel_hi:[0,1]
	v_mul_f32_e32 v55, 0xbfb8aa3b, v53
	v_pk_mul_f32 v[102:103], v[102:103], v[22:23]
	v_exp_f32_e32 v20, v20
	v_pk_mul_f32 v[22:23], v[46:47], v[16:17] op_sel_hi:[0,1]
	v_pk_fma_f32 v[94:95], v[44:45], v[116:117], v[94:95] op_sel_hi:[0,1,1]
	v_exp_f32_e32 v21, v21
	v_pk_mul_f32 v[48:49], v[94:95], v[132:133]
	v_pk_mul_f32 v[88:89], v[88:89], v[24:25]
	v_exp_f32_e32 v22, v22
	v_pk_mul_f32 v[24:25], v[46:47], v[10:11] op_sel_hi:[0,1]
	v_pk_fma_f32 v[102:103], v[44:45], v[118:119], v[102:103] op_sel_hi:[0,1,1]
	v_exp_f32_e32 v23, v23
	v_pk_fma_f32 v[48:49], v[102:103], v[134:135], v[48:49]
	v_exp_f32_e32 v55, v55
	v_pk_mul_f32 v[96:97], v[96:97], v[26:27]
	v_exp_f32_e32 v24, v24
	v_pk_mul_f32 v[26:27], v[46:47], v[12:13] op_sel_hi:[0,1]
	v_pk_fma_f32 v[88:89], v[44:45], v[120:121], v[88:89] op_sel_hi:[0,1,1]
	v_exp_f32_e32 v25, v25
	v_pk_fma_f32 v[48:49], v[88:89], v[136:137], v[48:49]
	v_pk_mul_f32 v[90:91], v[90:91], v[28:29]
	v_exp_f32_e32 v26, v26
	v_pk_mul_f32 v[28:29], v[46:47], v[6:7] op_sel_hi:[0,1]
	v_pk_fma_f32 v[96:97], v[44:45], v[122:123], v[96:97] op_sel_hi:[0,1,1]
	v_exp_f32_e32 v27, v27
	v_pk_fma_f32 v[48:49], v[96:97], v[138:139], v[48:49]
	v_add_f32_e32 v55, 1.0, v55
	v_pk_mul_f32 v[92:93], v[92:93], v[30:31]
	v_exp_f32_e32 v28, v28
	v_pk_mul_f32 v[30:31], v[46:47], v[8:9] op_sel_hi:[0,1]
	v_pk_fma_f32 v[90:91], v[44:45], v[124:125], v[90:91] op_sel_hi:[0,1,1]
	v_exp_f32_e32 v29, v29
	v_pk_fma_f32 v[48:49], v[90:91], v[140:141], v[48:49]
	v_pk_mul_f32 v[98:99], v[98:99], v[32:33]
	v_exp_f32_e32 v30, v30
	v_pk_mul_f32 v[32:33], v[46:47], v[2:3] op_sel_hi:[0,1]
	v_pk_fma_f32 v[92:93], v[44:45], v[126:127], v[92:93] op_sel_hi:[0,1,1]
	v_exp_f32_e32 v31, v31
	v_pk_fma_f32 v[48:49], v[92:93], v[142:143], v[48:49]
	v_rcp_f32_e32 v55, v55
	v_pk_mul_f32 v[100:101], v[100:101], v[34:35]
	v_exp_f32_e32 v32, v32
	v_pk_mul_f32 v[34:35], v[46:47], v[4:5] op_sel_hi:[0,1]
	v_pk_fma_f32 v[98:99], v[44:45], v[128:129], v[98:99] op_sel_hi:[0,1,1]
	v_exp_f32_e32 v33, v33
	v_pk_fma_f32 v[48:49], v[98:99], v[144:145], v[48:49]
	v_exp_f32_e32 v34, v34
	v_pk_fma_f32 v[100:101], v[44:45], v[130:131], v[100:101] op_sel_hi:[0,1,1]
	v_exp_f32_e32 v35, v35
	v_pk_fma_f32 v[48:49], v[100:101], v[146:147], v[48:49]
	v_add_f32_e32 v54, v48, v49
	v_fma_mix_f32 v54, v87, v186, v54 op_sel:[0,1,0] op_sel_hi:[0,1,0]
	v_mul_f32_e32 v54, v54, v53
	v_fma_mix_f32 v44, v187, v187, 0 op_sel:[0,1,0] op_sel_hi:[1,1,0]
	v_fma_mixlo_f16 v56, v54, v55, 0
	ds_write_b16 v19, v56
	v_add_u32_e32 v19, 0x210, v19
	s_waitcnt lgkmcnt(1)
	ds_read_b128 v[116:119], v57 offset:512
	ds_read_b128 v[120:123], v57 offset:528
	ds_read_b128 v[124:127], v57 offset:544
	ds_read_b128 v[128:131], v57 offset:560
	ds_read_b128 v[132:135], v57 offset:4608
	ds_read_b128 v[136:139], v57 offset:4624
	ds_read_b128 v[140:143], v57 offset:4640
	ds_read_b128 v[144:147], v57 offset:4656
	s_waitcnt vmcnt(2)
	v_cvt_f32_f16_e32 v46, v188
	v_cvt_f32_f16_e32 v53, v52
	ds_read_u16 v52, v19 offset:528
	v_pk_mul_f32 v[94:95], v[94:95], v[20:21]
	v_pk_mul_f32 v[20:21], v[46:47], v[14:15] op_sel_hi:[0,1]
	v_mul_f32_e32 v55, 0xbfb8aa3b, v53
	v_pk_mul_f32 v[102:103], v[102:103], v[22:23]
	v_exp_f32_e32 v20, v20
	v_pk_mul_f32 v[22:23], v[46:47], v[16:17] op_sel_hi:[0,1]
	v_pk_fma_f32 v[94:95], v[44:45], v[196:197], v[94:95] op_sel_hi:[0,1,1]
	v_exp_f32_e32 v21, v21
	v_pk_mul_f32 v[48:49], v[94:95], v[212:213]
	v_pk_mul_f32 v[88:89], v[88:89], v[24:25]
	v_exp_f32_e32 v22, v22
	v_pk_mul_f32 v[24:25], v[46:47], v[10:11] op_sel_hi:[0,1]
	v_pk_fma_f32 v[102:103], v[44:45], v[198:199], v[102:103] op_sel_hi:[0,1,1]
	v_exp_f32_e32 v23, v23
	v_pk_fma_f32 v[48:49], v[102:103], v[214:215], v[48:49]
	v_exp_f32_e32 v55, v55
	v_pk_mul_f32 v[96:97], v[96:97], v[26:27]
	v_exp_f32_e32 v24, v24
	v_pk_mul_f32 v[26:27], v[46:47], v[12:13] op_sel_hi:[0,1]
	v_pk_fma_f32 v[88:89], v[44:45], v[200:201], v[88:89] op_sel_hi:[0,1,1]
	v_exp_f32_e32 v25, v25
	v_pk_fma_f32 v[48:49], v[88:89], v[216:217], v[48:49]
	v_pk_mul_f32 v[90:91], v[90:91], v[28:29]
	v_exp_f32_e32 v26, v26
	v_pk_mul_f32 v[28:29], v[46:47], v[6:7] op_sel_hi:[0,1]
	v_pk_fma_f32 v[96:97], v[44:45], v[202:203], v[96:97] op_sel_hi:[0,1,1]
	v_exp_f32_e32 v27, v27
	v_pk_fma_f32 v[48:49], v[96:97], v[218:219], v[48:49]
	v_add_f32_e32 v55, 1.0, v55
	v_pk_mul_f32 v[92:93], v[92:93], v[30:31]
	v_exp_f32_e32 v28, v28
	v_pk_mul_f32 v[30:31], v[46:47], v[8:9] op_sel_hi:[0,1]
	v_pk_fma_f32 v[90:91], v[44:45], v[204:205], v[90:91] op_sel_hi:[0,1,1]
	v_exp_f32_e32 v29, v29
	v_pk_fma_f32 v[48:49], v[90:91], v[220:221], v[48:49]
	v_pk_mul_f32 v[98:99], v[98:99], v[32:33]
	v_exp_f32_e32 v30, v30
	v_pk_mul_f32 v[32:33], v[46:47], v[2:3] op_sel_hi:[0,1]
	v_pk_fma_f32 v[92:93], v[44:45], v[206:207], v[92:93] op_sel_hi:[0,1,1]
	v_exp_f32_e32 v31, v31
	v_pk_fma_f32 v[48:49], v[92:93], v[222:223], v[48:49]
	v_rcp_f32_e32 v55, v55
	v_pk_mul_f32 v[100:101], v[100:101], v[34:35]
	v_exp_f32_e32 v32, v32
	v_pk_mul_f32 v[34:35], v[46:47], v[4:5] op_sel_hi:[0,1]
	v_pk_fma_f32 v[98:99], v[44:45], v[208:209], v[98:99] op_sel_hi:[0,1,1]
	v_exp_f32_e32 v33, v33
	v_pk_fma_f32 v[48:49], v[98:99], v[224:225], v[48:49]
	v_exp_f32_e32 v34, v34
	v_pk_fma_f32 v[100:101], v[44:45], v[210:211], v[100:101] op_sel_hi:[0,1,1]
	v_exp_f32_e32 v35, v35
	v_pk_fma_f32 v[48:49], v[100:101], v[226:227], v[48:49]
	v_add_f32_e32 v54, v48, v49
	v_fma_mix_f32 v54, v87, v187, v54 op_sel:[0,1,0] op_sel_hi:[0,1,0]
	v_mul_f32_e32 v54, v54, v53
	v_fma_mix_f32 v44, v188, v188, 0 op_sel:[0,1,0] op_sel_hi:[1,1,0]
	global_load_dwordx4 v[184:187], v[58:59], off
	v_fma_mixlo_f16 v56, v54, v55, 0
	ds_write_b16 v19, v56
	v_add_u32_e32 v19, 0x210, v19
	s_waitcnt lgkmcnt(1)
	ds_read_b128 v[196:199], v57 offset:576
	ds_read_b128 v[200:203], v57 offset:592
	ds_read_b128 v[204:207], v57 offset:608
	ds_read_b128 v[208:211], v57 offset:624
	ds_read_b128 v[212:215], v57 offset:4672
	ds_read_b128 v[216:219], v57 offset:4688
	ds_read_b128 v[220:223], v57 offset:4704
	ds_read_b128 v[224:227], v57 offset:4720
	v_cvt_f32_f16_e32 v46, v189
	v_cvt_f32_f16_e32 v53, v52
	ds_read_u16 v52, v19 offset:528
	v_pk_mul_f32 v[94:95], v[94:95], v[20:21]
	v_pk_mul_f32 v[20:21], v[46:47], v[14:15] op_sel_hi:[0,1]
	v_mul_f32_e32 v55, 0xbfb8aa3b, v53
	v_pk_mul_f32 v[102:103], v[102:103], v[22:23]
	v_exp_f32_e32 v20, v20
	v_pk_mul_f32 v[22:23], v[46:47], v[16:17] op_sel_hi:[0,1]
	v_pk_fma_f32 v[94:95], v[44:45], v[116:117], v[94:95] op_sel_hi:[0,1,1]
	v_exp_f32_e32 v21, v21
	v_pk_mul_f32 v[48:49], v[94:95], v[132:133]
	v_pk_mul_f32 v[88:89], v[88:89], v[24:25]
	v_exp_f32_e32 v22, v22
	v_pk_mul_f32 v[24:25], v[46:47], v[10:11] op_sel_hi:[0,1]
	v_pk_fma_f32 v[102:103], v[44:45], v[118:119], v[102:103] op_sel_hi:[0,1,1]
	v_exp_f32_e32 v23, v23
	v_pk_fma_f32 v[48:49], v[102:103], v[134:135], v[48:49]
	v_exp_f32_e32 v55, v55
	v_pk_mul_f32 v[96:97], v[96:97], v[26:27]
	v_exp_f32_e32 v24, v24
	v_pk_mul_f32 v[26:27], v[46:47], v[12:13] op_sel_hi:[0,1]
	v_pk_fma_f32 v[88:89], v[44:45], v[120:121], v[88:89] op_sel_hi:[0,1,1]
	v_exp_f32_e32 v25, v25
	v_pk_fma_f32 v[48:49], v[88:89], v[136:137], v[48:49]
	v_pk_mul_f32 v[90:91], v[90:91], v[28:29]
	v_exp_f32_e32 v26, v26
	v_pk_mul_f32 v[28:29], v[46:47], v[6:7] op_sel_hi:[0,1]
	v_pk_fma_f32 v[96:97], v[44:45], v[122:123], v[96:97] op_sel_hi:[0,1,1]
	v_exp_f32_e32 v27, v27
	v_pk_fma_f32 v[48:49], v[96:97], v[138:139], v[48:49]
	v_add_f32_e32 v55, 1.0, v55
	v_pk_mul_f32 v[92:93], v[92:93], v[30:31]
	v_exp_f32_e32 v28, v28
	v_pk_mul_f32 v[30:31], v[46:47], v[8:9] op_sel_hi:[0,1]
	v_pk_fma_f32 v[90:91], v[44:45], v[124:125], v[90:91] op_sel_hi:[0,1,1]
	v_exp_f32_e32 v29, v29
	v_pk_fma_f32 v[48:49], v[90:91], v[140:141], v[48:49]
	v_pk_mul_f32 v[98:99], v[98:99], v[32:33]
	v_exp_f32_e32 v30, v30
	v_pk_mul_f32 v[32:33], v[46:47], v[2:3] op_sel_hi:[0,1]
	v_pk_fma_f32 v[92:93], v[44:45], v[126:127], v[92:93] op_sel_hi:[0,1,1]
	v_exp_f32_e32 v31, v31
	v_pk_fma_f32 v[48:49], v[92:93], v[142:143], v[48:49]
	v_rcp_f32_e32 v55, v55
	v_pk_mul_f32 v[100:101], v[100:101], v[34:35]
	v_exp_f32_e32 v32, v32
	v_pk_mul_f32 v[34:35], v[46:47], v[4:5] op_sel_hi:[0,1]
	v_pk_fma_f32 v[98:99], v[44:45], v[128:129], v[98:99] op_sel_hi:[0,1,1]
	v_exp_f32_e32 v33, v33
	v_pk_fma_f32 v[48:49], v[98:99], v[144:145], v[48:49]
	v_exp_f32_e32 v34, v34
	v_pk_fma_f32 v[100:101], v[44:45], v[130:131], v[100:101] op_sel_hi:[0,1,1]
	v_exp_f32_e32 v35, v35
	v_pk_fma_f32 v[48:49], v[100:101], v[146:147], v[48:49]
	v_add_f32_e32 v54, v48, v49
	v_fma_mix_f32 v54, v87, v188, v54 op_sel:[0,1,0] op_sel_hi:[0,1,0]
	v_mul_f32_e32 v54, v54, v53
	v_fma_mix_f32 v44, v189, v189, 0 op_sel:[0,1,0] op_sel_hi:[1,1,0]
	v_fma_mixlo_f16 v56, v54, v55, 0
	ds_write_b16 v19, v56
	v_add_u32_e32 v19, 0x210, v19
	s_waitcnt lgkmcnt(1)
	ds_read_b128 v[116:119], v57 offset:640
	ds_read_b128 v[120:123], v57 offset:656
	ds_read_b128 v[124:127], v57 offset:672
	ds_read_b128 v[128:131], v57 offset:688
	ds_read_b128 v[132:135], v57 offset:4736
	ds_read_b128 v[136:139], v57 offset:4752
	ds_read_b128 v[140:143], v57 offset:4768
	ds_read_b128 v[144:147], v57 offset:4784
	v_cvt_f32_f16_e32 v46, v190
	v_cvt_f32_f16_e32 v53, v52
	ds_read_u16 v52, v19 offset:528
	v_pk_mul_f32 v[94:95], v[94:95], v[20:21]
	v_pk_mul_f32 v[20:21], v[46:47], v[14:15] op_sel_hi:[0,1]
	v_mul_f32_e32 v55, 0xbfb8aa3b, v53
	v_pk_mul_f32 v[102:103], v[102:103], v[22:23]
	v_exp_f32_e32 v20, v20
	v_pk_mul_f32 v[22:23], v[46:47], v[16:17] op_sel_hi:[0,1]
	v_pk_fma_f32 v[94:95], v[44:45], v[196:197], v[94:95] op_sel_hi:[0,1,1]
	v_exp_f32_e32 v21, v21
	v_pk_mul_f32 v[48:49], v[94:95], v[212:213]
	v_pk_mul_f32 v[88:89], v[88:89], v[24:25]
	v_exp_f32_e32 v22, v22
	v_pk_mul_f32 v[24:25], v[46:47], v[10:11] op_sel_hi:[0,1]
	v_pk_fma_f32 v[102:103], v[44:45], v[198:199], v[102:103] op_sel_hi:[0,1,1]
	v_exp_f32_e32 v23, v23
	v_pk_fma_f32 v[48:49], v[102:103], v[214:215], v[48:49]
	v_exp_f32_e32 v55, v55
	v_pk_mul_f32 v[96:97], v[96:97], v[26:27]
	v_exp_f32_e32 v24, v24
	v_pk_mul_f32 v[26:27], v[46:47], v[12:13] op_sel_hi:[0,1]
	v_pk_fma_f32 v[88:89], v[44:45], v[200:201], v[88:89] op_sel_hi:[0,1,1]
	v_exp_f32_e32 v25, v25
	v_pk_fma_f32 v[48:49], v[88:89], v[216:217], v[48:49]
	v_pk_mul_f32 v[90:91], v[90:91], v[28:29]
	v_exp_f32_e32 v26, v26
	v_pk_mul_f32 v[28:29], v[46:47], v[6:7] op_sel_hi:[0,1]
	v_pk_fma_f32 v[96:97], v[44:45], v[202:203], v[96:97] op_sel_hi:[0,1,1]
	v_exp_f32_e32 v27, v27
	v_pk_fma_f32 v[48:49], v[96:97], v[218:219], v[48:49]
	v_add_f32_e32 v55, 1.0, v55
	v_pk_mul_f32 v[92:93], v[92:93], v[30:31]
	v_exp_f32_e32 v28, v28
	v_pk_mul_f32 v[30:31], v[46:47], v[8:9] op_sel_hi:[0,1]
	v_pk_fma_f32 v[90:91], v[44:45], v[204:205], v[90:91] op_sel_hi:[0,1,1]
	v_exp_f32_e32 v29, v29
	v_pk_fma_f32 v[48:49], v[90:91], v[220:221], v[48:49]
	v_pk_mul_f32 v[98:99], v[98:99], v[32:33]
	v_exp_f32_e32 v30, v30
	v_pk_mul_f32 v[32:33], v[46:47], v[2:3] op_sel_hi:[0,1]
	v_pk_fma_f32 v[92:93], v[44:45], v[206:207], v[92:93] op_sel_hi:[0,1,1]
	v_exp_f32_e32 v31, v31
	v_pk_fma_f32 v[48:49], v[92:93], v[222:223], v[48:49]
	v_rcp_f32_e32 v55, v55
	v_pk_mul_f32 v[100:101], v[100:101], v[34:35]
	v_exp_f32_e32 v32, v32
	v_pk_mul_f32 v[34:35], v[46:47], v[4:5] op_sel_hi:[0,1]
	v_pk_fma_f32 v[98:99], v[44:45], v[208:209], v[98:99] op_sel_hi:[0,1,1]
	v_exp_f32_e32 v33, v33
	v_pk_fma_f32 v[48:49], v[98:99], v[224:225], v[48:49]
	v_exp_f32_e32 v34, v34
	v_pk_fma_f32 v[100:101], v[44:45], v[210:211], v[100:101] op_sel_hi:[0,1,1]
	v_exp_f32_e32 v35, v35
	v_pk_fma_f32 v[48:49], v[100:101], v[226:227], v[48:49]
	v_add_f32_e32 v54, v48, v49
	v_fma_mix_f32 v54, v87, v189, v54 op_sel:[0,1,0] op_sel_hi:[0,1,0]
	v_mul_f32_e32 v54, v54, v53
	v_fma_mix_f32 v44, v190, v190, 0 op_sel:[0,1,0] op_sel_hi:[1,1,0]
	v_fma_mixlo_f16 v56, v54, v55, 0
	ds_write_b16 v19, v56
	v_add_u32_e32 v19, 0x210, v19
	s_waitcnt lgkmcnt(1)
	ds_read_b128 v[196:199], v57 offset:704
	ds_read_b128 v[200:203], v57 offset:720
	ds_read_b128 v[204:207], v57 offset:736
	ds_read_b128 v[208:211], v57 offset:752
	ds_read_b128 v[212:215], v57 offset:4800
	ds_read_b128 v[216:219], v57 offset:4816
	ds_read_b128 v[220:223], v57 offset:4832
	ds_read_b128 v[224:227], v57 offset:4848
	v_cvt_f32_f16_e32 v46, v191
	v_cvt_f32_f16_e32 v53, v52
	ds_read_u16 v52, v19 offset:528
	v_pk_mul_f32 v[94:95], v[94:95], v[20:21]
	v_pk_mul_f32 v[20:21], v[46:47], v[14:15] op_sel_hi:[0,1]
	v_mul_f32_e32 v55, 0xbfb8aa3b, v53
	v_pk_mul_f32 v[102:103], v[102:103], v[22:23]
	v_exp_f32_e32 v20, v20
	v_pk_mul_f32 v[22:23], v[46:47], v[16:17] op_sel_hi:[0,1]
	v_pk_fma_f32 v[94:95], v[44:45], v[116:117], v[94:95] op_sel_hi:[0,1,1]
	v_exp_f32_e32 v21, v21
	v_pk_mul_f32 v[48:49], v[94:95], v[132:133]
	v_pk_mul_f32 v[88:89], v[88:89], v[24:25]
	v_exp_f32_e32 v22, v22
	v_pk_mul_f32 v[24:25], v[46:47], v[10:11] op_sel_hi:[0,1]
	v_pk_fma_f32 v[102:103], v[44:45], v[118:119], v[102:103] op_sel_hi:[0,1,1]
	v_exp_f32_e32 v23, v23
	v_pk_fma_f32 v[48:49], v[102:103], v[134:135], v[48:49]
	v_exp_f32_e32 v55, v55
	v_pk_mul_f32 v[96:97], v[96:97], v[26:27]
	v_exp_f32_e32 v24, v24
	v_pk_mul_f32 v[26:27], v[46:47], v[12:13] op_sel_hi:[0,1]
	v_pk_fma_f32 v[88:89], v[44:45], v[120:121], v[88:89] op_sel_hi:[0,1,1]
	v_exp_f32_e32 v25, v25
	v_pk_fma_f32 v[48:49], v[88:89], v[136:137], v[48:49]
	v_pk_mul_f32 v[90:91], v[90:91], v[28:29]
	v_exp_f32_e32 v26, v26
	v_pk_mul_f32 v[28:29], v[46:47], v[6:7] op_sel_hi:[0,1]
	v_pk_fma_f32 v[96:97], v[44:45], v[122:123], v[96:97] op_sel_hi:[0,1,1]
	v_exp_f32_e32 v27, v27
	v_pk_fma_f32 v[48:49], v[96:97], v[138:139], v[48:49]
	v_add_f32_e32 v55, 1.0, v55
	v_pk_mul_f32 v[92:93], v[92:93], v[30:31]
	v_exp_f32_e32 v28, v28
	v_pk_mul_f32 v[30:31], v[46:47], v[8:9] op_sel_hi:[0,1]
	v_pk_fma_f32 v[90:91], v[44:45], v[124:125], v[90:91] op_sel_hi:[0,1,1]
	v_exp_f32_e32 v29, v29
	v_pk_fma_f32 v[48:49], v[90:91], v[140:141], v[48:49]
	v_pk_mul_f32 v[98:99], v[98:99], v[32:33]
	v_exp_f32_e32 v30, v30
	v_pk_mul_f32 v[32:33], v[46:47], v[2:3] op_sel_hi:[0,1]
	v_pk_fma_f32 v[92:93], v[44:45], v[126:127], v[92:93] op_sel_hi:[0,1,1]
	v_exp_f32_e32 v31, v31
	v_pk_fma_f32 v[48:49], v[92:93], v[142:143], v[48:49]
	v_rcp_f32_e32 v55, v55
	v_pk_mul_f32 v[100:101], v[100:101], v[34:35]
	v_exp_f32_e32 v32, v32
	v_pk_mul_f32 v[34:35], v[46:47], v[4:5] op_sel_hi:[0,1]
	v_pk_fma_f32 v[98:99], v[44:45], v[128:129], v[98:99] op_sel_hi:[0,1,1]
	v_exp_f32_e32 v33, v33
	v_pk_fma_f32 v[48:49], v[98:99], v[144:145], v[48:49]
	v_exp_f32_e32 v34, v34
	v_pk_fma_f32 v[100:101], v[44:45], v[130:131], v[100:101] op_sel_hi:[0,1,1]
	v_exp_f32_e32 v35, v35
	v_pk_fma_f32 v[48:49], v[100:101], v[146:147], v[48:49]
	v_add_f32_e32 v54, v48, v49
	v_fma_mix_f32 v54, v87, v190, v54 op_sel:[0,1,0] op_sel_hi:[0,1,0]
	v_mul_f32_e32 v54, v54, v53
	v_fma_mix_f32 v44, v191, v191, 0 op_sel:[0,1,0] op_sel_hi:[1,1,0]
	v_fma_mixlo_f16 v56, v54, v55, 0
	ds_write_b16 v19, v56
	v_add_u32_e32 v19, 0x210, v19
	s_waitcnt lgkmcnt(1)
	ds_read_b128 v[116:119], v57 offset:768
	ds_read_b128 v[120:123], v57 offset:784
	ds_read_b128 v[124:127], v57 offset:800
	ds_read_b128 v[128:131], v57 offset:816
	ds_read_b128 v[132:135], v57 offset:4864
	ds_read_b128 v[136:139], v57 offset:4880
	ds_read_b128 v[140:143], v57 offset:4896
	ds_read_b128 v[144:147], v57 offset:4912
	s_waitcnt vmcnt(2)
	v_cvt_f32_f16_e32 v46, v192
	v_cvt_f32_f16_e32 v53, v52
	ds_read_u16 v52, v19 offset:528
	v_pk_mul_f32 v[94:95], v[94:95], v[20:21]
	v_pk_mul_f32 v[20:21], v[46:47], v[14:15] op_sel_hi:[0,1]
	v_mul_f32_e32 v55, 0xbfb8aa3b, v53
	v_pk_mul_f32 v[102:103], v[102:103], v[22:23]
	v_exp_f32_e32 v20, v20
	v_pk_mul_f32 v[22:23], v[46:47], v[16:17] op_sel_hi:[0,1]
	v_pk_fma_f32 v[94:95], v[44:45], v[196:197], v[94:95] op_sel_hi:[0,1,1]
	v_exp_f32_e32 v21, v21
	v_pk_mul_f32 v[48:49], v[94:95], v[212:213]
	v_pk_mul_f32 v[88:89], v[88:89], v[24:25]
	v_exp_f32_e32 v22, v22
	v_pk_mul_f32 v[24:25], v[46:47], v[10:11] op_sel_hi:[0,1]
	v_pk_fma_f32 v[102:103], v[44:45], v[198:199], v[102:103] op_sel_hi:[0,1,1]
	v_exp_f32_e32 v23, v23
	v_pk_fma_f32 v[48:49], v[102:103], v[214:215], v[48:49]
	v_exp_f32_e32 v55, v55
	v_pk_mul_f32 v[96:97], v[96:97], v[26:27]
	v_exp_f32_e32 v24, v24
	v_pk_mul_f32 v[26:27], v[46:47], v[12:13] op_sel_hi:[0,1]
	v_pk_fma_f32 v[88:89], v[44:45], v[200:201], v[88:89] op_sel_hi:[0,1,1]
	v_exp_f32_e32 v25, v25
	v_pk_fma_f32 v[48:49], v[88:89], v[216:217], v[48:49]
	v_pk_mul_f32 v[90:91], v[90:91], v[28:29]
	v_exp_f32_e32 v26, v26
	v_pk_mul_f32 v[28:29], v[46:47], v[6:7] op_sel_hi:[0,1]
	v_pk_fma_f32 v[96:97], v[44:45], v[202:203], v[96:97] op_sel_hi:[0,1,1]
	v_exp_f32_e32 v27, v27
	v_pk_fma_f32 v[48:49], v[96:97], v[218:219], v[48:49]
	v_add_f32_e32 v55, 1.0, v55
	v_pk_mul_f32 v[92:93], v[92:93], v[30:31]
	v_exp_f32_e32 v28, v28
	v_pk_mul_f32 v[30:31], v[46:47], v[8:9] op_sel_hi:[0,1]
	v_pk_fma_f32 v[90:91], v[44:45], v[204:205], v[90:91] op_sel_hi:[0,1,1]
	v_exp_f32_e32 v29, v29
	v_pk_fma_f32 v[48:49], v[90:91], v[220:221], v[48:49]
	v_pk_mul_f32 v[98:99], v[98:99], v[32:33]
	v_exp_f32_e32 v30, v30
	v_pk_mul_f32 v[32:33], v[46:47], v[2:3] op_sel_hi:[0,1]
	v_pk_fma_f32 v[92:93], v[44:45], v[206:207], v[92:93] op_sel_hi:[0,1,1]
	v_exp_f32_e32 v31, v31
	v_pk_fma_f32 v[48:49], v[92:93], v[222:223], v[48:49]
	v_rcp_f32_e32 v55, v55
	v_pk_mul_f32 v[100:101], v[100:101], v[34:35]
	v_exp_f32_e32 v32, v32
	v_pk_mul_f32 v[34:35], v[46:47], v[4:5] op_sel_hi:[0,1]
	v_pk_fma_f32 v[98:99], v[44:45], v[208:209], v[98:99] op_sel_hi:[0,1,1]
	v_exp_f32_e32 v33, v33
	v_pk_fma_f32 v[48:49], v[98:99], v[224:225], v[48:49]
	v_exp_f32_e32 v34, v34
	v_pk_fma_f32 v[100:101], v[44:45], v[210:211], v[100:101] op_sel_hi:[0,1,1]
	v_exp_f32_e32 v35, v35
	v_pk_fma_f32 v[48:49], v[100:101], v[226:227], v[48:49]
	v_add_f32_e32 v54, v48, v49
	v_fma_mix_f32 v54, v87, v191, v54 op_sel:[0,1,0] op_sel_hi:[0,1,0]
	v_mul_f32_e32 v54, v54, v53
	v_fma_mix_f32 v44, v192, v192, 0 op_sel:[0,1,0] op_sel_hi:[1,1,0]
	global_load_dwordx4 v[188:191], v[50:51], off offset:-4096
	v_fma_mixlo_f16 v56, v54, v55, 0
	ds_write_b16 v19, v56
	v_add_u32_e32 v19, 0x210, v19
	s_waitcnt lgkmcnt(1)
	ds_read_b128 v[196:199], v57 offset:832
	ds_read_b128 v[200:203], v57 offset:848
	ds_read_b128 v[204:207], v57 offset:864
	ds_read_b128 v[208:211], v57 offset:880
	ds_read_b128 v[212:215], v57 offset:4928
	ds_read_b128 v[216:219], v57 offset:4944
	ds_read_b128 v[220:223], v57 offset:4960
	ds_read_b128 v[224:227], v57 offset:4976
	v_cvt_f32_f16_e32 v46, v193
	v_cvt_f32_f16_e32 v53, v52
	ds_read_u16 v52, v19 offset:528
	v_pk_mul_f32 v[94:95], v[94:95], v[20:21]
	v_pk_mul_f32 v[20:21], v[46:47], v[14:15] op_sel_hi:[0,1]
	v_mul_f32_e32 v55, 0xbfb8aa3b, v53
	v_pk_mul_f32 v[102:103], v[102:103], v[22:23]
	v_exp_f32_e32 v20, v20
	v_pk_mul_f32 v[22:23], v[46:47], v[16:17] op_sel_hi:[0,1]
	v_pk_fma_f32 v[94:95], v[44:45], v[116:117], v[94:95] op_sel_hi:[0,1,1]
	v_exp_f32_e32 v21, v21
	v_pk_mul_f32 v[48:49], v[94:95], v[132:133]
	v_pk_mul_f32 v[88:89], v[88:89], v[24:25]
	v_exp_f32_e32 v22, v22
	v_pk_mul_f32 v[24:25], v[46:47], v[10:11] op_sel_hi:[0,1]
	v_pk_fma_f32 v[102:103], v[44:45], v[118:119], v[102:103] op_sel_hi:[0,1,1]
	v_exp_f32_e32 v23, v23
	v_pk_fma_f32 v[48:49], v[102:103], v[134:135], v[48:49]
	v_exp_f32_e32 v55, v55
	v_pk_mul_f32 v[96:97], v[96:97], v[26:27]
	v_exp_f32_e32 v24, v24
	v_pk_mul_f32 v[26:27], v[46:47], v[12:13] op_sel_hi:[0,1]
	v_pk_fma_f32 v[88:89], v[44:45], v[120:121], v[88:89] op_sel_hi:[0,1,1]
	v_exp_f32_e32 v25, v25
	v_pk_fma_f32 v[48:49], v[88:89], v[136:137], v[48:49]
	v_pk_mul_f32 v[90:91], v[90:91], v[28:29]
	v_exp_f32_e32 v26, v26
	v_pk_mul_f32 v[28:29], v[46:47], v[6:7] op_sel_hi:[0,1]
	v_pk_fma_f32 v[96:97], v[44:45], v[122:123], v[96:97] op_sel_hi:[0,1,1]
	v_exp_f32_e32 v27, v27
	v_pk_fma_f32 v[48:49], v[96:97], v[138:139], v[48:49]
	v_add_f32_e32 v55, 1.0, v55
	v_pk_mul_f32 v[92:93], v[92:93], v[30:31]
	v_exp_f32_e32 v28, v28
	v_pk_mul_f32 v[30:31], v[46:47], v[8:9] op_sel_hi:[0,1]
	v_pk_fma_f32 v[90:91], v[44:45], v[124:125], v[90:91] op_sel_hi:[0,1,1]
	v_exp_f32_e32 v29, v29
	v_pk_fma_f32 v[48:49], v[90:91], v[140:141], v[48:49]
	v_pk_mul_f32 v[98:99], v[98:99], v[32:33]
	v_exp_f32_e32 v30, v30
	v_pk_mul_f32 v[32:33], v[46:47], v[2:3] op_sel_hi:[0,1]
	v_pk_fma_f32 v[92:93], v[44:45], v[126:127], v[92:93] op_sel_hi:[0,1,1]
	v_exp_f32_e32 v31, v31
	v_pk_fma_f32 v[48:49], v[92:93], v[142:143], v[48:49]
	v_rcp_f32_e32 v55, v55
	v_pk_mul_f32 v[100:101], v[100:101], v[34:35]
	v_exp_f32_e32 v32, v32
	v_pk_mul_f32 v[34:35], v[46:47], v[4:5] op_sel_hi:[0,1]
	v_pk_fma_f32 v[98:99], v[44:45], v[128:129], v[98:99] op_sel_hi:[0,1,1]
	v_exp_f32_e32 v33, v33
	v_pk_fma_f32 v[48:49], v[98:99], v[144:145], v[48:49]
	v_exp_f32_e32 v34, v34
	v_pk_fma_f32 v[100:101], v[44:45], v[130:131], v[100:101] op_sel_hi:[0,1,1]
	v_exp_f32_e32 v35, v35
	v_pk_fma_f32 v[48:49], v[100:101], v[146:147], v[48:49]
	v_add_f32_e32 v54, v48, v49
	v_fma_mix_f32 v54, v87, v192, v54 op_sel:[0,1,0] op_sel_hi:[0,1,0]
	v_mul_f32_e32 v54, v54, v53
	v_fma_mix_f32 v44, v193, v193, 0 op_sel:[0,1,0] op_sel_hi:[1,1,0]
	v_fma_mixlo_f16 v56, v54, v55, 0
	ds_write_b16 v19, v56
	v_add_u32_e32 v19, 0x210, v19
	s_waitcnt lgkmcnt(1)
	ds_read_b128 v[116:119], v57 offset:896
	ds_read_b128 v[120:123], v57 offset:912
	ds_read_b128 v[124:127], v57 offset:928
	ds_read_b128 v[128:131], v57 offset:944
	ds_read_b128 v[132:135], v57 offset:4992
	ds_read_b128 v[136:139], v57 offset:5008
	ds_read_b128 v[140:143], v57 offset:5024
	ds_read_b128 v[144:147], v57 offset:5040
	v_cvt_f32_f16_e32 v46, v194
	v_cvt_f32_f16_e32 v53, v52
	ds_read_u16 v52, v19 offset:528
	v_pk_mul_f32 v[94:95], v[94:95], v[20:21]
	v_pk_mul_f32 v[20:21], v[46:47], v[14:15] op_sel_hi:[0,1]
	v_mul_f32_e32 v55, 0xbfb8aa3b, v53
	v_pk_mul_f32 v[102:103], v[102:103], v[22:23]
	v_exp_f32_e32 v20, v20
	v_pk_mul_f32 v[22:23], v[46:47], v[16:17] op_sel_hi:[0,1]
	v_pk_fma_f32 v[94:95], v[44:45], v[196:197], v[94:95] op_sel_hi:[0,1,1]
	v_exp_f32_e32 v21, v21
	v_pk_mul_f32 v[48:49], v[94:95], v[212:213]
	v_pk_mul_f32 v[88:89], v[88:89], v[24:25]
	v_exp_f32_e32 v22, v22
	v_pk_mul_f32 v[24:25], v[46:47], v[10:11] op_sel_hi:[0,1]
	v_pk_fma_f32 v[102:103], v[44:45], v[198:199], v[102:103] op_sel_hi:[0,1,1]
	v_exp_f32_e32 v23, v23
	v_pk_fma_f32 v[48:49], v[102:103], v[214:215], v[48:49]
	v_exp_f32_e32 v55, v55
	v_pk_mul_f32 v[96:97], v[96:97], v[26:27]
	v_exp_f32_e32 v24, v24
	v_pk_mul_f32 v[26:27], v[46:47], v[12:13] op_sel_hi:[0,1]
	v_pk_fma_f32 v[88:89], v[44:45], v[200:201], v[88:89] op_sel_hi:[0,1,1]
	v_exp_f32_e32 v25, v25
	v_pk_fma_f32 v[48:49], v[88:89], v[216:217], v[48:49]
	v_pk_mul_f32 v[90:91], v[90:91], v[28:29]
	v_exp_f32_e32 v26, v26
	v_pk_mul_f32 v[28:29], v[46:47], v[6:7] op_sel_hi:[0,1]
	v_pk_fma_f32 v[96:97], v[44:45], v[202:203], v[96:97] op_sel_hi:[0,1,1]
	v_exp_f32_e32 v27, v27
	v_pk_fma_f32 v[48:49], v[96:97], v[218:219], v[48:49]
	v_add_f32_e32 v55, 1.0, v55
	v_pk_mul_f32 v[92:93], v[92:93], v[30:31]
	v_exp_f32_e32 v28, v28
	v_pk_mul_f32 v[30:31], v[46:47], v[8:9] op_sel_hi:[0,1]
	v_pk_fma_f32 v[90:91], v[44:45], v[204:205], v[90:91] op_sel_hi:[0,1,1]
	v_exp_f32_e32 v29, v29
	v_pk_fma_f32 v[48:49], v[90:91], v[220:221], v[48:49]
	v_pk_mul_f32 v[98:99], v[98:99], v[32:33]
	v_exp_f32_e32 v30, v30
	v_pk_mul_f32 v[32:33], v[46:47], v[2:3] op_sel_hi:[0,1]
	v_pk_fma_f32 v[92:93], v[44:45], v[206:207], v[92:93] op_sel_hi:[0,1,1]
	v_exp_f32_e32 v31, v31
	v_pk_fma_f32 v[48:49], v[92:93], v[222:223], v[48:49]
	v_rcp_f32_e32 v55, v55
	v_pk_mul_f32 v[100:101], v[100:101], v[34:35]
	v_exp_f32_e32 v32, v32
	v_pk_mul_f32 v[34:35], v[46:47], v[4:5] op_sel_hi:[0,1]
	v_pk_fma_f32 v[98:99], v[44:45], v[208:209], v[98:99] op_sel_hi:[0,1,1]
	v_exp_f32_e32 v33, v33
	v_pk_fma_f32 v[48:49], v[98:99], v[224:225], v[48:49]
	v_exp_f32_e32 v34, v34
	v_pk_fma_f32 v[100:101], v[44:45], v[210:211], v[100:101] op_sel_hi:[0,1,1]
	v_exp_f32_e32 v35, v35
	v_pk_fma_f32 v[48:49], v[100:101], v[226:227], v[48:49]
	v_add_f32_e32 v54, v48, v49
	v_fma_mix_f32 v54, v87, v193, v54 op_sel:[0,1,0] op_sel_hi:[0,1,0]
	v_mul_f32_e32 v54, v54, v53
	v_fma_mix_f32 v44, v194, v194, 0 op_sel:[0,1,0] op_sel_hi:[1,1,0]
	v_fma_mixlo_f16 v56, v54, v55, 0
	ds_write_b16 v19, v56
	v_add_u32_e32 v19, 0x210, v19
	s_waitcnt lgkmcnt(1)
	ds_read_b128 v[196:199], v57 offset:960
	ds_read_b128 v[200:203], v57 offset:976
	ds_read_b128 v[204:207], v57 offset:992
	ds_read_b128 v[208:211], v57 offset:1008
	ds_read_b128 v[212:215], v57 offset:5056
	ds_read_b128 v[216:219], v57 offset:5072
	ds_read_b128 v[220:223], v57 offset:5088
	ds_read_b128 v[224:227], v57 offset:5104
	v_cvt_f32_f16_e32 v46, v195
	v_cvt_f32_f16_e32 v53, v52
	ds_read_u16 v52, v19 offset:528
	v_pk_mul_f32 v[94:95], v[94:95], v[20:21]
	v_pk_mul_f32 v[20:21], v[46:47], v[14:15] op_sel_hi:[0,1]
	v_mul_f32_e32 v55, 0xbfb8aa3b, v53
	v_pk_mul_f32 v[102:103], v[102:103], v[22:23]
	v_exp_f32_e32 v20, v20
	v_pk_mul_f32 v[22:23], v[46:47], v[16:17] op_sel_hi:[0,1]
	v_pk_fma_f32 v[94:95], v[44:45], v[116:117], v[94:95] op_sel_hi:[0,1,1]
	v_exp_f32_e32 v21, v21
	v_pk_mul_f32 v[48:49], v[94:95], v[132:133]
	v_pk_mul_f32 v[88:89], v[88:89], v[24:25]
	v_exp_f32_e32 v22, v22
	v_pk_mul_f32 v[24:25], v[46:47], v[10:11] op_sel_hi:[0,1]
	v_pk_fma_f32 v[102:103], v[44:45], v[118:119], v[102:103] op_sel_hi:[0,1,1]
	v_exp_f32_e32 v23, v23
	v_pk_fma_f32 v[48:49], v[102:103], v[134:135], v[48:49]
	v_exp_f32_e32 v55, v55
	v_pk_mul_f32 v[96:97], v[96:97], v[26:27]
	v_exp_f32_e32 v24, v24
	v_pk_mul_f32 v[26:27], v[46:47], v[12:13] op_sel_hi:[0,1]
	v_pk_fma_f32 v[88:89], v[44:45], v[120:121], v[88:89] op_sel_hi:[0,1,1]
	v_exp_f32_e32 v25, v25
	v_pk_fma_f32 v[48:49], v[88:89], v[136:137], v[48:49]
	v_pk_mul_f32 v[90:91], v[90:91], v[28:29]
	v_exp_f32_e32 v26, v26
	v_pk_mul_f32 v[28:29], v[46:47], v[6:7] op_sel_hi:[0,1]
	v_pk_fma_f32 v[96:97], v[44:45], v[122:123], v[96:97] op_sel_hi:[0,1,1]
	v_exp_f32_e32 v27, v27
	v_pk_fma_f32 v[48:49], v[96:97], v[138:139], v[48:49]
	v_add_f32_e32 v55, 1.0, v55
	v_pk_mul_f32 v[92:93], v[92:93], v[30:31]
	v_exp_f32_e32 v28, v28
	v_pk_mul_f32 v[30:31], v[46:47], v[8:9] op_sel_hi:[0,1]
	v_pk_fma_f32 v[90:91], v[44:45], v[124:125], v[90:91] op_sel_hi:[0,1,1]
	v_exp_f32_e32 v29, v29
	v_pk_fma_f32 v[48:49], v[90:91], v[140:141], v[48:49]
	v_pk_mul_f32 v[98:99], v[98:99], v[32:33]
	v_exp_f32_e32 v30, v30
	v_pk_mul_f32 v[32:33], v[46:47], v[2:3] op_sel_hi:[0,1]
	v_pk_fma_f32 v[92:93], v[44:45], v[126:127], v[92:93] op_sel_hi:[0,1,1]
	v_exp_f32_e32 v31, v31
	v_pk_fma_f32 v[48:49], v[92:93], v[142:143], v[48:49]
	v_rcp_f32_e32 v55, v55
	v_pk_mul_f32 v[100:101], v[100:101], v[34:35]
	v_exp_f32_e32 v32, v32
	v_pk_mul_f32 v[34:35], v[46:47], v[4:5] op_sel_hi:[0,1]
	v_pk_fma_f32 v[98:99], v[44:45], v[128:129], v[98:99] op_sel_hi:[0,1,1]
	v_exp_f32_e32 v33, v33
	v_pk_fma_f32 v[48:49], v[98:99], v[144:145], v[48:49]
	v_exp_f32_e32 v34, v34
	v_pk_fma_f32 v[100:101], v[44:45], v[130:131], v[100:101] op_sel_hi:[0,1,1]
	v_exp_f32_e32 v35, v35
	v_pk_fma_f32 v[48:49], v[100:101], v[146:147], v[48:49]
	v_add_f32_e32 v54, v48, v49
	v_fma_mix_f32 v54, v87, v194, v54 op_sel:[0,1,0] op_sel_hi:[0,1,0]
	v_mul_f32_e32 v54, v54, v53
	v_fma_mix_f32 v44, v195, v195, 0 op_sel:[0,1,0] op_sel_hi:[1,1,0]
	v_fma_mixlo_f16 v56, v54, v55, 0
	ds_write_b16 v19, v56
	v_add_u32_e32 v19, 0x210, v19
	s_waitcnt lgkmcnt(1)
	ds_read_b128 v[116:119], v57 offset:1024
	ds_read_b128 v[120:123], v57 offset:1040
	ds_read_b128 v[124:127], v57 offset:1056
	ds_read_b128 v[128:131], v57 offset:1072
	ds_read_b128 v[132:135], v57 offset:5120
	ds_read_b128 v[136:139], v57 offset:5136
	ds_read_b128 v[140:143], v57 offset:5152
	ds_read_b128 v[144:147], v57 offset:5168
	s_waitcnt vmcnt(2)
	v_cvt_f32_f16_e32 v46, v180
	v_cvt_f32_f16_e32 v53, v52
	ds_read_u16 v52, v19 offset:528
	v_pk_mul_f32 v[94:95], v[94:95], v[20:21]
	v_pk_mul_f32 v[20:21], v[46:47], v[14:15] op_sel_hi:[0,1]
	v_mul_f32_e32 v55, 0xbfb8aa3b, v53
	v_pk_mul_f32 v[102:103], v[102:103], v[22:23]
	v_exp_f32_e32 v20, v20
	v_pk_mul_f32 v[22:23], v[46:47], v[16:17] op_sel_hi:[0,1]
	v_pk_fma_f32 v[94:95], v[44:45], v[196:197], v[94:95] op_sel_hi:[0,1,1]
	v_exp_f32_e32 v21, v21
	v_pk_mul_f32 v[48:49], v[94:95], v[212:213]
	v_pk_mul_f32 v[88:89], v[88:89], v[24:25]
	v_exp_f32_e32 v22, v22
	v_pk_mul_f32 v[24:25], v[46:47], v[10:11] op_sel_hi:[0,1]
	v_pk_fma_f32 v[102:103], v[44:45], v[198:199], v[102:103] op_sel_hi:[0,1,1]
	v_exp_f32_e32 v23, v23
	v_pk_fma_f32 v[48:49], v[102:103], v[214:215], v[48:49]
	v_exp_f32_e32 v55, v55
	v_pk_mul_f32 v[96:97], v[96:97], v[26:27]
	v_exp_f32_e32 v24, v24
	v_pk_mul_f32 v[26:27], v[46:47], v[12:13] op_sel_hi:[0,1]
	v_pk_fma_f32 v[88:89], v[44:45], v[200:201], v[88:89] op_sel_hi:[0,1,1]
	v_exp_f32_e32 v25, v25
	v_pk_fma_f32 v[48:49], v[88:89], v[216:217], v[48:49]
	v_pk_mul_f32 v[90:91], v[90:91], v[28:29]
	v_exp_f32_e32 v26, v26
	v_pk_mul_f32 v[28:29], v[46:47], v[6:7] op_sel_hi:[0,1]
	v_pk_fma_f32 v[96:97], v[44:45], v[202:203], v[96:97] op_sel_hi:[0,1,1]
	v_exp_f32_e32 v27, v27
	v_pk_fma_f32 v[48:49], v[96:97], v[218:219], v[48:49]
	v_add_f32_e32 v55, 1.0, v55
	v_pk_mul_f32 v[92:93], v[92:93], v[30:31]
	v_exp_f32_e32 v28, v28
	v_pk_mul_f32 v[30:31], v[46:47], v[8:9] op_sel_hi:[0,1]
	v_pk_fma_f32 v[90:91], v[44:45], v[204:205], v[90:91] op_sel_hi:[0,1,1]
	v_exp_f32_e32 v29, v29
	v_pk_fma_f32 v[48:49], v[90:91], v[220:221], v[48:49]
	v_pk_mul_f32 v[98:99], v[98:99], v[32:33]
	v_exp_f32_e32 v30, v30
	v_pk_mul_f32 v[32:33], v[46:47], v[2:3] op_sel_hi:[0,1]
	v_pk_fma_f32 v[92:93], v[44:45], v[206:207], v[92:93] op_sel_hi:[0,1,1]
	v_exp_f32_e32 v31, v31
	v_pk_fma_f32 v[48:49], v[92:93], v[222:223], v[48:49]
	v_rcp_f32_e32 v55, v55
	v_pk_mul_f32 v[100:101], v[100:101], v[34:35]
	v_exp_f32_e32 v32, v32
	v_pk_mul_f32 v[34:35], v[46:47], v[4:5] op_sel_hi:[0,1]
	v_pk_fma_f32 v[98:99], v[44:45], v[208:209], v[98:99] op_sel_hi:[0,1,1]
	v_exp_f32_e32 v33, v33
	v_pk_fma_f32 v[48:49], v[98:99], v[224:225], v[48:49]
	v_exp_f32_e32 v34, v34
	v_pk_fma_f32 v[100:101], v[44:45], v[210:211], v[100:101] op_sel_hi:[0,1,1]
	v_exp_f32_e32 v35, v35
	v_pk_fma_f32 v[48:49], v[100:101], v[226:227], v[48:49]
	v_add_f32_e32 v54, v48, v49
	v_fma_mix_f32 v54, v87, v195, v54 op_sel:[0,1,0] op_sel_hi:[0,1,0]
	v_mul_f32_e32 v54, v54, v53
	v_fma_mix_f32 v44, v180, v180, 0 op_sel:[0,1,0] op_sel_hi:[1,1,0]
	global_load_dwordx4 v[192:195], v[50:51], off
	v_fma_mixlo_f16 v56, v54, v55, 0
	ds_write_b16 v19, v56
	v_add_u32_e32 v19, 0x210, v19
	v_add_u32_e32 v57, 0x400, v57
	v_lshl_add_u64 v[58:59], v[58:59], 0, s[10:11]
	v_lshl_add_u64 v[50:51], v[50:51], 0, s[10:11]
	s_add_i32 s12, s12, 1
	s_cmp_eq_u32 s12, 4
	s_cbranch_scc0 .Lsc3_loop
	global_load_dwordx4 v[18:21], v86, s[4:5]
	global_load_dwordx4 v[34:37], v86, s[4:5] offset:1024
	global_load_dwordx4 v[38:41], v86, s[4:5] offset:2048
	global_load_dwordx4 v[42:45], v86, s[4:5] offset:3072
	v_mov_b32_e32 v87, 0
	v_and_b32_e32 v112, 31, v0
	v_lshl_add_u64 v[2:3], s[4:5], 0, v[86:87]
	v_and_b32_e32 v5, 8, v114
	v_mul_u32_u24_e32 v6, 0x210, v112
	v_add_co_u32_e32 v4, vcc, 0x1000, v2
	v_lshl_add_u32 v113, v5, 1, v6
	s_nop 0
	v_addc_co_u32_e32 v5, vcc, 0, v3, vcc
	global_load_dwordx4 v[46:49], v[4:5], off
	global_load_dwordx4 v[50:53], v[4:5], off offset:1024
	global_load_dwordx4 v[54:57], v[4:5], off offset:2048
	global_load_dwordx4 v[58:61], v[4:5], off offset:3072
	v_add_co_u32_e32 v6, vcc, 0x2000, v2
	s_movk_i32 s4, 0x110
	s_nop 0
	v_addc_co_u32_e32 v7, vcc, 0, v3, vcc
	global_load_dwordx4 v[62:65], v[6:7], off
	global_load_dwordx4 v[66:69], v[6:7], off offset:1024
	global_load_dwordx4 v[70:73], v[6:7], off offset:2048
	global_load_dwordx4 v[74:77], v[6:7], off offset:3072
	v_add_co_u32_e32 v2, vcc, 0x3000, v2
	s_lshl_b32 s2, s2, 12
	s_nop 0
	v_addc_co_u32_e32 v3, vcc, 0, v3, vcc
	global_load_dwordx4 v[78:81], v[2:3], off
	global_load_dwordx4 v[86:89], v[2:3], off offset:1024
	global_load_dwordx4 v[90:93], v[2:3], off offset:2048
	global_load_dwordx4 v[94:97], v[2:3], off offset:3072
	s_waitcnt lgkmcnt(0)
	s_barrier
	ds_read_b128 v[2:5], v113
	ds_read_b128 v[98:101], v113 offset:32
	ds_read_b128 v[22:25], v113 offset:16896
	ds_read_b128 v[102:105], v113 offset:16928
	s_and_b32 s2, s2, 0xf000
	s_add_u32 s0, s0, s2
	s_addc_u32 s1, s1, 0
	s_add_u32 s2, s6, s26
	s_addc_u32 s3, s7, 0
	v_cmp_eq_u32_e32 vcc, 0, v109
	s_waitcnt vmcnt(15) lgkmcnt(3)
	v_mfma_f32_32x32x16_f16 v[2:17], v[18:21], v[2:5], 0
	s_waitcnt lgkmcnt(1)
	v_mfma_f32_32x32x16_f16 v[18:33], v[18:21], v[22:25], 0
	s_waitcnt vmcnt(14)
	v_mfma_f32_32x32x16_f16 v[2:17], v[34:37], v[98:101], v[2:17]
	s_waitcnt lgkmcnt(0)
	v_mfma_f32_32x32x16_f16 v[18:33], v[34:37], v[102:105], v[18:33]
	ds_read_b128 v[34:37], v113 offset:64
	ds_read_b128 v[98:101], v113 offset:96
	s_waitcnt vmcnt(13) lgkmcnt(1)
	v_mfma_f32_32x32x16_f16 v[2:17], v[38:41], v[34:37], v[2:17]
	ds_read_b128 v[34:37], v113 offset:16960
	ds_read_b128 v[102:105], v113 offset:16992
	s_waitcnt lgkmcnt(1)
	v_mfma_f32_32x32x16_f16 v[18:33], v[38:41], v[34:37], v[18:33]
	ds_read_b128 v[34:37], v113 offset:128
	ds_read_b128 v[38:41], v113 offset:160
	s_waitcnt vmcnt(12)
	v_mfma_f32_32x32x16_f16 v[2:17], v[42:45], v[98:101], v[2:17]
	s_waitcnt lgkmcnt(2)
	v_mfma_f32_32x32x16_f16 v[18:33], v[42:45], v[102:105], v[18:33]
	s_waitcnt vmcnt(11) lgkmcnt(1)
	v_mfma_f32_32x32x16_f16 v[2:17], v[46:49], v[34:37], v[2:17]
	ds_read_b128 v[34:37], v113 offset:17024
	ds_read_b128 v[42:45], v113 offset:17056
	s_waitcnt lgkmcnt(1)
	v_mfma_f32_32x32x16_f16 v[18:33], v[46:49], v[34:37], v[18:33]
	s_waitcnt vmcnt(10)
	v_mfma_f32_32x32x16_f16 v[2:17], v[50:53], v[38:41], v[2:17]
	ds_read_b128 v[34:37], v113 offset:192
	ds_read_b128 v[38:41], v113 offset:224
	s_waitcnt lgkmcnt(2)
	v_mfma_f32_32x32x16_f16 v[18:33], v[50:53], v[42:45], v[18:33]
	s_waitcnt vmcnt(9) lgkmcnt(1)
	v_mfma_f32_32x32x16_f16 v[2:17], v[54:57], v[34:37], v[2:17]
	ds_read_b128 v[34:37], v113 offset:17088
	ds_read_b128 v[42:45], v113 offset:17120
	s_waitcnt lgkmcnt(1)
	v_mfma_f32_32x32x16_f16 v[18:33], v[54:57], v[34:37], v[18:33]
	s_waitcnt vmcnt(8)
	v_mfma_f32_32x32x16_f16 v[2:17], v[58:61], v[38:41], v[2:17]
	ds_read_b128 v[34:37], v113 offset:256
	ds_read_b128 v[38:41], v113 offset:288
	s_waitcnt lgkmcnt(2)
	v_mfma_f32_32x32x16_f16 v[18:33], v[58:61], v[42:45], v[18:33]
	s_waitcnt vmcnt(7) lgkmcnt(1)
	v_mfma_f32_32x32x16_f16 v[2:17], v[62:65], v[34:37], v[2:17]
	ds_read_b128 v[34:37], v113 offset:17152
	ds_read_b128 v[42:45], v113 offset:17184
	s_waitcnt lgkmcnt(1)
	v_mfma_f32_32x32x16_f16 v[18:33], v[62:65], v[34:37], v[18:33]
	s_waitcnt vmcnt(6)
	v_mfma_f32_32x32x16_f16 v[2:17], v[66:69], v[38:41], v[2:17]
	ds_read_b128 v[34:37], v113 offset:320
	ds_read_b128 v[38:41], v113 offset:352
	s_waitcnt lgkmcnt(2)
	v_mfma_f32_32x32x16_f16 v[18:33], v[66:69], v[42:45], v[18:33]
	s_waitcnt vmcnt(5) lgkmcnt(1)
	v_mfma_f32_32x32x16_f16 v[2:17], v[70:73], v[34:37], v[2:17]
	ds_read_b128 v[34:37], v113 offset:17216
	ds_read_b128 v[42:45], v113 offset:17248
	s_waitcnt lgkmcnt(1)
	v_mfma_f32_32x32x16_f16 v[18:33], v[70:73], v[34:37], v[18:33]
	s_waitcnt vmcnt(4)
	v_mfma_f32_32x32x16_f16 v[2:17], v[74:77], v[38:41], v[2:17]
	ds_read_b128 v[34:37], v113 offset:384
	ds_read_b128 v[38:41], v113 offset:416
	s_waitcnt lgkmcnt(2)
	v_mfma_f32_32x32x16_f16 v[18:33], v[74:77], v[42:45], v[18:33]
	s_waitcnt vmcnt(3) lgkmcnt(1)
	v_mfma_f32_32x32x16_f16 v[2:17], v[78:81], v[34:37], v[2:17]
	ds_read_b128 v[34:37], v113 offset:17280
	ds_read_b128 v[42:45], v113 offset:17312
	s_waitcnt lgkmcnt(1)
	v_mfma_f32_32x32x16_f16 v[18:33], v[78:81], v[34:37], v[18:33]
	s_waitcnt vmcnt(2)
	v_mfma_f32_32x32x16_f16 v[2:17], v[86:89], v[38:41], v[2:17]
	ds_read_b128 v[34:37], v113 offset:448
	ds_read_b128 v[38:41], v113 offset:480
	s_waitcnt lgkmcnt(2)
	v_mfma_f32_32x32x16_f16 v[18:33], v[86:89], v[42:45], v[18:33]
	s_waitcnt vmcnt(1) lgkmcnt(1)
	v_mfma_f32_32x32x16_f16 v[2:17], v[90:93], v[34:37], v[2:17]
	ds_read_b128 v[34:37], v113 offset:17344
	ds_read_b128 v[42:45], v113 offset:17376
	s_waitcnt lgkmcnt(0)
	s_barrier
	v_mfma_f32_32x32x16_f16 v[18:33], v[90:93], v[34:37], v[18:33]
	v_lshrrev_b32_e32 v34, 3, v0
	v_and_b32_e32 v34, 4, v34
	v_lshl_or_b32 v34, v107, 5, v34
	v_mul_u32_u24_e32 v34, 0x110, v34
	v_lshl_add_u32 v34, v112, 2, v34
	s_waitcnt vmcnt(0)
	v_mfma_f32_32x32x16_f16 v[2:17], v[94:97], v[38:41], v[2:17]
	v_mfma_f32_32x32x16_f16 v[18:33], v[94:97], v[42:45], v[18:33]
	s_nop 11
	ds_write2_b32 v34, v2, v18 offset1:32
	ds_write2_b32 v34, v3, v19 offset0:68 offset1:100
	ds_write2_b32 v34, v4, v20 offset0:136 offset1:168
	ds_write2_b32 v34, v5, v21 offset0:204 offset1:236
	v_add_u32_e32 v2, 0x800, v34
	ds_write2_b32 v2, v6, v22 offset0:32 offset1:64
	ds_write2_b32 v2, v7, v23 offset0:100 offset1:132
	ds_write2_b32 v2, v8, v24 offset0:168 offset1:200
	v_add_u32_e32 v2, 0xa00, v34
	ds_write2_b32 v2, v9, v25 offset0:108 offset1:140
	v_add_u32_e32 v2, 0x1000, v34
	ds_write2_b32 v2, v10, v26 offset0:64 offset1:96
	ds_write2_b32 v2, v11, v27 offset0:132 offset1:164
	ds_write2_b32 v2, v12, v28 offset0:200 offset1:232
	v_add_u32_e32 v2, 0x1400, v34
	ds_write2_b32 v2, v13, v29 offset0:12 offset1:44
	v_add_u32_e32 v2, 0x1800, v34
	v_and_b32_e32 v5, 60, v84
	v_mov_b32_e32 v8, 0x8800
	ds_write2_b32 v2, v14, v30 offset0:96 offset1:128
	ds_write2_b32 v2, v15, v31 offset0:164 offset1:196
	v_add_u32_e32 v2, 0x1a00, v34
	v_lshlrev_b32_e32 v6, 2, v5
	v_lshl_or_b32 v8, v82, 1, v8
	ds_write2_b32 v2, v16, v32 offset0:104 offset1:136
	v_add_u32_e32 v2, 0x1c00, v34
	v_add_u32_e32 v7, v6, v111
	v_mad_u32_u24 v9, v5, s4, v8
	ds_write2_b32 v2, v17, v33 offset0:44 offset1:76
	s_waitcnt lgkmcnt(0)
	s_barrier
	ds_read_b128 v[10:13], v7
	ds_read_u16 v14, v9
	ds_read_u16 v15, v9 offset:272
	ds_read_u16 v16, v9 offset:544
	ds_read_u16 v9, v9 offset:816
	v_or_b32_e32 v2, s20, v5
	v_mul_u32_u24_e32 v7, 0x110, v5
	s_waitcnt lgkmcnt(3)
	v_cvt_f32_f16_e32 v5, v14
	s_waitcnt lgkmcnt(2)
	v_cvt_f32_f16_e32 v14, v15
	s_waitcnt lgkmcnt(1)
	v_cvt_f32_f16_e32 v15, v16
	s_waitcnt lgkmcnt(0)
	v_cvt_f32_f16_e32 v9, v9
	v_or_b32_e32 v4, s8, v82
	v_ashrrev_i32_e32 v3, 31, v2
	v_add_f32_e32 v16, v10, v5
	v_ashrrev_i32_e32 v5, 31, v4
	v_lshl_add_u64 v[2:3], v[2:3], 1, s[2:3]
	v_add_f32_e32 v14, v11, v14
	v_add_f32_e32 v15, v12, v15
	v_add_f32_e32 v9, v13, v9
	v_lshlrev_b64 v[12:13], 13, v[4:5]
	v_cvt_pk_f16_f32 v11, v15, v9
	v_cvt_pk_f16_f32 v10, v16, v14
	v_lshl_add_u64 v[12:13], v[2:3], 0, v[12:13]
	global_store_dwordx2 v[12:13], v[10:11], off sc1
	v_mul_f32_e32 v11, v14, v14
	v_add_f32_e32 v10, v16, v14
	v_fmac_f32_e32 v11, v16, v16
	v_add_f32_e32 v10, v15, v10
	v_fmac_f32_e32 v11, v15, v15
	v_add_f32_e32 v10, v9, v10
	v_fmac_f32_e32 v11, v9, v9
	s_nop 0
	v_add_f32_dpp v9, v10, v10 quad_perm:[1,0,3,2] row_mask:0xf bank_mask:0xf bound_ctrl:1
	v_add_f32_dpp v11, v11, v11 quad_perm:[1,0,3,2] row_mask:0xf bank_mask:0xf bound_ctrl:1
	s_nop 0
	v_add_f32_dpp v9, v9, v9 quad_perm:[2,3,0,1] row_mask:0xf bank_mask:0xf bound_ctrl:1
	v_add_f32_dpp v11, v11, v11 quad_perm:[2,3,0,1] row_mask:0xf bank_mask:0xf bound_ctrl:1
	s_nop 0
	v_add_f32_dpp v9, v9, v9 row_half_mirror row_mask:0xf bank_mask:0xf bound_ctrl:1
	v_add_f32_dpp v11, v11, v11 row_half_mirror row_mask:0xf bank_mask:0xf bound_ctrl:1
	s_nop 0
	v_mov_b32_dpp v10, v9 row_mirror row_mask:0xf bank_mask:0xf bound_ctrl:1
	v_mov_b32_dpp v12, v11 row_mirror row_mask:0xf bank_mask:0xf bound_ctrl:1
	s_and_saveexec_b64 s[2:3], vcc
	s_cbranch_execz .LBB3_4
	v_lshl_add_u64 v[4:5], v[4:5], 2, s[0:1]
	v_add_f32_e32 v9, v9, v10
	v_add_f32_e32 v11, v11, v12
	global_atomic_add_f32 v[4:5], v9, off
	global_atomic_add_f32 v[4:5], v11, off offset:2048
.LBB3_4:
	s_or_b64 exec, exec, s[2:3]
	v_add_u32_e32 v4, v6, v110
	v_lshl_add_u32 v5, v106, 1, v7
	ds_read_b128 v[10:13], v4
	ds_read_u16 v9, v5 offset:34816
	ds_read_u16 v14, v5 offset:35088
	ds_read_u16 v15, v5 offset:35360
	ds_read_u16 v5, v5 offset:35632
	v_or_b32_e32 v4, s8, v106
	s_waitcnt lgkmcnt(3)
	v_cvt_f32_f16_e32 v9, v9
	s_waitcnt lgkmcnt(2)
	v_cvt_f32_f16_e32 v14, v14
	s_waitcnt lgkmcnt(1)
	v_cvt_f32_f16_e32 v15, v15
	s_waitcnt lgkmcnt(0)
	v_cvt_f32_f16_e32 v5, v5
	v_add_f32_e32 v9, v10, v9
	v_add_f32_e32 v14, v11, v14
	v_add_f32_e32 v15, v12, v15
	v_add_f32_e32 v16, v13, v5
	v_ashrrev_i32_e32 v5, 31, v4
	v_lshlrev_b64 v[12:13], 13, v[4:5]
	v_cvt_pk_f16_f32 v11, v15, v16
	v_cvt_pk_f16_f32 v10, v9, v14
	v_lshl_add_u64 v[12:13], v[2:3], 0, v[12:13]
	global_store_dwordx2 v[12:13], v[10:11], off sc1
	v_mul_f32_e32 v11, v14, v14
	v_add_f32_e32 v10, v9, v14
	v_fmac_f32_e32 v11, v9, v9
	v_add_f32_e32 v10, v15, v10
	v_fmac_f32_e32 v11, v15, v15
	v_add_f32_e32 v10, v16, v10
	v_fmac_f32_e32 v11, v16, v16
	s_nop 0
	v_add_f32_dpp v9, v10, v10 quad_perm:[1,0,3,2] row_mask:0xf bank_mask:0xf bound_ctrl:1
	v_add_f32_dpp v11, v11, v11 quad_perm:[1,0,3,2] row_mask:0xf bank_mask:0xf bound_ctrl:1
	s_nop 0
	v_add_f32_dpp v9, v9, v9 quad_perm:[2,3,0,1] row_mask:0xf bank_mask:0xf bound_ctrl:1
	v_add_f32_dpp v11, v11, v11 quad_perm:[2,3,0,1] row_mask:0xf bank_mask:0xf bound_ctrl:1
	s_nop 0
	v_add_f32_dpp v9, v9, v9 row_half_mirror row_mask:0xf bank_mask:0xf bound_ctrl:1
	v_add_f32_dpp v11, v11, v11 row_half_mirror row_mask:0xf bank_mask:0xf bound_ctrl:1
	s_nop 0
	v_mov_b32_dpp v10, v9 row_mirror row_mask:0xf bank_mask:0xf bound_ctrl:1
	v_mov_b32_dpp v12, v11 row_mirror row_mask:0xf bank_mask:0xf bound_ctrl:1
	s_and_saveexec_b64 s[2:3], vcc
	s_cbranch_execz .LBB3_6
	v_lshl_add_u64 v[4:5], v[4:5], 2, s[0:1]
	v_add_f32_e32 v9, v9, v10
	v_add_f32_e32 v11, v11, v12
	global_atomic_add_f32 v[4:5], v9, off
	global_atomic_add_f32 v[4:5], v11, off offset:2048
.LBB3_6:
	s_or_b64 exec, exec, s[2:3]
	v_add_u32_e32 v4, v6, v108
	v_lshl_add_u32 v5, v83, 1, v7
	ds_read_b128 v[10:13], v4
	ds_read_u16 v9, v5 offset:34816
	ds_read_u16 v14, v5 offset:35088
	ds_read_u16 v15, v5 offset:35360
	ds_read_u16 v5, v5 offset:35632
	v_or_b32_e32 v4, s8, v83
	s_waitcnt lgkmcnt(3)
	v_cvt_f32_f16_e32 v9, v9
	s_waitcnt lgkmcnt(2)
	v_cvt_f32_f16_e32 v14, v14
	s_waitcnt lgkmcnt(1)
	v_cvt_f32_f16_e32 v15, v15
	s_waitcnt lgkmcnt(0)
	v_cvt_f32_f16_e32 v5, v5
	v_add_f32_e32 v9, v10, v9
	v_add_f32_e32 v14, v11, v14
	v_add_f32_e32 v15, v12, v15
	v_add_f32_e32 v16, v13, v5
	v_ashrrev_i32_e32 v5, 31, v4
	v_lshlrev_b64 v[12:13], 13, v[4:5]
	v_cvt_pk_f16_f32 v11, v15, v16
	v_cvt_pk_f16_f32 v10, v9, v14
	v_lshl_add_u64 v[12:13], v[2:3], 0, v[12:13]
	global_store_dwordx2 v[12:13], v[10:11], off sc1
	v_mul_f32_e32 v11, v14, v14
	v_add_f32_e32 v10, v9, v14
	v_fmac_f32_e32 v11, v9, v9
	v_add_f32_e32 v10, v15, v10
	v_fmac_f32_e32 v11, v15, v15
	v_add_f32_e32 v10, v16, v10
	v_fmac_f32_e32 v11, v16, v16
	s_nop 0
	v_add_f32_dpp v9, v10, v10 quad_perm:[1,0,3,2] row_mask:0xf bank_mask:0xf bound_ctrl:1
	v_add_f32_dpp v11, v11, v11 quad_perm:[1,0,3,2] row_mask:0xf bank_mask:0xf bound_ctrl:1
	s_nop 0
	v_add_f32_dpp v9, v9, v9 quad_perm:[2,3,0,1] row_mask:0xf bank_mask:0xf bound_ctrl:1
	v_add_f32_dpp v11, v11, v11 quad_perm:[2,3,0,1] row_mask:0xf bank_mask:0xf bound_ctrl:1
	s_nop 0
	v_add_f32_dpp v9, v9, v9 row_half_mirror row_mask:0xf bank_mask:0xf bound_ctrl:1
	v_add_f32_dpp v11, v11, v11 row_half_mirror row_mask:0xf bank_mask:0xf bound_ctrl:1
	s_nop 0
	v_mov_b32_dpp v10, v9 row_mirror row_mask:0xf bank_mask:0xf bound_ctrl:1
	v_mov_b32_dpp v12, v11 row_mirror row_mask:0xf bank_mask:0xf bound_ctrl:1
	s_and_saveexec_b64 s[2:3], vcc
	s_cbranch_execz .LBB3_8
	v_lshl_add_u64 v[4:5], v[4:5], 2, s[0:1]
	v_add_f32_e32 v9, v9, v10
	v_add_f32_e32 v11, v11, v12
	global_atomic_add_f32 v[4:5], v9, off
	global_atomic_add_f32 v[4:5], v11, off offset:2048
.LBB3_8:
	s_or_b64 exec, exec, s[2:3]
	v_add_u32_e32 v4, v6, v85
	v_lshl_add_u32 v5, v1, 1, v7
	ds_read_b128 v[10:13], v4
	ds_read_u16 v9, v5 offset:34816
	ds_read_u16 v14, v5 offset:35088
	ds_read_u16 v15, v5 offset:35360
	ds_read_u16 v5, v5 offset:35632
	v_or_b32_e32 v4, s8, v1
	s_waitcnt lgkmcnt(3)
	v_cvt_f32_f16_e32 v1, v9
	s_waitcnt lgkmcnt(2)
	v_cvt_f32_f16_e32 v9, v14
	s_waitcnt lgkmcnt(1)
	v_cvt_f32_f16_e32 v14, v15
	s_waitcnt lgkmcnt(0)
	v_cvt_f32_f16_e32 v5, v5
	v_add_f32_e32 v1, v10, v1
	v_add_f32_e32 v9, v11, v9
	v_add_f32_e32 v14, v12, v14
	v_add_f32_e32 v15, v13, v5
	v_ashrrev_i32_e32 v5, 31, v4
	v_lshlrev_b64 v[12:13], 13, v[4:5]
	v_cvt_pk_f16_f32 v11, v14, v15
	v_cvt_pk_f16_f32 v10, v1, v9
	v_lshl_add_u64 v[12:13], v[2:3], 0, v[12:13]
	global_store_dwordx2 v[12:13], v[10:11], off sc1
	v_mul_f32_e32 v11, v9, v9
	v_add_f32_e32 v10, v1, v9
	v_fmac_f32_e32 v11, v1, v1
	v_add_f32_e32 v10, v14, v10
	v_fmac_f32_e32 v11, v14, v14
	v_add_f32_e32 v10, v15, v10
	v_fmac_f32_e32 v11, v15, v15
	s_nop 0
	v_add_f32_dpp v1, v10, v10 quad_perm:[1,0,3,2] row_mask:0xf bank_mask:0xf bound_ctrl:1
	v_add_f32_dpp v10, v11, v11 quad_perm:[1,0,3,2] row_mask:0xf bank_mask:0xf bound_ctrl:1
	s_nop 0
	v_add_f32_dpp v1, v1, v1 quad_perm:[2,3,0,1] row_mask:0xf bank_mask:0xf bound_ctrl:1
	v_add_f32_dpp v10, v10, v10 quad_perm:[2,3,0,1] row_mask:0xf bank_mask:0xf bound_ctrl:1
	s_nop 0
	v_add_f32_dpp v1, v1, v1 row_half_mirror row_mask:0xf bank_mask:0xf bound_ctrl:1
	v_add_f32_dpp v10, v10, v10 row_half_mirror row_mask:0xf bank_mask:0xf bound_ctrl:1
	s_nop 0
	v_mov_b32_dpp v9, v1 row_mirror row_mask:0xf bank_mask:0xf bound_ctrl:1
	v_mov_b32_dpp v11, v10 row_mirror row_mask:0xf bank_mask:0xf bound_ctrl:1
	s_and_saveexec_b64 s[2:3], vcc
	s_cbranch_execz .LBB3_10
	v_lshl_add_u64 v[4:5], v[4:5], 2, s[0:1]
	v_add_f32_e32 v1, v1, v9
	v_add_f32_e32 v10, v10, v11
	global_atomic_add_f32 v[4:5], v1, off
	global_atomic_add_f32 v[4:5], v10, off offset:2048
.LBB3_10:
	s_or_b64 exec, exec, s[2:3]
	v_or_b32_e32 v1, 64, v82
	v_mad_u32_u24 v4, v1, s4, v6
	v_add_u32_e32 v5, v8, v7
	ds_read_b128 v[8:11], v4
	ds_read_u16 v12, v5 offset:128
	ds_read_u16 v13, v5 offset:400
	ds_read_u16 v14, v5 offset:672
	ds_read_u16 v5, v5 offset:944
	v_or_b32_e32 v4, s8, v1
	s_waitcnt lgkmcnt(3)
	v_cvt_f32_f16_e32 v1, v12
	s_waitcnt lgkmcnt(2)
	v_cvt_f32_f16_e32 v12, v13
	s_waitcnt lgkmcnt(1)
	v_cvt_f32_f16_e32 v13, v14
	s_waitcnt lgkmcnt(0)
	v_cvt_f32_f16_e32 v5, v5
	v_add_f32_e32 v1, v8, v1
	v_add_f32_e32 v12, v9, v12
	v_add_f32_e32 v10, v10, v13
	v_add_f32_e32 v11, v11, v5
	v_ashrrev_i32_e32 v5, 31, v4
	v_lshlrev_b64 v[4:5], 13, v[4:5]
	v_cvt_pk_f16_f32 v9, v10, v11
	v_cvt_pk_f16_f32 v8, v1, v12
	v_lshl_add_u64 v[4:5], v[2:3], 0, v[4:5]
	global_store_dwordx2 v[4:5], v[8:9], off sc1
	v_mul_f32_e32 v5, v12, v12
	v_add_f32_e32 v4, v1, v12
	v_fmac_f32_e32 v5, v1, v1
	v_add_f32_e32 v4, v10, v4
	v_fmac_f32_e32 v5, v10, v10
	v_add_f32_e32 v4, v11, v4
	v_fmac_f32_e32 v5, v11, v11
	s_nop 0
	v_add_f32_dpp v1, v4, v4 quad_perm:[1,0,3,2] row_mask:0xf bank_mask:0xf bound_ctrl:1
	v_add_f32_dpp v5, v5, v5 quad_perm:[1,0,3,2] row_mask:0xf bank_mask:0xf bound_ctrl:1
	s_nop 0
	v_add_f32_dpp v1, v1, v1 quad_perm:[2,3,0,1] row_mask:0xf bank_mask:0xf bound_ctrl:1
	v_add_f32_dpp v5, v5, v5 quad_perm:[2,3,0,1] row_mask:0xf bank_mask:0xf bound_ctrl:1
	s_nop 0
	v_add_f32_dpp v1, v1, v1 row_half_mirror row_mask:0xf bank_mask:0xf bound_ctrl:1
	v_add_f32_dpp v5, v5, v5 row_half_mirror row_mask:0xf bank_mask:0xf bound_ctrl:1
	s_nop 0
	v_mov_b32_dpp v4, v1 row_mirror row_mask:0xf bank_mask:0xf bound_ctrl:1
	v_mov_b32_dpp v8, v5 row_mirror row_mask:0xf bank_mask:0xf bound_ctrl:1
	s_and_saveexec_b64 s[2:3], vcc
	s_cbranch_execz .LBB3_12
	v_mov_b32_e32 v83, 0
	v_lshl_add_u64 v[10:11], v[82:83], 0, s[8:9]
	v_lshl_add_u64 v[10:11], v[10:11], 2, s[0:1]
	v_add_f32_e32 v1, v1, v4
	v_add_f32_e32 v5, v5, v8
	global_atomic_add_f32 v[10:11], v1, off offset:256
	global_atomic_add_f32 v[10:11], v5, off offset:2304
.LBB3_12:
	s_or_b64 exec, exec, s[2:3]
	v_or_b32_e32 v1, 0x500, v0
	v_lshrrev_b32_e32 v1, 4, v1
	v_mad_u32_u24 v4, v1, s4, v6
	v_lshl_add_u32 v5, v1, 1, v7
	ds_read_b128 v[8:11], v4
	ds_read_u16 v12, v5 offset:34816
	ds_read_u16 v13, v5 offset:35088
	ds_read_u16 v14, v5 offset:35360
	ds_read_u16 v5, v5 offset:35632
	v_add_u32_e32 v4, s8, v1
	s_waitcnt lgkmcnt(3)
	v_cvt_f32_f16_e32 v1, v12
	s_waitcnt lgkmcnt(2)
	v_cvt_f32_f16_e32 v12, v13
	s_waitcnt lgkmcnt(1)
	v_cvt_f32_f16_e32 v13, v14
	s_waitcnt lgkmcnt(0)
	v_cvt_f32_f16_e32 v5, v5
	v_add_f32_e32 v1, v8, v1
	v_add_f32_e32 v12, v9, v12
	v_add_f32_e32 v13, v10, v13
	v_add_f32_e32 v14, v11, v5
	v_ashrrev_i32_e32 v5, 31, v4
	v_lshlrev_b64 v[10:11], 13, v[4:5]
	v_cvt_pk_f16_f32 v9, v13, v14
	v_cvt_pk_f16_f32 v8, v1, v12
	v_lshl_add_u64 v[10:11], v[2:3], 0, v[10:11]
	global_store_dwordx2 v[10:11], v[8:9], off sc1
	v_mul_f32_e32 v9, v12, v12
	v_add_f32_e32 v8, v1, v12
	v_fmac_f32_e32 v9, v1, v1
	v_add_f32_e32 v8, v13, v8
	v_fmac_f32_e32 v9, v13, v13
	v_add_f32_e32 v8, v14, v8
	v_fmac_f32_e32 v9, v14, v14
	s_nop 0
	v_add_f32_dpp v1, v8, v8 quad_perm:[1,0,3,2] row_mask:0xf bank_mask:0xf bound_ctrl:1
	v_add_f32_dpp v9, v9, v9 quad_perm:[1,0,3,2] row_mask:0xf bank_mask:0xf bound_ctrl:1
	s_nop 0
	v_add_f32_dpp v1, v1, v1 quad_perm:[2,3,0,1] row_mask:0xf bank_mask:0xf bound_ctrl:1
	v_add_f32_dpp v9, v9, v9 quad_perm:[2,3,0,1] row_mask:0xf bank_mask:0xf bound_ctrl:1
	s_nop 0
	v_add_f32_dpp v1, v1, v1 row_half_mirror row_mask:0xf bank_mask:0xf bound_ctrl:1
	v_add_f32_dpp v9, v9, v9 row_half_mirror row_mask:0xf bank_mask:0xf bound_ctrl:1
	s_nop 0
	v_mov_b32_dpp v8, v1 row_mirror row_mask:0xf bank_mask:0xf bound_ctrl:1
	v_mov_b32_dpp v10, v9 row_mirror row_mask:0xf bank_mask:0xf bound_ctrl:1
	s_and_saveexec_b64 s[2:3], vcc
	s_cbranch_execz .LBB3_14
	v_lshl_add_u64 v[4:5], v[4:5], 2, s[0:1]
	v_add_f32_e32 v1, v1, v8
	v_add_f32_e32 v9, v9, v10
	global_atomic_add_f32 v[4:5], v1, off
	global_atomic_add_f32 v[4:5], v9, off offset:2048
.LBB3_14:
	s_or_b64 exec, exec, s[2:3]
	v_or_b32_e32 v1, 0x600, v0
	v_lshrrev_b32_e32 v1, 4, v1
	v_mad_u32_u24 v4, v1, s4, v6
	v_lshl_add_u32 v5, v1, 1, v7
	ds_read_b128 v[8:11], v4
	ds_read_u16 v12, v5 offset:34816
	ds_read_u16 v13, v5 offset:35088
	ds_read_u16 v14, v5 offset:35360
	ds_read_u16 v5, v5 offset:35632
	v_add_u32_e32 v4, s8, v1
	s_waitcnt lgkmcnt(3)
	v_cvt_f32_f16_e32 v1, v12
	s_waitcnt lgkmcnt(2)
	v_cvt_f32_f16_e32 v12, v13
	s_waitcnt lgkmcnt(1)
	v_cvt_f32_f16_e32 v13, v14
	s_waitcnt lgkmcnt(0)
	v_cvt_f32_f16_e32 v5, v5
	v_add_f32_e32 v1, v8, v1
	v_add_f32_e32 v12, v9, v12
	v_add_f32_e32 v13, v10, v13
	v_add_f32_e32 v14, v11, v5
	v_ashrrev_i32_e32 v5, 31, v4
	v_lshlrev_b64 v[10:11], 13, v[4:5]
	v_cvt_pk_f16_f32 v9, v13, v14
	v_cvt_pk_f16_f32 v8, v1, v12
	v_lshl_add_u64 v[10:11], v[2:3], 0, v[10:11]
	global_store_dwordx2 v[10:11], v[8:9], off sc1
	v_mul_f32_e32 v9, v12, v12
	v_add_f32_e32 v8, v1, v12
	v_fmac_f32_e32 v9, v1, v1
	v_add_f32_e32 v8, v13, v8
	v_fmac_f32_e32 v9, v13, v13
	v_add_f32_e32 v8, v14, v8
	v_fmac_f32_e32 v9, v14, v14
	s_nop 0
	v_add_f32_dpp v1, v8, v8 quad_perm:[1,0,3,2] row_mask:0xf bank_mask:0xf bound_ctrl:1
	v_add_f32_dpp v9, v9, v9 quad_perm:[1,0,3,2] row_mask:0xf bank_mask:0xf bound_ctrl:1
	s_nop 0
	v_add_f32_dpp v1, v1, v1 quad_perm:[2,3,0,1] row_mask:0xf bank_mask:0xf bound_ctrl:1
	v_add_f32_dpp v9, v9, v9 quad_perm:[2,3,0,1] row_mask:0xf bank_mask:0xf bound_ctrl:1
	s_nop 0
	v_add_f32_dpp v1, v1, v1 row_half_mirror row_mask:0xf bank_mask:0xf bound_ctrl:1
	v_add_f32_dpp v9, v9, v9 row_half_mirror row_mask:0xf bank_mask:0xf bound_ctrl:1
	s_nop 0
	v_mov_b32_dpp v8, v1 row_mirror row_mask:0xf bank_mask:0xf bound_ctrl:1
	v_mov_b32_dpp v10, v9 row_mirror row_mask:0xf bank_mask:0xf bound_ctrl:1
	s_and_saveexec_b64 s[2:3], vcc
	s_cbranch_execz .LBB3_16
	v_lshl_add_u64 v[4:5], v[4:5], 2, s[0:1]
	v_add_f32_e32 v1, v1, v8
	v_add_f32_e32 v9, v9, v10
	global_atomic_add_f32 v[4:5], v1, off
	global_atomic_add_f32 v[4:5], v9, off offset:2048
.LBB3_16:
	s_or_b64 exec, exec, s[2:3]
	v_or_b32_e32 v0, 0x700, v0
	v_lshrrev_b32_e32 v0, 4, v0
	v_mad_u32_u24 v1, v0, s4, v6
	v_lshl_add_u32 v8, v0, 1, v7
	ds_read_b128 v[4:7], v1
	ds_read_u16 v1, v8 offset:34816
	ds_read_u16 v9, v8 offset:35088
	ds_read_u16 v10, v8 offset:35360
	ds_read_u16 v8, v8 offset:35632
	v_add_u32_e32 v0, s8, v0
	s_waitcnt lgkmcnt(3)
	v_cvt_f32_f16_e32 v1, v1
	s_waitcnt lgkmcnt(2)
	v_cvt_f32_f16_e32 v9, v9
	s_waitcnt lgkmcnt(1)
	v_cvt_f32_f16_e32 v10, v10
	s_waitcnt lgkmcnt(0)
	v_cvt_f32_f16_e32 v8, v8
	v_add_f32_e32 v11, v4, v1
	v_ashrrev_i32_e32 v1, 31, v0
	v_add_f32_e32 v9, v5, v9
	v_add_f32_e32 v10, v6, v10
	v_add_f32_e32 v8, v7, v8
	v_lshlrev_b64 v[6:7], 13, v[0:1]
	v_cvt_pk_f16_f32 v5, v10, v8
	v_cvt_pk_f16_f32 v4, v11, v9
	v_lshl_add_u64 v[2:3], v[2:3], 0, v[6:7]
	global_store_dwordx2 v[2:3], v[4:5], off sc1
	v_mul_f32_e32 v4, v9, v9
	v_add_f32_e32 v2, v11, v9
	v_fmac_f32_e32 v4, v11, v11
	v_add_f32_e32 v2, v10, v2
	v_fmac_f32_e32 v4, v10, v10
	v_add_f32_e32 v2, v8, v2
	v_fmac_f32_e32 v4, v8, v8
	s_nop 0
	v_add_f32_dpp v2, v2, v2 quad_perm:[1,0,3,2] row_mask:0xf bank_mask:0xf bound_ctrl:1
	v_add_f32_dpp v4, v4, v4 quad_perm:[1,0,3,2] row_mask:0xf bank_mask:0xf bound_ctrl:1
	s_nop 0
	v_add_f32_dpp v2, v2, v2 quad_perm:[2,3,0,1] row_mask:0xf bank_mask:0xf bound_ctrl:1
	v_add_f32_dpp v4, v4, v4 quad_perm:[2,3,0,1] row_mask:0xf bank_mask:0xf bound_ctrl:1
	s_nop 0
	v_add_f32_dpp v2, v2, v2 row_half_mirror row_mask:0xf bank_mask:0xf bound_ctrl:1
	v_add_f32_dpp v4, v4, v4 row_half_mirror row_mask:0xf bank_mask:0xf bound_ctrl:1
	s_nop 0
	v_mov_b32_dpp v3, v2 row_mirror row_mask:0xf bank_mask:0xf bound_ctrl:1
	v_mov_b32_dpp v5, v4 row_mirror row_mask:0xf bank_mask:0xf bound_ctrl:1
	s_and_saveexec_b64 s[2:3], vcc
	s_cbranch_execz .LBB3_18
	v_lshl_add_u64 v[0:1], v[0:1], 2, s[0:1]
	v_add_f32_e32 v2, v2, v3
	v_add_f32_e32 v4, v4, v5
	global_atomic_add_f32 v[0:1], v2, off
	global_atomic_add_f32 v[0:1], v4, off offset:2048

.LBB4_16:
	s_or_b64 exec, exec, s[0:1]
	v_or_b32_e32 v1, 0x800, v10
	v_and_b32_e32 v10, 56, v10
	v_lshrrev_b32_e32 v11, 3, v0
	v_lshlrev_b32_e32 v10, 2, v10
	s_movk_i32 s0, 0x120
	s_waitcnt vmcnt(1)
	v_cvt_f32_f16_sdwa v12, v6 dst_sel:DWORD dst_unused:UNUSED_PAD src0_sel:WORD_1
	v_cvt_f32_f16_e32 v6, v6
	v_lshrrev_b32_e32 v1, 6, v1
	v_mad_u32_u24 v11, v11, s0, v10
	v_cvt_f32_f16_sdwa v13, v7 dst_sel:DWORD dst_unused:UNUSED_PAD src0_sel:WORD_1
	v_cvt_f32_f16_e32 v7, v7
	v_mad_u32_u24 v1, v1, s0, v10
	s_mul_i32 s0, s2, 49
	v_cvt_f32_f16_sdwa v14, v8 dst_sel:DWORD dst_unused:UNUSED_PAD src0_sel:WORD_1
	v_cvt_f32_f16_e32 v8, v8
	s_ashr_i32 s1, s0, 31
	v_cvt_f32_f16_sdwa v15, v9 dst_sel:DWORD dst_unused:UNUSED_PAD src0_sel:WORD_1
	v_cvt_f32_f16_e32 v9, v9
	s_lshl_b64 s[0:1], s[0:1], 2
	ds_write2_b32 v11, v6, v12 offset0:219 offset1:220
	ds_write2_b32 v11, v7, v13 offset0:221 offset1:222
	ds_write2_b32 v11, v8, v14 offset0:223 offset1:224
	ds_write2_b32 v11, v9, v15 offset0:225 offset1:226
	s_waitcnt vmcnt(0)
	v_cvt_f32_f16_sdwa v6, v2 dst_sel:DWORD dst_unused:UNUSED_PAD src0_sel:WORD_1
	v_cvt_f32_f16_e32 v2, v2
	s_waitcnt lgkmcnt(0)
	s_add_u32 s56, s8, s0
	v_cvt_f32_f16_sdwa v7, v3 dst_sel:DWORD dst_unused:UNUSED_PAD src0_sel:WORD_1
	v_cvt_f32_f16_e32 v3, v3
	s_addc_u32 s57, s9, s1
	v_lshrrev_b32_e32 v50, 5, v0
	s_lshl_b64 s[0:1], s[2:3], 2
	v_cvt_f32_f16_sdwa v8, v4 dst_sel:DWORD dst_unused:UNUSED_PAD src0_sel:WORD_1
	v_cvt_f32_f16_e32 v4, v4
	v_and_b32_e32 v51, 31, v0
	v_mul_u32_u24_e32 v0, 0x900, v50
	s_add_u32 s0, s10, s0
	v_cvt_f32_f16_sdwa v9, v5 dst_sel:DWORD dst_unused:UNUSED_PAD src0_sel:WORD_1
	v_cvt_f32_f16_e32 v5, v5
	v_lshl_or_b32 v52, v51, 3, v0
	s_addc_u32 s1, s11, s1
	ds_write2_b32 v1, v2, v6 offset0:219 offset1:220
	ds_write2_b32 v1, v3, v7 offset0:221 offset1:222
	ds_write2_b32 v1, v4, v8 offset0:223 offset1:224
	ds_write2_b32 v1, v5, v9 offset0:225 offset1:226
	s_waitcnt lgkmcnt(0)
	s_barrier
	ds_read2_b64 v[8:11], v52 offset1:1
	ds_read2_b64 v[54:57], v52 offset0:2 offset1:3
	s_load_dword s64, s[0:1], 0x0
	ds_read2_b64 v[24:27], v52 offset0:36 offset1:37
	ds_read2_b64 v[16:19], v52 offset0:38 offset1:39
	s_load_dword s76, s[56:57], 0x58
	s_load_dwordx2 s[42:43], s[56:57], 0x58
	s_load_dwordx2 s[36:37], s[56:57], 0x5c
	s_load_dwordx2 s[44:45], s[56:57], 0x50
	s_load_dwordx4 s[16:19], s[56:57], 0x0
	s_load_dword s66, s[56:57], 0x8
	s_load_dwordx2 s[20:21], s[56:57], 0xc
	s_load_dwordx2 s[62:63], s[56:57], 0x10
	s_load_dwordx2 s[60:61], s[56:57], 0x14
	s_load_dwordx2 s[58:59], s[56:57], 0x18
	s_load_dwordx2 s[52:53], s[56:57], 0x1c
	s_load_dwordx2 s[54:55], s[56:57], 0x20
	s_load_dwordx2 s[50:51], s[56:57], 0x24
	s_load_dwordx2 s[46:47], s[56:57], 0x28
	s_load_dwordx2 s[48:49], s[56:57], 0x2c
	s_load_dwordx8 s[8:15], s[56:57], 0x30
	ds_read2_b64 v[44:47], v52 offset0:72 offset1:73
	ds_read2_b64 v[40:43], v52 offset0:74 offset1:75
	ds_read2_b64 v[36:39], v52 offset0:108 offset1:109
	ds_read2_b64 v[32:35], v52 offset0:110 offset1:111
	s_load_dwordx2 s[40:41], s[56:57], 0x60
	s_load_dwordx2 s[38:39], s[56:57], 0x64
	s_load_dword s22, s[56:57], 0xa0
	s_load_dwordx2 s[34:35], s[56:57], 0x98
	s_load_dwordx4 s[24:27], s[56:57], 0x88
	s_load_dwordx8 s[0:7], s[56:57], 0x68
	s_waitcnt lgkmcnt(0)
	v_mov_b64_e32 v[48:49], s[64:65]
	v_pk_fma_f32 v[12:13], v[8:9], s[16:17], v[48:49] op_sel_hi:[1,0,0]
	v_pk_mov_b32 v[8:9], v[8:9], v[10:11] op_sel:[1,0]
	v_pk_mov_b32 v[58:59], v[44:45], v[46:47] op_sel:[1,0]
	v_pk_fma_f32 v[8:9], v[8:9], s[16:17], v[12:13] op_sel:[0,1,0]
	s_mov_b32 s64, s11
	v_pk_fma_f32 v[8:9], v[10:11], s[66:67], v[8:9] op_sel_hi:[1,0,1]
	v_pk_mov_b32 v[10:11], v[10:11], v[54:55] op_sel:[1,0]
	s_mov_b32 s68, s13
	v_pk_fma_f32 v[8:9], v[10:11], s[18:19], v[8:9] op_sel:[0,1,0]
	v_pk_mov_b32 v[10:11], v[54:55], v[56:57] op_sel:[1,0]
	v_pk_fma_f32 v[8:9], v[54:55], s[20:21], v[8:9] op_sel:[0,1,0]
	ds_read2_b64 v[28:31], v52 offset0:144 offset1:145
	ds_read2_b64 v[20:23], v52 offset0:146 offset1:147
	ds_read2_b64 v[4:7], v52 offset0:180 offset1:181
	ds_read2_b64 v[0:3], v52 offset0:182 offset1:183
	v_pk_fma_f32 v[54:55], v[10:11], s[62:63], v[8:9] op_sel:[0,1,0]
	s_mov_b32 s70, s3
	v_pk_fma_f32 v[54:55], v[56:57], s[60:61], v[54:55] op_sel:[0,1,0]
	v_pk_mov_b32 v[56:57], v[24:25], v[26:27] op_sel:[1,0]
	v_pk_fma_f32 v[54:55], v[24:25], s[58:59], v[54:55] op_sel:[0,1,0]
	v_pk_fma_f32 v[24:25], v[24:25], s[16:17], v[48:49] op_sel_hi:[1,0,0]
	v_pk_fma_f32 v[54:55], v[56:57], s[52:53], v[54:55] op_sel:[0,1,0]
	v_pk_fma_f32 v[24:25], v[56:57], s[16:17], v[24:25] op_sel:[0,1,0]
	v_pk_fma_f32 v[54:55], v[26:27], s[54:55], v[54:55] op_sel:[0,1,0]
	v_pk_mov_b32 v[56:57], v[26:27], v[16:17] op_sel:[1,0]
	v_pk_fma_f32 v[24:25], v[26:27], s[66:67], v[24:25] op_sel_hi:[1,0,1]
	v_pk_fma_f32 v[54:55], v[56:57], s[50:51], v[54:55] op_sel:[0,1,0]
	v_pk_fma_f32 v[24:25], v[56:57], s[18:19], v[24:25] op_sel:[0,1,0]
	v_pk_fma_f32 v[54:55], v[16:17], s[46:47], v[54:55] op_sel:[0,1,0]
	v_pk_mov_b32 v[26:27], v[16:17], v[18:19] op_sel:[1,0]
	v_pk_fma_f32 v[16:17], v[16:17], s[20:21], v[24:25] op_sel:[0,1,0]
	v_pk_fma_f32 v[54:55], v[26:27], s[48:49], v[54:55] op_sel:[0,1,0]
	v_pk_fma_f32 v[16:17], v[26:27], s[62:63], v[16:17] op_sel:[0,1,0]
	v_pk_fma_f32 v[54:55], v[18:19], s[8:9], v[54:55] op_sel:[0,1,0]
	v_pk_fma_f32 v[16:17], v[18:19], s[60:61], v[16:17] op_sel:[0,1,0]
	v_pk_fma_f32 v[54:55], v[44:45], s[10:11], v[54:55] op_sel_hi:[1,0,1]
	v_pk_fma_f32 v[16:17], v[44:45], s[58:59], v[16:17] op_sel:[0,1,0]
	v_pk_fma_f32 v[54:55], v[58:59], s[64:65], v[54:55] op_sel_hi:[1,0,1]
	v_pk_fma_f32 v[56:57], v[58:59], s[52:53], v[16:17] op_sel:[0,1,0]
	v_pk_fma_f32 v[16:17], v[44:45], s[16:17], v[48:49] op_sel_hi:[1,0,0]
	v_pk_fma_f32 v[54:55], v[46:47], s[12:13], v[54:55] op_sel_hi:[1,0,1]
	v_pk_fma_f32 v[44:45], v[58:59], s[16:17], v[16:17] op_sel:[0,1,0]
	v_pk_fma_f32 v[56:57], v[46:47], s[54:55], v[56:57] op_sel:[0,1,0]
	v_pk_fma_f32 v[44:45], v[46:47], s[66:67], v[44:45] op_sel_hi:[1,0,1]
	v_pk_mov_b32 v[46:47], v[46:47], v[40:41] op_sel:[1,0]
	v_pk_mov_b32 v[58:59], v[40:41], v[42:43] op_sel:[1,0]
	v_pk_fma_f32 v[54:55], v[46:47], s[68:69], v[54:55] op_sel_hi:[1,0,1]
	v_pk_fma_f32 v[56:57], v[46:47], s[50:51], v[56:57] op_sel:[0,1,0]
	v_pk_fma_f32 v[44:45], v[46:47], s[18:19], v[44:45] op_sel:[0,1,0]
	v_pk_fma_f32 v[54:55], v[40:41], s[14:15], v[54:55] op_sel_hi:[1,0,1]
	s_mov_b32 s66, s15
	v_pk_fma_f32 v[56:57], v[40:41], s[46:47], v[56:57] op_sel:[0,1,0]
	v_pk_fma_f32 v[40:41], v[40:41], s[20:21], v[44:45] op_sel:[0,1,0]
	v_pk_fma_f32 v[54:55], v[58:59], s[66:67], v[54:55] op_sel_hi:[1,0,1]
	v_pk_fma_f32 v[40:41], v[58:59], s[62:63], v[40:41] op_sel:[0,1,0]
	v_pk_fma_f32 v[54:55], v[42:43], s[44:45], v[54:55] op_sel_hi:[1,0,1]
	v_pk_fma_f32 v[40:41], v[42:43], s[60:61], v[40:41] op_sel:[0,1,0]
	v_pk_fma_f32 v[54:55], v[36:37], s[44:45], v[54:55] op_sel:[0,1,0]
	v_pk_mov_b32 v[46:47], v[36:37], v[38:39] op_sel:[1,0]
	v_pk_fma_f32 v[40:41], v[36:37], s[58:59], v[40:41] op_sel:[0,1,0]
	v_pk_fma_f32 v[54:55], v[46:47], s[76:77], v[54:55] op_sel_hi:[1,0,1]
	v_pk_fma_f32 v[40:41], v[46:47], s[52:53], v[40:41] op_sel:[0,1,0]
	v_pk_fma_f32 v[54:55], v[38:39], s[42:43], v[54:55] op_sel:[0,1,0]
	v_pk_mov_b32 v[44:45], v[38:39], v[32:33] op_sel:[1,0]
	v_pk_fma_f32 v[40:41], v[38:39], s[54:55], v[40:41] op_sel:[0,1,0]
	v_pk_fma_f32 v[56:57], v[58:59], s[48:49], v[56:57] op_sel:[0,1,0]
	v_pk_fma_f32 v[54:55], v[44:45], s[36:37], v[54:55] op_sel:[0,1,0]
	v_pk_fma_f32 v[40:41], v[44:45], s[50:51], v[40:41] op_sel:[0,1,0]
	v_pk_fma_f32 v[54:55], v[32:33], s[40:41], v[54:55] op_sel:[0,1,0]
	v_pk_fma_f32 v[56:57], v[42:43], s[8:9], v[56:57] op_sel:[0,1,0]
	v_pk_mov_b32 v[42:43], v[32:33], v[34:35] op_sel:[1,0]
	v_pk_fma_f32 v[40:41], v[32:33], s[46:47], v[40:41] op_sel:[0,1,0]
	v_pk_fma_f32 v[54:55], v[42:43], s[38:39], v[54:55] op_sel:[0,1,0]
	v_pk_fma_f32 v[40:41], v[42:43], s[48:49], v[40:41] op_sel:[0,1,0]
	v_pk_fma_f32 v[54:55], v[34:35], s[0:1], v[54:55] op_sel:[0,1,0]
	v_pk_fma_f32 v[56:57], v[36:37], s[10:11], v[56:57] op_sel_hi:[1,0,1]
	v_pk_fma_f32 v[36:37], v[36:37], s[16:17], v[48:49] op_sel_hi:[1,0,0]
	v_pk_fma_f32 v[40:41], v[34:35], s[8:9], v[40:41] op_sel:[0,1,0]
	s_waitcnt lgkmcnt(3)
	v_pk_fma_f32 v[54:55], v[28:29], s[2:3], v[54:55] op_sel_hi:[1,0,1]
	v_pk_fma_f32 v[56:57], v[46:47], s[64:65], v[56:57] op_sel_hi:[1,0,1]
	v_pk_fma_f32 v[36:37], v[46:47], s[16:17], v[36:37] op_sel:[0,1,0]
	v_pk_mov_b32 v[46:47], v[28:29], v[30:31] op_sel:[1,0]
	v_pk_fma_f32 v[40:41], v[28:29], s[10:11], v[40:41] op_sel_hi:[1,0,1]
	v_pk_fma_f32 v[54:55], v[46:47], s[70:71], v[54:55] op_sel_hi:[1,0,1]
	v_pk_fma_f32 v[40:41], v[46:47], s[64:65], v[40:41] op_sel_hi:[1,0,1]
	v_pk_fma_f32 v[54:55], v[30:31], s[4:5], v[54:55] op_sel_hi:[1,0,1]
	v_pk_fma_f32 v[56:57], v[38:39], s[12:13], v[56:57] op_sel_hi:[1,0,1]
	s_waitcnt lgkmcnt(2)
	v_pk_mov_b32 v[58:59], v[30:31], v[20:21] op_sel:[1,0]
	s_mov_b32 s72, s5
	v_pk_fma_f32 v[40:41], v[30:31], s[12:13], v[40:41] op_sel_hi:[1,0,1]
	v_pk_fma_f32 v[36:37], v[38:39], s[18:19], v[36:37] op_sel_hi:[1,0,1]
	v_pk_fma_f32 v[38:39], v[58:59], s[72:73], v[54:55] op_sel_hi:[1,0,1]
	v_pk_fma_f32 v[56:57], v[44:45], s[68:69], v[56:57] op_sel_hi:[1,0,1]
	v_pk_fma_f32 v[40:41], v[58:59], s[68:69], v[40:41] op_sel_hi:[1,0,1]
	v_pk_fma_f32 v[38:39], v[20:21], s[6:7], v[38:39] op_sel_hi:[1,0,1]
	v_pk_mov_b32 v[54:55], v[20:21], v[22:23] op_sel:[1,0]
	s_mov_b32 s74, s7
	v_pk_fma_f32 v[56:57], v[32:33], s[14:15], v[56:57] op_sel_hi:[1,0,1]
	v_pk_fma_f32 v[40:41], v[20:21], s[14:15], v[40:41] op_sel_hi:[1,0,1]
	v_pk_fma_f32 v[38:39], v[54:55], s[74:75], v[38:39] op_sel_hi:[1,0,1]
	v_pk_fma_f32 v[56:57], v[42:43], s[66:67], v[56:57] op_sel_hi:[1,0,1]
	v_pk_fma_f32 v[40:41], v[54:55], s[66:67], v[40:41] op_sel_hi:[1,0,1]
	v_pk_fma_f32 v[38:39], v[22:23], s[24:25], v[38:39] op_sel_hi:[1,0,1]
	v_pk_fma_f32 v[56:57], v[34:35], s[44:45], v[56:57] op_sel_hi:[1,0,1]
	v_pk_fma_f32 v[40:41], v[22:23], s[44:45], v[40:41] op_sel_hi:[1,0,1]
	s_waitcnt lgkmcnt(1)
	v_pk_fma_f32 v[38:39], v[4:5], s[24:25], v[38:39] op_sel:[0,1,0]
	v_pk_fma_f32 v[36:37], v[44:45], s[20:21], v[36:37] op_sel_hi:[1,0,1]
	v_pk_mov_b32 v[44:45], v[4:5], v[6:7] op_sel:[1,0]
	v_pk_fma_f32 v[56:57], v[28:29], s[44:45], v[56:57] op_sel:[0,1,0]
	v_pk_fma_f32 v[40:41], v[4:5], s[44:45], v[40:41] op_sel:[0,1,0]
	v_pk_fma_f32 v[38:39], v[44:45], s[26:27], v[38:39] op_sel_hi:[1,0,1]
	v_pk_fma_f32 v[56:57], v[46:47], s[76:77], v[56:57] op_sel_hi:[1,0,1]
	v_pk_fma_f32 v[60:61], v[44:45], s[76:77], v[40:41] op_sel_hi:[1,0,1]
	s_mov_b32 s76, s27
	v_pk_fma_f32 v[38:39], v[6:7], s[76:77], v[38:39] op_sel_hi:[1,0,1]
	v_pk_fma_f32 v[32:33], v[32:33], s[62:63], v[36:37] op_sel_hi:[1,0,1]
	s_waitcnt lgkmcnt(0)
	v_pk_mov_b32 v[36:37], v[6:7], v[0:1] op_sel:[1,0]
	v_pk_fma_f32 v[32:33], v[42:43], s[60:61], v[32:33] op_sel_hi:[1,0,1]
	v_pk_fma_f32 v[38:39], v[36:37], s[34:35], v[38:39] op_sel_hi:[1,0,1]
	v_pk_fma_f32 v[40:41], v[34:35], s[58:59], v[32:33] op_sel_hi:[1,0,1]
	v_pk_fma_f32 v[38:39], v[0:1], s[34:35], v[38:39] op_sel:[0,1,0]
	v_pk_mov_b32 v[34:35], v[0:1], v[2:3] op_sel:[1,0]
	ds_read2_b64 v[12:15], v52 offset0:216 offset1:217
	ds_read2_b64 v[8:11], v52 offset0:218 offset1:219
	v_pk_fma_f32 v[32:33], v[34:35], s[22:23], v[38:39] op_sel_hi:[1,0,1]
	v_pk_fma_f32 v[38:39], v[28:29], s[52:53], v[40:41] op_sel_hi:[1,0,1]
	v_pk_fma_f32 v[28:29], v[28:29], s[16:17], v[48:49] op_sel_hi:[1,0,0]
	v_pk_fma_f32 v[40:41], v[30:31], s[42:43], v[56:57] op_sel:[0,1,0]
	v_pk_fma_f32 v[38:39], v[46:47], s[54:55], v[38:39] op_sel_hi:[1,0,1]
	v_pk_fma_f32 v[28:29], v[46:47], s[16:17], v[28:29] op_sel:[0,1,0]
	v_pk_fma_f32 v[40:41], v[58:59], s[36:37], v[40:41] op_sel:[0,1,0]
	v_pk_fma_f32 v[42:43], v[30:31], s[50:51], v[38:39] op_sel_hi:[1,0,1]
	v_pk_fma_f32 v[28:29], v[30:31], s[18:19], v[28:29] op_sel_hi:[1,0,1]
	v_pk_fma_f32 v[40:41], v[20:21], s[40:41], v[40:41] op_sel:[0,1,0]
	v_pk_fma_f32 v[42:43], v[58:59], s[46:47], v[42:43] op_sel_hi:[1,0,1]
	v_pk_fma_f32 v[40:41], v[54:55], s[38:39], v[40:41] op_sel:[0,1,0]
	v_pk_fma_f32 v[28:29], v[58:59], s[20:21], v[28:29] op_sel_hi:[1,0,1]
	v_pk_fma_f32 v[40:41], v[22:23], s[0:1], v[40:41] op_sel:[0,1,0]
	v_pk_fma_f32 v[42:43], v[20:21], s[48:49], v[42:43] op_sel_hi:[1,0,1]
	v_pk_fma_f32 v[20:21], v[20:21], s[62:63], v[28:29] op_sel_hi:[1,0,1]
	v_pk_fma_f32 v[40:41], v[4:5], s[2:3], v[40:41] op_sel_hi:[1,0,1]
	v_pk_fma_f32 v[42:43], v[54:55], s[8:9], v[42:43] op_sel_hi:[1,0,1]
	v_pk_fma_f32 v[20:21], v[54:55], s[60:61], v[20:21] op_sel_hi:[1,0,1]
	v_pk_fma_f32 v[54:55], v[6:7], s[42:43], v[60:61] op_sel:[0,1,0]
	v_pk_fma_f32 v[40:41], v[44:45], s[70:71], v[40:41] op_sel_hi:[1,0,1]
	v_pk_fma_f32 v[54:55], v[36:37], s[36:37], v[54:55] op_sel:[0,1,0]
	v_pk_fma_f32 v[40:41], v[6:7], s[4:5], v[40:41] op_sel_hi:[1,0,1]
	v_pk_fma_f32 v[54:55], v[0:1], s[40:41], v[54:55] op_sel:[0,1,0]
	v_pk_fma_f32 v[40:41], v[36:37], s[72:73], v[40:41] op_sel_hi:[1,0,1]
	v_pk_fma_f32 v[54:55], v[34:35], s[38:39], v[54:55] op_sel:[0,1,0]
	v_pk_fma_f32 v[40:41], v[0:1], s[6:7], v[40:41] op_sel_hi:[1,0,1]
	v_pk_fma_f32 v[54:55], v[2:3], s[0:1], v[54:55] op_sel:[0,1,0]
	s_waitcnt lgkmcnt(1)
	v_pk_mov_b32 v[46:47], v[12:13], v[14:15] op_sel:[1,0]
	v_pk_fma_f32 v[40:41], v[34:35], s[74:75], v[40:41] op_sel_hi:[1,0,1]
	v_pk_fma_f32 v[54:55], v[12:13], s[2:3], v[54:55] op_sel_hi:[1,0,1]
	v_pk_fma_f32 v[40:41], v[2:3], s[24:25], v[40:41] op_sel_hi:[1,0,1]
	v_pk_fma_f32 v[54:55], v[46:47], s[70:71], v[54:55] op_sel_hi:[1,0,1]
	s_waitcnt lgkmcnt(0)
	v_pk_mov_b32 v[38:39], v[14:15], v[8:9] op_sel:[1,0]
	v_pk_fma_f32 v[40:41], v[12:13], s[24:25], v[40:41] op_sel:[0,1,0]
	v_pk_fma_f32 v[54:55], v[14:15], s[4:5], v[54:55] op_sel_hi:[1,0,1]
	ds_read2_b64 v[24:27], v52 offset0:252 offset1:253
	ds_read2_b64 v[16:19], v52 offset0:254 offset1:255
	v_pk_fma_f32 v[40:41], v[46:47], s[26:27], v[40:41] op_sel_hi:[1,0,1]
	v_pk_fma_f32 v[54:55], v[38:39], s[72:73], v[54:55] op_sel_hi:[1,0,1]
	v_pk_mov_b32 v[30:31], v[8:9], v[10:11] op_sel:[1,0]
	v_pk_fma_f32 v[40:41], v[14:15], s[76:77], v[40:41] op_sel_hi:[1,0,1]
	v_pk_fma_f32 v[54:55], v[8:9], s[6:7], v[54:55] op_sel_hi:[1,0,1]
	v_pk_fma_f32 v[40:41], v[38:39], s[34:35], v[40:41] op_sel_hi:[1,0,1]
	v_pk_fma_f32 v[54:55], v[30:31], s[74:75], v[54:55] op_sel_hi:[1,0,1]
	v_pk_fma_f32 v[40:41], v[8:9], s[34:35], v[40:41] op_sel:[0,1,0]
	v_pk_fma_f32 v[54:55], v[10:11], s[24:25], v[54:55] op_sel_hi:[1,0,1]
	v_pk_fma_f32 v[56:57], v[30:31], s[22:23], v[40:41] op_sel_hi:[1,0,1]
	s_waitcnt lgkmcnt(1)
	v_pk_mov_b32 v[40:41], v[24:25], v[26:27] op_sel:[1,0]
	v_pk_fma_f32 v[42:43], v[22:23], s[8:9], v[42:43] op_sel:[0,1,0]
	v_pk_fma_f32 v[22:23], v[22:23], s[58:59], v[20:21] op_sel_hi:[1,0,1]
	v_pk_fma_f32 v[54:55], v[24:25], s[24:25], v[54:55] op_sel:[0,1,0]
	v_pk_fma_f32 v[42:43], v[4:5], s[10:11], v[42:43] op_sel_hi:[1,0,1]
	v_pk_fma_f32 v[54:55], v[40:41], s[26:27], v[54:55] op_sel_hi:[1,0,1]
	v_pk_fma_f32 v[22:23], v[4:5], s[52:53], v[22:23] op_sel_hi:[1,0,1]
	v_pk_fma_f32 v[4:5], v[4:5], s[16:17], v[48:49] op_sel_hi:[1,0,0]
	s_waitcnt lgkmcnt(0)
	v_pk_mov_b32 v[28:29], v[26:27], v[16:17] op_sel:[1,0]
	v_pk_fma_f32 v[54:55], v[26:27], s[76:77], v[54:55] op_sel_hi:[1,0,1]
	v_pk_fma_f32 v[42:43], v[44:45], s[64:65], v[42:43] op_sel_hi:[1,0,1]
	v_pk_fma_f32 v[22:23], v[44:45], s[54:55], v[22:23] op_sel_hi:[1,0,1]
	v_pk_fma_f32 v[4:5], v[44:45], s[16:17], v[4:5] op_sel:[0,1,0]
	v_pk_fma_f32 v[44:45], v[12:13], s[16:17], v[48:49] op_sel_hi:[1,0,0]
	v_pk_fma_f32 v[54:55], v[28:29], s[34:35], v[54:55] op_sel_hi:[1,0,1]
	v_pk_fma_f32 v[44:45], v[46:47], s[16:17], v[44:45] op_sel:[0,1,0]
	v_pk_mov_b32 v[20:21], v[16:17], v[18:19] op_sel:[1,0]
	v_pk_fma_f32 v[54:55], v[16:17], s[34:35], v[54:55] op_sel:[0,1,0]
	v_pk_fma_f32 v[44:45], v[14:15], s[18:19], v[44:45] op_sel_hi:[1,0,1]
	v_pk_fma_f32 v[58:59], v[20:21], s[22:23], v[54:55] op_sel_hi:[1,0,1]
	v_pk_fma_f32 v[54:55], v[38:39], s[20:21], v[44:45] op_sel_hi:[1,0,1]
	v_pk_fma_f32 v[44:45], v[24:25], s[16:17], v[48:49] op_sel_hi:[1,0,0]
	v_pk_fma_f32 v[4:5], v[6:7], s[18:19], v[4:5] op_sel_hi:[1,0,1]
	v_pk_fma_f32 v[44:45], v[40:41], s[16:17], v[44:45] op_sel:[0,1,0]
	v_pk_fma_f32 v[4:5], v[36:37], s[20:21], v[4:5] op_sel_hi:[1,0,1]
	v_pk_fma_f32 v[44:45], v[26:27], s[18:19], v[44:45] op_sel_hi:[1,0,1]
	v_pk_fma_f32 v[42:43], v[6:7], s[12:13], v[42:43] op_sel_hi:[1,0,1]
	v_pk_fma_f32 v[48:49], v[28:29], s[20:21], v[44:45] op_sel_hi:[1,0,1]
	s_load_dwordx8 s[16:23], s[56:57], 0xa0
	v_pk_fma_f32 v[6:7], v[6:7], s[50:51], v[22:23] op_sel_hi:[1,0,1]
	v_pk_fma_f32 v[22:23], v[36:37], s[68:69], v[42:43] op_sel_hi:[1,0,1]
	v_pk_fma_f32 v[6:7], v[36:37], s[46:47], v[6:7] op_sel_hi:[1,0,1]
	v_pk_fma_f32 v[22:23], v[0:1], s[14:15], v[22:23] op_sel_hi:[1,0,1]
	v_pk_fma_f32 v[6:7], v[0:1], s[48:49], v[6:7] op_sel_hi:[1,0,1]
	v_pk_fma_f32 v[0:1], v[0:1], s[62:63], v[4:5] op_sel_hi:[1,0,1]
	v_pk_fma_f32 v[22:23], v[34:35], s[66:67], v[22:23] op_sel_hi:[1,0,1]
	v_pk_fma_f32 v[6:7], v[34:35], s[8:9], v[6:7] op_sel_hi:[1,0,1]
	v_pk_fma_f32 v[0:1], v[34:35], s[60:61], v[0:1] op_sel_hi:[1,0,1]
	s_waitcnt lgkmcnt(0)
	v_pk_fma_f32 v[4:5], v[2:3], s[16:17], v[32:33] op_sel:[0,1,0]
	s_load_dword s78, s[56:57], 0xc0
	v_pk_fma_f32 v[22:23], v[2:3], s[44:45], v[22:23] op_sel_hi:[1,0,1]
	v_pk_fma_f32 v[6:7], v[2:3], s[8:9], v[6:7] op_sel:[0,1,0]
	v_pk_fma_f32 v[0:1], v[2:3], s[58:59], v[0:1] op_sel_hi:[1,0,1]
	v_pk_fma_f32 v[2:3], v[12:13], s[18:19], v[4:5] op_sel_hi:[1,0,1]
	s_mov_b32 s56, s19
	v_pk_fma_f32 v[2:3], v[46:47], s[56:57], v[2:3] op_sel_hi:[1,0,1]
	v_pk_fma_f32 v[4:5], v[8:9], s[62:63], v[54:55] op_sel_hi:[1,0,1]
	v_pk_fma_f32 v[54:55], v[14:15], s[20:21], v[2:3] op_sel_hi:[1,0,1]
	v_pk_fma_f32 v[2:3], v[12:13], s[44:45], v[22:23] op_sel:[0,1,0]
	v_pk_fma_f32 v[0:1], v[12:13], s[52:53], v[0:1] op_sel_hi:[1,0,1]
	v_pk_fma_f32 v[2:3], v[46:47], s[42:43], v[2:3] op_sel_hi:[1,0,1]
	v_pk_fma_f32 v[32:33], v[16:17], s[62:63], v[48:49] op_sel_hi:[1,0,1]
	v_pk_fma_f32 v[22:23], v[14:15], s[36:37], v[2:3] op_sel_hi:[1,0,1]
	v_pk_fma_f32 v[2:3], v[12:13], s[10:11], v[6:7] op_sel_hi:[1,0,1]
	v_pk_fma_f32 v[0:1], v[46:47], s[54:55], v[0:1] op_sel_hi:[1,0,1]
	v_pk_fma_f32 v[2:3], v[46:47], s[64:65], v[2:3] op_sel_hi:[1,0,1]
	v_pk_fma_f32 v[12:13], v[14:15], s[50:51], v[0:1] op_sel_hi:[1,0,1]
	v_pk_fma_f32 v[60:61], v[14:15], s[12:13], v[2:3] op_sel_hi:[1,0,1]
	v_pk_fma_f32 v[4:5], v[30:31], s[60:61], v[4:5] op_sel_hi:[1,0,1]
	v_pk_fma_f32 v[6:7], v[20:21], s[60:61], v[32:33] op_sel_hi:[1,0,1]
	s_mov_b32 s60, s21
	v_pk_fma_f32 v[14:15], v[38:39], s[60:61], v[54:55] op_sel_hi:[1,0,1]
	v_pk_fma_f32 v[22:23], v[38:39], s[40:41], v[22:23] op_sel_hi:[1,0,1]
	v_pk_fma_f32 v[32:33], v[38:39], s[68:69], v[60:61] op_sel_hi:[1,0,1]
	v_pk_fma_f32 v[12:13], v[38:39], s[46:47], v[12:13] op_sel_hi:[1,0,1]
	v_add_u32_e32 v44, 0x900, v52
	v_add_u32_e32 v45, 0x910, v52
	v_add_u32_e32 v53, 0xa20, v52
	v_add_u32_e32 v62, 0xa30, v52
	v_pk_fma_f32 v[14:15], v[8:9], s[22:23], v[14:15] op_sel_hi:[1,0,1]
	v_pk_fma_f32 v[22:23], v[8:9], s[38:39], v[22:23] op_sel_hi:[1,0,1]
	v_pk_fma_f32 v[32:33], v[8:9], s[14:15], v[32:33] op_sel_hi:[1,0,1]
	v_pk_fma_f32 v[8:9], v[8:9], s[48:49], v[12:13] op_sel_hi:[1,0,1]
	ds_read2_b64 v[34:37], v44 offset1:1
	ds_read2_b64 v[42:45], v45 offset1:1
	ds_read2_b64 v[0:3], v53 offset1:1
	ds_read2_b64 v[46:49], v62 offset1:1
	v_pk_fma_f32 v[4:5], v[10:11], s[58:59], v[4:5] op_sel_hi:[1,0,1]
	v_pk_fma_f32 v[62:63], v[18:19], s[58:59], v[6:7] op_sel_hi:[1,0,1]
	s_mov_b32 s58, s23
	v_pk_fma_f32 v[22:23], v[30:31], s[0:1], v[22:23] op_sel_hi:[1,0,1]
	v_pk_fma_f32 v[32:33], v[30:31], s[66:67], v[32:33] op_sel_hi:[1,0,1]
	v_pk_fma_f32 v[8:9], v[30:31], s[8:9], v[8:9] op_sel_hi:[1,0,1]
	v_pk_fma_f32 v[6:7], v[30:31], s[58:59], v[14:15] op_sel_hi:[1,0,1]
	v_pk_fma_f32 v[14:15], v[10:11], s[16:17], v[56:57] op_sel:[0,1,0]
	v_pk_fma_f32 v[22:23], v[10:11], s[0:1], v[22:23] op_sel:[0,1,0]
	v_pk_fma_f32 v[60:61], v[10:11], s[44:45], v[32:33] op_sel_hi:[1,0,1]
	v_pk_fma_f32 v[8:9], v[10:11], s[8:9], v[8:9] op_sel:[0,1,0]
	s_waitcnt lgkmcnt(0)
	v_pk_fma_f32 v[6:7], v[10:11], s[78:79], v[6:7] op_sel_hi:[1,0,1]
	v_pk_fma_f32 v[10:11], v[24:25], s[18:19], v[14:15] op_sel_hi:[1,0,1]
	v_pk_fma_f32 v[12:13], v[24:25], s[2:3], v[22:23] op_sel_hi:[1,0,1]
	v_pk_fma_f32 v[14:15], v[24:25], s[44:45], v[60:61] op_sel:[0,1,0]
	v_pk_fma_f32 v[8:9], v[24:25], s[10:11], v[8:9] op_sel_hi:[1,0,1]
	v_pk_fma_f32 v[4:5], v[24:25], s[52:53], v[4:5] op_sel_hi:[1,0,1]
	v_pk_fma_f32 v[12:13], v[40:41], s[70:71], v[12:13] op_sel_hi:[1,0,1]
	v_pk_fma_f32 v[14:15], v[40:41], s[42:43], v[14:15] op_sel_hi:[1,0,1]
	v_pk_fma_f32 v[8:9], v[40:41], s[64:65], v[8:9] op_sel_hi:[1,0,1]
	v_pk_fma_f32 v[4:5], v[40:41], s[54:55], v[4:5] op_sel_hi:[1,0,1]
	v_pk_fma_f32 v[10:11], v[40:41], s[56:57], v[10:11] op_sel_hi:[1,0,1]
	v_pk_fma_f32 v[12:13], v[26:27], s[4:5], v[12:13] op_sel_hi:[1,0,1]
	v_pk_fma_f32 v[14:15], v[26:27], s[36:37], v[14:15] op_sel_hi:[1,0,1]
	v_pk_fma_f32 v[8:9], v[26:27], s[12:13], v[8:9] op_sel_hi:[1,0,1]
	v_pk_fma_f32 v[4:5], v[26:27], s[50:51], v[4:5] op_sel_hi:[1,0,1]
	v_pk_fma_f32 v[10:11], v[26:27], s[20:21], v[10:11] op_sel_hi:[1,0,1]
	v_pk_fma_f32 v[12:13], v[28:29], s[72:73], v[12:13] op_sel_hi:[1,0,1]
	v_pk_fma_f32 v[14:15], v[28:29], s[40:41], v[14:15] op_sel_hi:[1,0,1]
	v_pk_fma_f32 v[8:9], v[28:29], s[68:69], v[8:9] op_sel_hi:[1,0,1]
	v_pk_fma_f32 v[4:5], v[28:29], s[46:47], v[4:5] op_sel_hi:[1,0,1]
	v_pk_fma_f32 v[10:11], v[28:29], s[60:61], v[10:11] op_sel_hi:[1,0,1]
	v_pk_fma_f32 v[12:13], v[16:17], s[6:7], v[12:13] op_sel_hi:[1,0,1]
	v_pk_fma_f32 v[14:15], v[16:17], s[38:39], v[14:15] op_sel_hi:[1,0,1]
	v_pk_fma_f32 v[8:9], v[16:17], s[14:15], v[8:9] op_sel_hi:[1,0,1]
	v_pk_fma_f32 v[4:5], v[16:17], s[48:49], v[4:5] op_sel_hi:[1,0,1]
	v_pk_fma_f32 v[10:11], v[16:17], s[22:23], v[10:11] op_sel_hi:[1,0,1]
	v_pk_fma_f32 v[12:13], v[20:21], s[74:75], v[12:13] op_sel_hi:[1,0,1]
	v_pk_fma_f32 v[14:15], v[20:21], s[0:1], v[14:15] op_sel_hi:[1,0,1]
	v_pk_fma_f32 v[8:9], v[20:21], s[66:67], v[8:9] op_sel_hi:[1,0,1]
	v_pk_fma_f32 v[4:5], v[20:21], s[8:9], v[4:5] op_sel_hi:[1,0,1]
	v_pk_fma_f32 v[10:11], v[20:21], s[58:59], v[10:11] op_sel_hi:[1,0,1]
	v_pk_fma_f32 v[26:27], v[18:19], s[16:17], v[58:59] op_sel:[0,1,0]
	v_pk_fma_f32 v[12:13], v[18:19], s[24:25], v[12:13] op_sel_hi:[1,0,1]
	v_pk_fma_f32 v[14:15], v[18:19], s[0:1], v[14:15] op_sel:[0,1,0]
	v_pk_fma_f32 v[8:9], v[18:19], s[44:45], v[8:9] op_sel_hi:[1,0,1]
	v_pk_fma_f32 v[4:5], v[18:19], s[8:9], v[4:5] op_sel:[0,1,0]
	v_add_u32_e32 v53, 0xb40, v52
	v_pk_fma_f32 v[10:11], v[18:19], s[78:79], v[10:11] op_sel_hi:[1,0,1]
	v_pk_fma_f32 v[26:27], v[34:35], s[18:19], v[26:27] op_sel_hi:[1,0,1]
	v_pk_mov_b32 v[16:17], v[34:35], v[36:37] op_sel:[1,0]
	v_pk_fma_f32 v[12:13], v[34:35], s[24:25], v[12:13] op_sel:[0,1,0]
	v_pk_fma_f32 v[14:15], v[34:35], s[2:3], v[14:15] op_sel_hi:[1,0,1]
	v_pk_fma_f32 v[8:9], v[34:35], s[44:45], v[8:9] op_sel:[0,1,0]
	v_pk_fma_f32 v[4:5], v[34:35], s[10:11], v[4:5] op_sel_hi:[1,0,1]
	v_pk_fma_f32 v[18:19], v[34:35], s[52:53], v[62:63] op_sel_hi:[1,0,1]
	v_add_u32_e32 v64, 0xb50, v52
	ds_read2_b64 v[30:33], v53 offset1:1
	ds_read2_b64 v[54:57], v64 offset1:1
	v_add_u32_e32 v38, 0xc60, v52
	v_add_u32_e32 v39, 0xc70, v52
	v_add_u32_e32 v53, 0xd80, v52
	v_add_u32_e32 v28, 0xd90, v52
	v_pk_fma_f32 v[58:59], v[16:17], s[56:57], v[26:27] op_sel_hi:[1,0,1]
	v_pk_fma_f32 v[12:13], v[16:17], s[26:27], v[12:13] op_sel_hi:[1,0,1]
	v_pk_fma_f32 v[14:15], v[16:17], s[70:71], v[14:15] op_sel_hi:[1,0,1]
	v_pk_fma_f32 v[8:9], v[16:17], s[42:43], v[8:9] op_sel_hi:[1,0,1]
	v_pk_fma_f32 v[4:5], v[16:17], s[64:65], v[4:5] op_sel_hi:[1,0,1]
	v_pk_fma_f32 v[16:17], v[16:17], s[54:55], v[18:19] op_sel_hi:[1,0,1]
	ds_read2_b64 v[22:25], v38 offset1:1
	ds_read2_b64 v[38:41], v39 offset1:1
	ds_read2_b64 v[18:21], v53 offset1:1
	ds_read2_b64 v[26:29], v28 offset1:1
	v_add_u32_e32 v60, 0xea0, v52
	v_add_u32_e32 v61, 0xeb0, v52
	v_pk_fma_f32 v[34:35], v[36:37], s[20:21], v[58:59] op_sel_hi:[1,0,1]
	v_pk_fma_f32 v[52:53], v[36:37], s[76:77], v[12:13] op_sel_hi:[1,0,1]
	v_pk_fma_f32 v[14:15], v[36:37], s[4:5], v[14:15] op_sel_hi:[1,0,1]
	v_pk_fma_f32 v[8:9], v[36:37], s[36:37], v[8:9] op_sel_hi:[1,0,1]
	v_pk_fma_f32 v[4:5], v[36:37], s[12:13], v[4:5] op_sel_hi:[1,0,1]
	v_pk_fma_f32 v[16:17], v[36:37], s[50:51], v[16:17] op_sel_hi:[1,0,1]
	v_pk_mov_b32 v[36:37], v[36:37], v[42:43] op_sel:[1,0]
	v_pk_mov_b32 v[58:59], v[0:1], v[2:3] op_sel:[1,0]
	v_pk_fma_f32 v[14:15], v[36:37], s[72:73], v[14:15] op_sel_hi:[1,0,1]
	v_pk_fma_f32 v[12:13], v[36:37], s[60:61], v[34:35] op_sel_hi:[1,0,1]
	v_pk_mov_b32 v[34:35], v[42:43], v[44:45] op_sel:[1,0]
	v_pk_fma_f32 v[52:53], v[36:37], s[34:35], v[52:53] op_sel_hi:[1,0,1]
	v_pk_fma_f32 v[14:15], v[42:43], s[6:7], v[14:15] op_sel_hi:[1,0,1]
	v_pk_fma_f32 v[8:9], v[36:37], s[40:41], v[8:9] op_sel_hi:[1,0,1]
	v_pk_fma_f32 v[4:5], v[36:37], s[68:69], v[4:5] op_sel_hi:[1,0,1]
	v_pk_fma_f32 v[16:17], v[36:37], s[46:47], v[16:17] op_sel_hi:[1,0,1]
	v_pk_fma_f32 v[52:53], v[42:43], s[34:35], v[52:53] op_sel:[0,1,0]
	v_pk_fma_f32 v[14:15], v[34:35], s[74:75], v[14:15] op_sel_hi:[1,0,1]
	v_pk_fma_f32 v[8:9], v[42:43], s[38:39], v[8:9] op_sel_hi:[1,0,1]
	v_pk_fma_f32 v[4:5], v[42:43], s[14:15], v[4:5] op_sel_hi:[1,0,1]
	v_pk_fma_f32 v[16:17], v[42:43], s[48:49], v[16:17] op_sel_hi:[1,0,1]
	v_pk_fma_f32 v[52:53], v[34:35], s[16:17], v[52:53] op_sel_hi:[1,0,1]
	v_pk_fma_f32 v[14:15], v[44:45], s[24:25], v[14:15] op_sel_hi:[1,0,1]
	v_pk_fma_f32 v[8:9], v[34:35], s[0:1], v[8:9] op_sel_hi:[1,0,1]
	v_pk_fma_f32 v[4:5], v[34:35], s[66:67], v[4:5] op_sel_hi:[1,0,1]
	v_pk_fma_f32 v[16:17], v[34:35], s[8:9], v[16:17] op_sel_hi:[1,0,1]
	v_pk_fma_f32 v[52:53], v[44:45], s[16:17], v[52:53] op_sel:[0,1,0]
	v_pk_fma_f32 v[8:9], v[44:45], s[0:1], v[8:9] op_sel:[0,1,0]
	v_pk_fma_f32 v[4:5], v[44:45], s[44:45], v[4:5] op_sel_hi:[1,0,1]
	v_pk_fma_f32 v[16:17], v[44:45], s[8:9], v[16:17] op_sel:[0,1,0]
	v_pk_fma_f32 v[14:15], v[0:1], s[24:25], v[14:15] op_sel:[0,1,0]
	v_pk_fma_f32 v[52:53], v[0:1], s[18:19], v[52:53] op_sel_hi:[1,0,1]
	v_pk_fma_f32 v[14:15], v[58:59], s[26:27], v[14:15] op_sel_hi:[1,0,1]
	v_pk_fma_f32 v[8:9], v[0:1], s[2:3], v[8:9] op_sel_hi:[1,0,1]
	v_pk_fma_f32 v[4:5], v[0:1], s[44:45], v[4:5] op_sel:[0,1,0]
	v_pk_fma_f32 v[0:1], v[0:1], s[10:11], v[16:17] op_sel_hi:[1,0,1]
	v_pk_fma_f32 v[52:53], v[58:59], s[56:57], v[52:53] op_sel_hi:[1,0,1]
	v_pk_fma_f32 v[8:9], v[58:59], s[70:71], v[8:9] op_sel_hi:[1,0,1]
	v_pk_fma_f32 v[4:5], v[58:59], s[42:43], v[4:5] op_sel_hi:[1,0,1]
	v_pk_fma_f32 v[0:1], v[58:59], s[64:65], v[0:1] op_sel_hi:[1,0,1]
	v_pk_mov_b32 v[58:59], v[2:3], v[46:47] op_sel:[1,0]
	v_pk_fma_f32 v[14:15], v[2:3], s[76:77], v[14:15] op_sel_hi:[1,0,1]
	v_pk_fma_f32 v[52:53], v[2:3], s[20:21], v[52:53] op_sel_hi:[1,0,1]
	v_pk_fma_f32 v[14:15], v[58:59], s[34:35], v[14:15] op_sel_hi:[1,0,1]
	v_pk_fma_f32 v[8:9], v[2:3], s[4:5], v[8:9] op_sel_hi:[1,0,1]
	v_pk_fma_f32 v[4:5], v[2:3], s[36:37], v[4:5] op_sel_hi:[1,0,1]
	v_pk_fma_f32 v[0:1], v[2:3], s[12:13], v[0:1] op_sel_hi:[1,0,1]
	v_pk_mov_b32 v[2:3], v[46:47], v[48:49] op_sel:[1,0]
	v_pk_fma_f32 v[14:15], v[46:47], s[34:35], v[14:15] op_sel:[0,1,0]
	v_pk_fma_f32 v[16:17], v[58:59], s[60:61], v[52:53] op_sel_hi:[1,0,1]
	v_pk_fma_f32 v[14:15], v[2:3], s[16:17], v[14:15] op_sel_hi:[1,0,1]
	s_waitcnt lgkmcnt(5)
	v_pk_mov_b32 v[52:53], v[30:31], v[32:33] op_sel:[1,0]
	v_pk_fma_f32 v[14:15], v[48:49], s[16:17], v[14:15] op_sel:[0,1,0]
	v_pk_fma_f32 v[8:9], v[58:59], s[72:73], v[8:9] op_sel_hi:[1,0,1]
	v_pk_fma_f32 v[14:15], v[30:31], s[18:19], v[14:15] op_sel_hi:[1,0,1]
	v_pk_fma_f32 v[4:5], v[58:59], s[40:41], v[4:5] op_sel_hi:[1,0,1]
	v_pk_fma_f32 v[14:15], v[52:53], s[56:57], v[14:15] op_sel_hi:[1,0,1]
	v_pk_fma_f32 v[0:1], v[58:59], s[68:69], v[0:1] op_sel_hi:[1,0,1]
	v_pk_fma_f32 v[14:15], v[32:33], s[20:21], v[14:15] op_sel_hi:[1,0,1]
	s_waitcnt lgkmcnt(4)
	v_pk_mov_b32 v[58:59], v[32:33], v[54:55] op_sel:[1,0]
	v_pk_fma_f32 v[12:13], v[42:43], s[22:23], v[12:13] op_sel_hi:[1,0,1]
	v_pk_fma_f32 v[14:15], v[58:59], s[60:61], v[14:15] op_sel_hi:[1,0,1]
	v_pk_fma_f32 v[12:13], v[34:35], s[58:59], v[12:13] op_sel_hi:[1,0,1]
	v_pk_fma_f32 v[16:17], v[46:47], s[22:23], v[16:17] op_sel_hi:[1,0,1]
	v_pk_fma_f32 v[14:15], v[54:55], s[22:23], v[14:15] op_sel_hi:[1,0,1]
	v_pk_fma_f32 v[8:9], v[46:47], s[6:7], v[8:9] op_sel_hi:[1,0,1]
	v_pk_fma_f32 v[4:5], v[46:47], s[38:39], v[4:5] op_sel_hi:[1,0,1]
	v_pk_fma_f32 v[0:1], v[46:47], s[14:15], v[0:1] op_sel_hi:[1,0,1]
	v_pk_mov_b32 v[46:47], v[54:55], v[56:57] op_sel:[1,0]
	v_pk_fma_f32 v[12:13], v[44:45], s[78:79], v[12:13] op_sel_hi:[1,0,1]
	ds_read2_b64 v[34:37], v60 offset1:1
	ds_read2_b64 v[42:45], v61 offset1:1
	v_pk_fma_f32 v[16:17], v[2:3], s[58:59], v[16:17] op_sel_hi:[1,0,1]
	v_pk_fma_f32 v[60:61], v[2:3], s[74:75], v[8:9] op_sel_hi:[1,0,1]
	v_pk_fma_f32 v[4:5], v[2:3], s[0:1], v[4:5] op_sel_hi:[1,0,1]
	v_pk_fma_f32 v[0:1], v[2:3], s[66:67], v[0:1] op_sel_hi:[1,0,1]
	v_pk_fma_f32 v[2:3], v[46:47], s[58:59], v[14:15] op_sel_hi:[1,0,1]
	v_pk_fma_f32 v[0:1], v[48:49], s[44:45], v[0:1] op_sel_hi:[1,0,1]
	v_pk_fma_f32 v[8:9], v[56:57], s[78:79], v[2:3] op_sel_hi:[1,0,1]
	v_pk_fma_f32 v[2:3], v[48:49], s[24:25], v[60:61] op_sel_hi:[1,0,1]
	v_pk_fma_f32 v[0:1], v[30:31], s[44:45], v[0:1] op_sel:[0,1,0]
	v_pk_fma_f32 v[2:3], v[30:31], s[24:25], v[2:3] op_sel:[0,1,0]
	v_pk_fma_f32 v[0:1], v[52:53], s[42:43], v[0:1] op_sel_hi:[1,0,1]
	v_pk_fma_f32 v[2:3], v[52:53], s[26:27], v[2:3] op_sel_hi:[1,0,1]
	v_pk_fma_f32 v[0:1], v[32:33], s[36:37], v[0:1] op_sel_hi:[1,0,1]
	v_pk_fma_f32 v[2:3], v[32:33], s[76:77], v[2:3] op_sel_hi:[1,0,1]
	v_pk_fma_f32 v[0:1], v[58:59], s[40:41], v[0:1] op_sel_hi:[1,0,1]
	v_pk_fma_f32 v[2:3], v[58:59], s[34:35], v[2:3] op_sel_hi:[1,0,1]
	v_pk_fma_f32 v[0:1], v[54:55], s[38:39], v[0:1] op_sel_hi:[1,0,1]
	v_pk_fma_f32 v[2:3], v[54:55], s[34:35], v[2:3] op_sel:[0,1,0]
	s_waitcnt lgkmcnt(5)
	v_pk_mov_b32 v[14:15], v[22:23], v[24:25] op_sel:[1,0]
	v_pk_fma_f32 v[2:3], v[46:47], s[16:17], v[2:3] op_sel_hi:[1,0,1]
	v_pk_fma_f32 v[0:1], v[46:47], s[0:1], v[0:1] op_sel_hi:[1,0,1]
	v_pk_fma_f32 v[2:3], v[56:57], s[16:17], v[2:3] op_sel:[0,1,0]
	v_pk_fma_f32 v[0:1], v[56:57], s[0:1], v[0:1] op_sel:[0,1,0]
	v_pk_fma_f32 v[2:3], v[22:23], s[18:19], v[2:3] op_sel_hi:[1,0,1]
	v_pk_fma_f32 v[16:17], v[48:49], s[78:79], v[16:17] op_sel_hi:[1,0,1]
	v_pk_fma_f32 v[2:3], v[14:15], s[56:57], v[2:3] op_sel_hi:[1,0,1]
	v_pk_fma_f32 v[4:5], v[48:49], s[0:1], v[4:5] op_sel:[0,1,0]
	v_pk_fma_f32 v[2:3], v[24:25], s[20:21], v[2:3] op_sel_hi:[1,0,1]
	s_waitcnt lgkmcnt(4)
	v_pk_mov_b32 v[48:49], v[24:25], v[38:39] op_sel:[1,0]
	v_pk_fma_f32 v[0:1], v[22:23], s[2:3], v[0:1] op_sel_hi:[1,0,1]
	v_pk_fma_f32 v[2:3], v[48:49], s[60:61], v[2:3] op_sel_hi:[1,0,1]
	v_pk_fma_f32 v[0:1], v[14:15], s[70:71], v[0:1] op_sel_hi:[1,0,1]
	v_pk_fma_f32 v[2:3], v[38:39], s[22:23], v[2:3] op_sel_hi:[1,0,1]
	v_pk_fma_f32 v[4:5], v[30:31], s[2:3], v[4:5] op_sel_hi:[1,0,1]
	v_pk_mov_b32 v[30:31], v[38:39], v[40:41] op_sel:[1,0]
	v_pk_fma_f32 v[0:1], v[24:25], s[4:5], v[0:1] op_sel_hi:[1,0,1]
	v_pk_fma_f32 v[60:61], v[52:53], s[70:71], v[4:5] op_sel_hi:[1,0,1]
	v_pk_fma_f32 v[2:3], v[30:31], s[58:59], v[2:3] op_sel_hi:[1,0,1]
	v_pk_fma_f32 v[0:1], v[48:49], s[72:73], v[0:1] op_sel_hi:[1,0,1]
	v_pk_fma_f32 v[4:5], v[40:41], s[78:79], v[2:3] op_sel_hi:[1,0,1]
	v_pk_fma_f32 v[2:3], v[32:33], s[4:5], v[60:61] op_sel_hi:[1,0,1]
	v_pk_fma_f32 v[0:1], v[38:39], s[6:7], v[0:1] op_sel_hi:[1,0,1]
	v_pk_fma_f32 v[2:3], v[58:59], s[72:73], v[2:3] op_sel_hi:[1,0,1]
	v_pk_fma_f32 v[0:1], v[30:31], s[74:75], v[0:1] op_sel_hi:[1,0,1]
	v_pk_fma_f32 v[2:3], v[54:55], s[6:7], v[2:3] op_sel_hi:[1,0,1]
	v_pk_fma_f32 v[0:1], v[40:41], s[24:25], v[0:1] op_sel_hi:[1,0,1]
	v_pk_fma_f32 v[2:3], v[46:47], s[74:75], v[2:3] op_sel_hi:[1,0,1]
	s_waitcnt lgkmcnt(3)
	v_pk_mov_b32 v[32:33], v[18:19], v[20:21] op_sel:[1,0]
	v_pk_fma_f32 v[0:1], v[18:19], s[24:25], v[0:1] op_sel:[0,1,0]
	v_pk_fma_f32 v[2:3], v[56:57], s[24:25], v[2:3] op_sel_hi:[1,0,1]
	v_pk_fma_f32 v[0:1], v[32:33], s[26:27], v[0:1] op_sel_hi:[1,0,1]
	v_pk_fma_f32 v[2:3], v[22:23], s[24:25], v[2:3] op_sel:[0,1,0]
	s_waitcnt lgkmcnt(2)
	v_pk_mov_b32 v[52:53], v[20:21], v[26:27] op_sel:[1,0]
	v_pk_fma_f32 v[0:1], v[20:21], s[76:77], v[0:1] op_sel_hi:[1,0,1]
	v_pk_fma_f32 v[2:3], v[14:15], s[26:27], v[2:3] op_sel_hi:[1,0,1]
	v_pk_fma_f32 v[0:1], v[52:53], s[34:35], v[0:1] op_sel_hi:[1,0,1]
	v_pk_fma_f32 v[2:3], v[24:25], s[76:77], v[2:3] op_sel_hi:[1,0,1]
	v_pk_mov_b32 v[58:59], v[26:27], v[28:29] op_sel:[1,0]
	v_pk_fma_f32 v[0:1], v[26:27], s[34:35], v[0:1] op_sel:[0,1,0]
	v_pk_fma_f32 v[2:3], v[48:49], s[34:35], v[2:3] op_sel_hi:[1,0,1]
	v_pk_fma_f32 v[0:1], v[58:59], s[16:17], v[0:1] op_sel_hi:[1,0,1]
	v_pk_fma_f32 v[2:3], v[38:39], s[34:35], v[2:3] op_sel:[0,1,0]
	v_pk_fma_f32 v[0:1], v[28:29], s[16:17], v[0:1] op_sel:[0,1,0]
	v_pk_fma_f32 v[2:3], v[30:31], s[16:17], v[2:3] op_sel_hi:[1,0,1]
	s_waitcnt lgkmcnt(1)
	v_pk_fma_f32 v[0:1], v[34:35], s[18:19], v[0:1] op_sel_hi:[1,0,1]
	v_pk_mov_b32 v[14:15], v[34:35], v[36:37] op_sel:[1,0]
	v_pk_fma_f32 v[2:3], v[40:41], s[16:17], v[2:3] op_sel:[0,1,0]
	v_pk_fma_f32 v[0:1], v[14:15], s[56:57], v[0:1] op_sel_hi:[1,0,1]
	v_pk_fma_f32 v[2:3], v[18:19], s[18:19], v[2:3] op_sel_hi:[1,0,1]
	v_pk_fma_f32 v[0:1], v[36:37], s[20:21], v[0:1] op_sel_hi:[1,0,1]
	s_waitcnt lgkmcnt(0)
	v_pk_mov_b32 v[14:15], v[36:37], v[42:43] op_sel:[1,0]
	s_add_u32 s0, s30, s28
	v_pk_fma_f32 v[2:3], v[32:33], s[56:57], v[2:3] op_sel_hi:[1,0,1]
	v_pk_fma_f32 v[0:1], v[14:15], s[60:61], v[0:1] op_sel_hi:[1,0,1]
	s_addc_u32 s1, s31, s29
	v_lshlrev_b32_e32 v18, 2, v51
	v_mov_b32_e32 v19, 0
	v_pk_fma_f32 v[2:3], v[20:21], s[20:21], v[2:3] op_sel_hi:[1,0,1]
	v_pk_fma_f32 v[0:1], v[42:43], s[22:23], v[0:1] op_sel_hi:[1,0,1]
	v_pk_mov_b32 v[14:15], v[42:43], v[44:45] op_sel:[1,0]
	v_lshl_add_u64 v[20:21], s[0:1], 0, v[18:19]
	s_mov_b32 s1, 0x3f3504f3
	v_pk_fma_f32 v[0:1], v[14:15], s[58:59], v[0:1] op_sel_hi:[1,0,1]
	v_mul_f32_e64 v14, |v6|, s1
	s_mov_b32 s3, 0x3ea7ba05
	v_fma_f32 v15, v14, s3, 1.0
	v_mul_f32_e32 v14, v14, v14
	v_mul_f32_e32 v14, 0xbfb8aa3b, v14
	v_mul_f32_e64 v18, |v7|, s1
	v_exp_f32_e32 v24, v14
	v_fma_f32 v14, v18, s3, 1.0
	v_rcp_f32_e32 v22, v15
	v_rcp_f32_e32 v23, v14
	s_mov_b32 s2, 0xbfba00e3
	v_pk_fma_f32 v[2:3], v[52:53], s[60:61], v[2:3] op_sel_hi:[1,0,1]
	s_mov_b32 s0, 0x3f87dc22
	v_mov_b64_e32 v[14:15], s[2:3]
	v_mul_f32_e32 v18, v18, v18
	v_pk_fma_f32 v[2:3], v[26:27], s[22:23], v[2:3] op_sel_hi:[1,0,1]
	v_pk_fma_f32 v[26:27], v[22:23], s[0:1], v[14:15] op_sel_hi:[1,0,0]
	s_mov_b32 s2, 0x3fb5f0e3
	v_mul_f32_e32 v18, 0xbfb8aa3b, v18
	v_pk_fma_f32 v[26:27], v[22:23], v[26:27], s[2:3] op_sel_hi:[1,1,0]
	v_exp_f32_e32 v25, v18
	s_mov_b32 s4, 0xbe91a98e
	v_pk_fma_f32 v[26:27], v[22:23], v[26:27], s[4:5] op_sel_hi:[1,1,0]
	s_mov_b32 s6, 0x3e827906
	v_pk_fma_f32 v[26:27], v[22:23], v[26:27], s[6:7] op_sel_hi:[1,1,0]
	v_cmp_gt_f32_e32 vcc, 0, v7
	v_pk_mul_f32 v[22:23], v[22:23], v[26:27]
	v_lshlrev_b32_e32 v18, 10, v50
	v_pk_fma_f32 v[22:23], v[24:25], v[22:23], 1.0 op_sel_hi:[1,1,0] neg_lo:[1,0,0] neg_hi:[1,0,0]
	v_pk_fma_f32 v[2:3], v[58:59], s[58:59], v[2:3] op_sel_hi:[1,0,1]
	v_cndmask_b32_e64 v23, v23, -v23, vcc
	v_cmp_gt_f32_e32 vcc, 0, v6
	v_pk_mul_f32 v[6:7], v[6:7], 0.5 op_sel_hi:[1,0]
	v_pk_fma_f32 v[2:3], v[28:29], s[78:79], v[2:3] op_sel_hi:[1,0,1]
	v_cndmask_b32_e64 v22, v22, -v22, vcc
	v_pk_add_f32 v[22:23], v[22:23], 1.0 op_sel_hi:[1,0]
	v_cmp_gt_f32_e32 vcc, 0, v11
	v_pk_mul_f32 v[6:7], v[6:7], v[22:23]
	v_pk_fma_f32 v[0:1], v[44:45], s[78:79], v[0:1] op_sel_hi:[1,0,1]
	v_cvt_pk_f16_f32 v22, v6, v7
	v_lshl_add_u64 v[6:7], v[20:21], 0, v[18:19]
	v_mul_f32_e64 v20, |v10|, s1
	v_mul_f32_e64 v21, |v11|, s1
	v_fma_f32 v18, v20, s3, 1.0
	v_fma_f32 v19, v21, s3, 1.0
	v_rcp_f32_e32 v18, v18
	v_rcp_f32_e32 v19, v19
	v_mul_f32_e32 v20, v20, v20
	v_mul_f32_e32 v21, v21, v21
	global_store_dword v[6:7], v22, off sc1
	v_mul_f32_e32 v20, 0xbfb8aa3b, v20
	v_pk_fma_f32 v[22:23], v[18:19], s[0:1], v[14:15] op_sel_hi:[1,0,0]
	v_mul_f32_e32 v21, 0xbfb8aa3b, v21
	v_exp_f32_e32 v20, v20
	v_pk_fma_f32 v[22:23], v[18:19], v[22:23], s[2:3] op_sel_hi:[1,1,0]
	v_exp_f32_e32 v21, v21
	v_pk_fma_f32 v[22:23], v[18:19], v[22:23], s[4:5] op_sel_hi:[1,1,0]
	s_nop 0
	v_pk_fma_f32 v[22:23], v[18:19], v[22:23], s[6:7] op_sel_hi:[1,1,0]
	s_nop 0
	v_pk_mul_f32 v[18:19], v[18:19], v[22:23]
	s_nop 0
	v_pk_fma_f32 v[18:19], v[20:21], v[18:19], 1.0 op_sel_hi:[1,1,0] neg_lo:[1,0,0] neg_hi:[1,0,0]
	s_nop 0
	v_cndmask_b32_e64 v19, v19, -v19, vcc
	v_cmp_gt_f32_e32 vcc, 0, v10
	v_pk_mul_f32 v[10:11], v[10:11], 0.5 op_sel_hi:[1,0]
	s_nop 0
	v_cndmask_b32_e64 v18, v18, -v18, vcc
	v_pk_add_f32 v[18:19], v[18:19], 1.0 op_sel_hi:[1,0]
	v_cmp_gt_f32_e32 vcc, 0, v13
	v_pk_mul_f32 v[10:11], v[10:11], v[18:19]
	v_mul_f32_e64 v18, |v12|, s1
	v_cvt_pk_f16_f32 v10, v10, v11
	v_mul_f32_e64 v19, |v13|, s1
	global_store_dword v[6:7], v10, off offset:128 sc1
	v_fma_f32 v10, v18, s3, 1.0
	v_fma_f32 v11, v19, s3, 1.0
	v_rcp_f32_e32 v10, v10
	v_rcp_f32_e32 v11, v11
	v_mul_f32_e32 v18, v18, v18
	v_mul_f32_e32 v19, v19, v19
	v_mul_f32_e32 v18, 0xbfb8aa3b, v18
	v_pk_fma_f32 v[20:21], v[10:11], s[0:1], v[14:15] op_sel_hi:[1,0,0]
	v_mul_f32_e32 v19, 0xbfb8aa3b, v19
	v_exp_f32_e32 v18, v18
	v_pk_fma_f32 v[20:21], v[10:11], v[20:21], s[2:3] op_sel_hi:[1,1,0]
	v_exp_f32_e32 v19, v19
	v_pk_fma_f32 v[20:21], v[10:11], v[20:21], s[4:5] op_sel_hi:[1,1,0]
	s_nop 0
	v_pk_fma_f32 v[20:21], v[10:11], v[20:21], s[6:7] op_sel_hi:[1,1,0]
	s_nop 0
	v_pk_mul_f32 v[10:11], v[10:11], v[20:21]
	s_nop 0
	v_pk_fma_f32 v[10:11], v[18:19], v[10:11], 1.0 op_sel_hi:[1,1,0] neg_lo:[1,0,0] neg_hi:[1,0,0]
	s_nop 0
	v_cndmask_b32_e64 v11, v11, -v11, vcc
	v_cmp_gt_f32_e32 vcc, 0, v12
	v_pk_mul_f32 v[12:13], v[12:13], 0.5 op_sel_hi:[1,0]
	s_nop 0
	v_cndmask_b32_e64 v10, v10, -v10, vcc
	v_pk_add_f32 v[10:11], v[10:11], 1.0 op_sel_hi:[1,0]
	v_cmp_gt_f32_e32 vcc, 0, v17
	v_pk_mul_f32 v[10:11], v[12:13], v[10:11]
	v_mul_f32_e64 v12, |v16|, s1
	v_cvt_pk_f16_f32 v10, v10, v11
	v_mul_f32_e64 v13, |v17|, s1
	global_store_dword v[6:7], v10, off offset:256 sc1
	v_fma_f32 v10, v12, s3, 1.0
	v_fma_f32 v11, v13, s3, 1.0
	v_rcp_f32_e32 v10, v10
	v_rcp_f32_e32 v11, v11
	v_mul_f32_e32 v12, v12, v12
	v_mul_f32_e32 v13, v13, v13
	v_mul_f32_e32 v12, 0xbfb8aa3b, v12
	v_pk_fma_f32 v[18:19], v[10:11], s[0:1], v[14:15] op_sel_hi:[1,0,0]
	v_mul_f32_e32 v13, 0xbfb8aa3b, v13
	v_exp_f32_e32 v12, v12
	v_pk_fma_f32 v[18:19], v[10:11], v[18:19], s[2:3] op_sel_hi:[1,1,0]
	v_exp_f32_e32 v13, v13
	v_pk_fma_f32 v[18:19], v[10:11], v[18:19], s[4:5] op_sel_hi:[1,1,0]
	s_nop 0
	v_pk_fma_f32 v[18:19], v[10:11], v[18:19], s[6:7] op_sel_hi:[1,1,0]
	s_nop 0
	v_pk_mul_f32 v[10:11], v[10:11], v[18:19]
	s_nop 0
	v_pk_fma_f32 v[10:11], v[12:13], v[10:11], 1.0 op_sel_hi:[1,1,0] neg_lo:[1,0,0] neg_hi:[1,0,0]
	v_pk_mul_f32 v[12:13], v[16:17], 0.5 op_sel_hi:[1,0]
	v_cndmask_b32_e64 v11, v11, -v11, vcc
	v_cmp_gt_f32_e32 vcc, 0, v16
	s_nop 1
	v_cndmask_b32_e64 v10, v10, -v10, vcc
	v_pk_add_f32 v[10:11], v[10:11], 1.0 op_sel_hi:[1,0]
	v_cmp_gt_f32_e32 vcc, 0, v9
	v_pk_mul_f32 v[10:11], v[12:13], v[10:11]
	v_mul_f32_e64 v12, |v8|, s1
	v_cvt_pk_f16_f32 v10, v10, v11
	v_mul_f32_e64 v13, |v9|, s1
	global_store_dword v[6:7], v10, off offset:384 sc1
	v_fma_f32 v10, v12, s3, 1.0
	v_fma_f32 v11, v13, s3, 1.0
	v_rcp_f32_e32 v10, v10
	v_rcp_f32_e32 v11, v11
	v_mul_f32_e32 v12, v12, v12
	v_mul_f32_e32 v13, v13, v13
	v_mul_f32_e32 v12, 0xbfb8aa3b, v12
	v_pk_fma_f32 v[16:17], v[10:11], s[0:1], v[14:15] op_sel_hi:[1,0,0]
	v_mul_f32_e32 v13, 0xbfb8aa3b, v13
	v_exp_f32_e32 v12, v12
	v_pk_fma_f32 v[16:17], v[10:11], v[16:17], s[2:3] op_sel_hi:[1,1,0]
	v_exp_f32_e32 v13, v13
	v_pk_fma_f32 v[16:17], v[10:11], v[16:17], s[4:5] op_sel_hi:[1,1,0]
	s_nop 0
	v_pk_fma_f32 v[16:17], v[10:11], v[16:17], s[6:7] op_sel_hi:[1,1,0]
	s_nop 0
	v_pk_mul_f32 v[10:11], v[10:11], v[16:17]
	s_nop 0
	v_pk_fma_f32 v[10:11], v[12:13], v[10:11], 1.0 op_sel_hi:[1,1,0] neg_lo:[1,0,0] neg_hi:[1,0,0]
	s_nop 0
	v_cndmask_b32_e64 v11, v11, -v11, vcc
	v_cmp_gt_f32_e32 vcc, 0, v8
	v_pk_mul_f32 v[8:9], v[8:9], 0.5 op_sel_hi:[1,0]
	s_nop 0
	v_cndmask_b32_e64 v10, v10, -v10, vcc
	v_pk_add_f32 v[10:11], v[10:11], 1.0 op_sel_hi:[1,0]
	v_cmp_gt_f32_e32 vcc, 0, v5
	v_pk_mul_f32 v[8:9], v[8:9], v[10:11]
	v_mul_f32_e64 v10, |v4|, s1
	v_cvt_pk_f16_f32 v8, v8, v9
	v_mul_f32_e64 v11, |v5|, s1
	global_store_dword v[6:7], v8, off offset:512 sc1
	v_fma_f32 v8, v10, s3, 1.0
	v_fma_f32 v9, v11, s3, 1.0
	v_rcp_f32_e32 v8, v8
	v_rcp_f32_e32 v9, v9
	v_mul_f32_e32 v10, v10, v10
	v_mul_f32_e32 v11, v11, v11
	v_mul_f32_e32 v10, 0xbfb8aa3b, v10
	v_pk_fma_f32 v[12:13], v[8:9], s[0:1], v[14:15] op_sel_hi:[1,0,0]
	v_mul_f32_e32 v11, 0xbfb8aa3b, v11
	v_exp_f32_e32 v10, v10
	v_pk_fma_f32 v[12:13], v[8:9], v[12:13], s[2:3] op_sel_hi:[1,1,0]
	v_exp_f32_e32 v11, v11
	v_pk_fma_f32 v[12:13], v[8:9], v[12:13], s[4:5] op_sel_hi:[1,1,0]
	s_nop 0
	v_pk_fma_f32 v[12:13], v[8:9], v[12:13], s[6:7] op_sel_hi:[1,1,0]
	s_nop 0
	v_pk_mul_f32 v[8:9], v[8:9], v[12:13]
	s_nop 0
	v_pk_fma_f32 v[8:9], v[10:11], v[8:9], 1.0 op_sel_hi:[1,1,0] neg_lo:[1,0,0] neg_hi:[1,0,0]
	s_nop 0
	v_cndmask_b32_e64 v9, v9, -v9, vcc
	v_cmp_gt_f32_e32 vcc, 0, v4
	v_pk_mul_f32 v[4:5], v[4:5], 0.5 op_sel_hi:[1,0]
	s_nop 0
	v_cndmask_b32_e64 v8, v8, -v8, vcc
	v_pk_add_f32 v[8:9], v[8:9], 1.0 op_sel_hi:[1,0]
	v_cmp_gt_f32_e32 vcc, 0, v3
	v_pk_mul_f32 v[4:5], v[4:5], v[8:9]
	v_mul_f32_e64 v8, |v2|, s1
	v_cvt_pk_f16_f32 v4, v4, v5
	v_mul_f32_e64 v9, |v3|, s1
	global_store_dword v[6:7], v4, off offset:640 sc1
	v_fma_f32 v4, v8, s3, 1.0
	v_fma_f32 v5, v9, s3, 1.0
	v_rcp_f32_e32 v4, v4
	v_rcp_f32_e32 v5, v5
	v_mul_f32_e32 v8, v8, v8
	v_mul_f32_e32 v9, v9, v9
	v_mul_f32_e32 v8, 0xbfb8aa3b, v8
	v_pk_fma_f32 v[10:11], v[4:5], s[0:1], v[14:15] op_sel_hi:[1,0,0]
	v_mul_f32_e32 v9, 0xbfb8aa3b, v9
	v_exp_f32_e32 v8, v8
	v_pk_fma_f32 v[10:11], v[4:5], v[10:11], s[2:3] op_sel_hi:[1,1,0]
	v_exp_f32_e32 v9, v9
	v_pk_fma_f32 v[10:11], v[4:5], v[10:11], s[4:5] op_sel_hi:[1,1,0]
	s_nop 0
	v_pk_fma_f32 v[10:11], v[4:5], v[10:11], s[6:7] op_sel_hi:[1,1,0]
	s_nop 0
	v_pk_mul_f32 v[4:5], v[4:5], v[10:11]
	s_nop 0
	v_pk_fma_f32 v[4:5], v[8:9], v[4:5], 1.0 op_sel_hi:[1,1,0] neg_lo:[1,0,0] neg_hi:[1,0,0]
	s_nop 0
	v_cndmask_b32_e64 v5, v5, -v5, vcc
	v_cmp_gt_f32_e32 vcc, 0, v2
	v_pk_mul_f32 v[2:3], v[2:3], 0.5 op_sel_hi:[1,0]
	s_nop 0
	v_cndmask_b32_e64 v4, v4, -v4, vcc
	v_pk_add_f32 v[4:5], v[4:5], 1.0 op_sel_hi:[1,0]
	v_cmp_gt_f32_e32 vcc, 0, v1
	v_pk_mul_f32 v[2:3], v[2:3], v[4:5]
	v_mul_f32_e64 v4, |v0|, s1
	v_cvt_pk_f16_f32 v2, v2, v3
	v_mul_f32_e64 v5, |v1|, s1
	global_store_dword v[6:7], v2, off offset:768 sc1
	v_fma_f32 v2, v4, s3, 1.0
	v_fma_f32 v3, v5, s3, 1.0
	v_rcp_f32_e32 v2, v2
	v_rcp_f32_e32 v3, v3
	v_mul_f32_e32 v4, v4, v4
	v_mul_f32_e32 v5, v5, v5
	v_mul_f32_e32 v4, 0xbfb8aa3b, v4
	v_pk_fma_f32 v[8:9], v[2:3], s[0:1], v[14:15] op_sel_hi:[1,0,0]
	v_mul_f32_e32 v5, 0xbfb8aa3b, v5
	v_exp_f32_e32 v4, v4
	v_pk_fma_f32 v[8:9], v[2:3], v[8:9], s[2:3] op_sel_hi:[1,1,0]
	v_exp_f32_e32 v5, v5
	v_pk_fma_f32 v[8:9], v[2:3], v[8:9], s[4:5] op_sel_hi:[1,1,0]
	s_nop 0
	v_pk_fma_f32 v[8:9], v[2:3], v[8:9], s[6:7] op_sel_hi:[1,1,0]
	s_nop 0
	v_pk_mul_f32 v[2:3], v[2:3], v[8:9]
	s_nop 0
	v_pk_fma_f32 v[2:3], v[4:5], v[2:3], 1.0 op_sel_hi:[1,1,0] neg_lo:[1,0,0] neg_hi:[1,0,0]
	s_nop 0
	v_cndmask_b32_e64 v3, v3, -v3, vcc
	v_cmp_gt_f32_e32 vcc, 0, v0
	v_pk_mul_f32 v[0:1], v[0:1], 0.5 op_sel_hi:[1,0]
	s_nop 0
	v_cndmask_b32_e64 v2, v2, -v2, vcc
	v_pk_add_f32 v[2:3], v[2:3], 1.0 op_sel_hi:[1,0]
	s_nop 0
	v_pk_mul_f32 v[0:1], v[0:1], v[2:3]
	s_nop 0
	v_cvt_pk_f16_f32 v0, v0, v1
	global_store_dword v[6:7], v0, off offset:896 sc1
	s_endpgm
	.p2alignl 8, 3212836864

.LBB5_32:
	s_nop 0
	v_cvt_pk_f16_f32 v38, v38, v39
	v_cvt_pk_f16_f32 v39, v40, v41
	v_cvt_pk_f16_f32 v40, v46, v47
	v_cvt_pk_f16_f32 v41, v48, v49
	ds_write_b128 v106, v[38:41] offset:9216
	s_waitcnt lgkmcnt(0)
	s_barrier
	ds_read_b64_tr_b16 v[38:39], v87 offset:9216
	ds_read_b64_tr_b16 v[40:41], v87 offset:9792
	ds_read_b64_tr_b16 v[48:49], v87 offset:9856
	ds_read_b64_tr_b16 v[46:47], v87 offset:9280
	s_waitcnt vmcnt(3) lgkmcnt(2)
	v_mfma_f32_32x32x16_f16 v[2:17], v[58:61], v[38:41], v[2:17]
	s_lshl_b32 s0, s3, 7
	s_movk_i32 s1, 0x110
	s_lshl_b64 s[4:5], s[16:17], 22
	s_add_u32 s3, s12, s4
	s_addc_u32 s4, s13, s5
	s_lshl_b32 s2, s2, 1
	s_add_u32 s2, s3, s2
	s_waitcnt lgkmcnt(0)
	v_mfma_f32_32x32x16_f16 v[18:33], v[58:61], v[46:49], v[18:33]
	ds_read_b64_tr_b16 v[38:39], v87 offset:11520
	ds_read_b64_tr_b16 v[40:41], v87 offset:12096
	ds_read_b64_tr_b16 v[48:49], v87 offset:12160
	ds_read_b64_tr_b16 v[46:47], v87 offset:11584
	s_addc_u32 s3, s4, 0
	v_lshrrev_b32_e32 v1, 4, v1
	s_waitcnt vmcnt(2) lgkmcnt(2)
	v_mfma_f32_32x32x16_f16 v[2:17], v[54:57], v[38:41], v[2:17]
	s_waitcnt lgkmcnt(0)
	v_mfma_f32_32x32x16_f16 v[18:33], v[54:57], v[46:49], v[18:33]
	ds_read_b64_tr_b16 v[38:39], v87 offset:13824
	ds_read_b64_tr_b16 v[40:41], v87 offset:14400
	ds_read_b64_tr_b16 v[48:49], v87 offset:14464
	ds_read_b64_tr_b16 v[46:47], v87 offset:13888
	s_waitcnt vmcnt(1) lgkmcnt(2)
	v_mfma_f32_32x32x16_f16 v[2:17], v[42:45], v[38:41], v[2:17]
	s_waitcnt lgkmcnt(0)
	v_mfma_f32_32x32x16_f16 v[18:33], v[42:45], v[46:49], v[18:33]
	ds_read_b64_tr_b16 v[38:39], v87 offset:16128
	ds_read_b64_tr_b16 v[40:41], v87 offset:16704
	ds_read_b64_tr_b16 v[44:45], v87 offset:16768
	ds_read_b64_tr_b16 v[42:43], v87 offset:16192
	s_waitcnt lgkmcnt(0)
	s_barrier
	s_waitcnt vmcnt(0)
	v_mfma_f32_32x32x16_f16 v[2:17], v[34:37], v[38:41], v[2:17]
	v_and_b32_e32 v38, 4, v100
	v_lshl_or_b32 v38, v99, 5, v38
	v_and_b32_e32 v39, 31, v0
	v_mul_u32_u24_e32 v38, 0x110, v38
	v_lshl_add_u32 v38, v39, 2, v38
	v_mfma_f32_32x32x16_f16 v[18:33], v[34:37], v[42:45], v[18:33]
	s_nop 11
	ds_write2_b32 v38, v2, v18 offset1:32
	ds_write2_b32 v38, v3, v19 offset0:68 offset1:100
	ds_write2_b32 v38, v4, v20 offset0:136 offset1:168
	ds_write2_b32 v38, v5, v21 offset0:204 offset1:236
	v_add_u32_e32 v2, 0x800, v38
	ds_write2_b32 v2, v6, v22 offset0:32 offset1:64
	ds_write2_b32 v2, v7, v23 offset0:100 offset1:132
	ds_write2_b32 v2, v8, v24 offset0:168 offset1:200
	v_add_u32_e32 v2, 0xa00, v38
	ds_write2_b32 v2, v9, v25 offset0:108 offset1:140
	v_add_u32_e32 v2, 0x1000, v38
	ds_write2_b32 v2, v10, v26 offset0:64 offset1:96
	ds_write2_b32 v2, v11, v27 offset0:132 offset1:164
	ds_write2_b32 v2, v12, v28 offset0:200 offset1:232
	v_add_u32_e32 v2, 0x1400, v38
	ds_write2_b32 v2, v13, v29 offset0:12 offset1:44
	v_add_u32_e32 v2, 0x1800, v38
	ds_write2_b32 v2, v14, v30 offset0:96 offset1:128
	ds_write2_b32 v2, v15, v31 offset0:164 offset1:196
	v_add_u32_e32 v2, 0x1a00, v38
	ds_write2_b32 v2, v16, v32 offset0:104 offset1:136
	v_add_u32_e32 v2, 0x1c00, v38
	v_lshrrev_b32_e32 v6, 4, v0
	ds_write2_b32 v2, v17, v33 offset0:44 offset1:76
	v_or_b32_e32 v2, s0, v6
	v_ashrrev_i32_e32 v3, 31, v2
	v_lshl_add_u64 v[4:5], v[2:3], 2, s[10:11]
	s_waitcnt lgkmcnt(0)
	s_barrier
	global_load_dword v8, v[4:5], off
	v_and_b32_e32 v4, 60, v86
	v_lshlrev_b32_e32 v18, 2, v4
	v_lshlrev_b32_e32 v10, 1, v4
	v_mad_u32_u24 v4, v6, s1, v18
	ds_read_b128 v[4:7], v4
	v_mov_b32_e32 v11, 0
	v_lshlrev_b64 v[14:15], 13, v[2:3]
	v_lshl_add_u64 v[2:3], s[2:3], 0, v[10:11]
	v_lshl_add_u64 v[10:11], v[2:3], 0, v[14:15]
	s_waitcnt lgkmcnt(0)
	v_mov_b32_e32 v14, v5
	v_mov_b32_e32 v15, v6
	v_lshrrev_b32_e32 v9, 4, v98
	v_or_b32_e32 v12, s0, v9
	v_ashrrev_i32_e32 v13, 31, v12
	v_lshl_add_u64 v[16:17], v[12:13], 2, s[10:11]
	v_lshlrev_b64 v[12:13], 13, v[12:13]
	v_lshl_add_u64 v[12:13], v[2:3], 0, v[12:13]
	s_waitcnt vmcnt(0)
	v_add_f32_e32 v4, v4, v8
	v_add_f32_e32 v5, v7, v8
	v_cvt_f16_f32_e32 v6, v4
	v_cvt_f16_f32_e32 v7, v5
	v_pk_add_f32 v[4:5], v[14:15], v[8:9] op_sel_hi:[1,0]
	s_nop 0
	v_cvt_pk_f16_f32 v5, v4, v5
	v_pack_b32_f16 v4, v6, v5
	v_alignbit_b32 v5, v7, v5, 16
	global_store_dwordx2 v[10:11], v[4:5], off sc1
	global_load_dword v8, v[16:17], off
	v_or_b32_e32 v4, 0x200, v0
	v_lshrrev_b32_e32 v19, 4, v4
	v_mad_u32_u24 v4, v9, s1, v18
	ds_read_b128 v[4:7], v4
	v_or_b32_e32 v10, s0, v19
	v_ashrrev_i32_e32 v11, 31, v10
	v_lshl_add_u64 v[14:15], v[10:11], 2, s[10:11]
	v_lshlrev_b64 v[10:11], 13, v[10:11]
	s_waitcnt lgkmcnt(0)
	v_mov_b32_e32 v16, v5
	v_mov_b32_e32 v17, v6
	v_lshl_add_u64 v[10:11], v[2:3], 0, v[10:11]
	s_waitcnt vmcnt(0)
	v_add_f32_e32 v4, v4, v8
	v_add_f32_e32 v5, v7, v8
	v_cvt_f16_f32_e32 v6, v4
	v_cvt_f16_f32_e32 v7, v5
	v_pk_add_f32 v[4:5], v[16:17], v[8:9] op_sel_hi:[1,0]
	s_nop 0
	v_cvt_pk_f16_f32 v5, v4, v5
	v_pack_b32_f16 v4, v6, v5
	v_alignbit_b32 v5, v7, v5, 16
	global_store_dwordx2 v[12:13], v[4:5], off sc1
	global_load_dword v8, v[14:15], off
	v_or_b32_e32 v4, 0x300, v0
	v_lshrrev_b32_e32 v9, 4, v4
	v_mad_u32_u24 v4, v19, s1, v18
	ds_read_b128 v[4:7], v4
	v_or_b32_e32 v12, s0, v9
	v_ashrrev_i32_e32 v13, 31, v12
	v_lshl_add_u64 v[14:15], v[12:13], 2, s[10:11]
	v_lshlrev_b64 v[12:13], 13, v[12:13]
	s_waitcnt lgkmcnt(0)
	v_mov_b32_e32 v16, v5
	v_mov_b32_e32 v17, v6
	v_lshl_add_u64 v[12:13], v[2:3], 0, v[12:13]
	s_waitcnt vmcnt(0)
	v_add_f32_e32 v4, v4, v8
	v_add_f32_e32 v5, v7, v8
	v_cvt_f16_f32_e32 v6, v4
	v_cvt_f16_f32_e32 v7, v5
	v_pk_add_f32 v[4:5], v[16:17], v[8:9] op_sel_hi:[1,0]
	s_nop 0
	v_cvt_pk_f16_f32 v5, v4, v5
	v_pack_b32_f16 v4, v6, v5
	v_alignbit_b32 v5, v7, v5, 16
	global_store_dwordx2 v[10:11], v[4:5], off sc1
	global_load_dword v8, v[14:15], off
	v_mad_u32_u24 v4, v9, s1, v18
	ds_read_b128 v[4:7], v4
	v_or_b32_e32 v10, s0, v1
	v_ashrrev_i32_e32 v11, 31, v10
	v_lshl_add_u64 v[14:15], v[10:11], 2, s[10:11]
	v_mad_u32_u24 v1, v1, s1, v18
	s_waitcnt lgkmcnt(0)
	v_mov_b32_e32 v16, v5
	v_mov_b32_e32 v17, v6
	v_lshlrev_b64 v[10:11], 13, v[10:11]
	v_lshl_add_u64 v[10:11], v[2:3], 0, v[10:11]
	s_waitcnt vmcnt(0)
	v_add_f32_e32 v4, v4, v8
	v_add_f32_e32 v5, v7, v8
	v_cvt_f16_f32_e32 v6, v4
	v_cvt_f16_f32_e32 v7, v5
	v_pk_add_f32 v[4:5], v[16:17], v[8:9] op_sel_hi:[1,0]
	s_nop 0
	v_cvt_pk_f16_f32 v5, v4, v5
	v_pack_b32_f16 v4, v6, v5
	v_alignbit_b32 v5, v7, v5, 16
	global_store_dwordx2 v[12:13], v[4:5], off sc1
	global_load_dword v8, v[14:15], off
	v_or_b32_e32 v4, 0x500, v0
	v_lshrrev_b32_e32 v9, 4, v4
	ds_read_b128 v[4:7], v1
	v_or_b32_e32 v12, s0, v9
	v_ashrrev_i32_e32 v13, 31, v12
	v_lshl_add_u64 v[14:15], v[12:13], 2, s[10:11]
	v_lshlrev_b64 v[12:13], 13, v[12:13]
	s_waitcnt lgkmcnt(0)
	v_mov_b32_e32 v17, v6
	v_mov_b32_e32 v16, v5
	v_lshl_add_u64 v[12:13], v[2:3], 0, v[12:13]
	s_waitcnt vmcnt(0)
	v_add_f32_e32 v1, v4, v8
	v_add_f32_e32 v4, v7, v8
	v_cvt_f16_f32_e32 v1, v1
	v_cvt_f16_f32_e32 v6, v4
	v_pk_add_f32 v[4:5], v[16:17], v[8:9] op_sel_hi:[1,0]
	s_nop 0
	v_cvt_pk_f16_f32 v5, v4, v5
	v_pack_b32_f16 v4, v1, v5
	v_alignbit_b32 v5, v6, v5, 16
	global_store_dwordx2 v[10:11], v[4:5], off sc1
	global_load_dword v8, v[14:15], off
	v_mad_u32_u24 v4, v9, s1, v18
	ds_read_b128 v[4:7], v4
	v_or_b32_e32 v1, 0x600, v0
	v_lshrrev_b32_e32 v1, 4, v1
	v_or_b32_e32 v10, s0, v1
	v_ashrrev_i32_e32 v11, 31, v10
	s_waitcnt lgkmcnt(0)
	v_mov_b32_e32 v16, v5
	v_mov_b32_e32 v17, v6
	v_lshl_add_u64 v[14:15], v[10:11], 2, s[10:11]
	v_mad_u32_u24 v1, v1, s1, v18
	v_or_b32_e32 v0, 0x700, v0
	v_lshlrev_b64 v[10:11], 13, v[10:11]
	v_lshl_add_u64 v[10:11], v[2:3], 0, v[10:11]
	s_waitcnt vmcnt(0)
	v_add_f32_e32 v4, v4, v8
	v_add_f32_e32 v5, v7, v8
	v_cvt_f16_f32_e32 v6, v4
	v_cvt_f16_f32_e32 v7, v5
	v_pk_add_f32 v[4:5], v[16:17], v[8:9] op_sel_hi:[1,0]
	v_lshrrev_b32_e32 v9, 4, v0
	v_cvt_pk_f16_f32 v5, v4, v5
	v_pack_b32_f16 v4, v6, v5
	v_alignbit_b32 v5, v7, v5, 16
	global_store_dwordx2 v[12:13], v[4:5], off sc1
	global_load_dword v8, v[14:15], off
	ds_read_b128 v[4:7], v1
	v_or_b32_e32 v0, s0, v9
	v_ashrrev_i32_e32 v1, 31, v0
	v_lshl_add_u64 v[12:13], v[0:1], 2, s[10:11]
	v_lshlrev_b64 v[0:1], 13, v[0:1]
	s_waitcnt lgkmcnt(0)
	v_mov_b32_e32 v14, v5
	v_mov_b32_e32 v15, v6
	v_lshl_add_u64 v[0:1], v[2:3], 0, v[0:1]
	s_waitcnt vmcnt(0)
	v_add_f32_e32 v4, v4, v8
	v_add_f32_e32 v5, v7, v8
	v_cvt_f16_f32_e32 v6, v4
	v_cvt_f16_f32_e32 v7, v5
	v_pk_add_f32 v[4:5], v[14:15], v[8:9] op_sel_hi:[1,0]
	s_nop 0
	v_cvt_pk_f16_f32 v5, v4, v5
	v_pack_b32_f16 v4, v6, v5
	v_alignbit_b32 v5, v7, v5, 16
	global_store_dwordx2 v[10:11], v[4:5], off sc1
	global_load_dword v8, v[12:13], off
	v_mad_u32_u24 v4, v9, s1, v18
	ds_read_b128 v[4:7], v4
	s_waitcnt lgkmcnt(0)
	v_mov_b32_e32 v10, v5
	v_mov_b32_e32 v11, v6
	s_waitcnt vmcnt(0)
	v_add_f32_e32 v4, v4, v8
	v_add_f32_e32 v5, v7, v8
	v_cvt_f16_f32_e32 v6, v4
	v_cvt_f16_f32_e32 v7, v5
	v_pk_add_f32 v[4:5], v[10:11], v[8:9] op_sel_hi:[1,0]
	s_nop 0
	v_cvt_pk_f16_f32 v5, v4, v5
	v_pack_b32_f16 v4, v6, v5
	v_alignbit_b32 v5, v7, v5, 16
	global_store_dwordx2 v[0:1], v[4:5], off sc1
	s_endpgm
	.p2alignl 8, 3212836864
